# gather-prep loops rewritten in both MoE layers: all tok_e / blk_cnt loads issued up front, branch-free slot/rowtok body
# baseline (speedup 1.0000x reference)
.LBB0_762:
	s_or_b64 exec, exec, s[0:1]
	s_abs_i32 s11, s80
	v_cvt_f32_u32_e32 v1, s11
	v_mov_b32_e32 v11, 0
	s_sub_i32 s0, 0, s11
	s_waitcnt lgkmcnt(0)
	v_rcp_iflag_f32_e32 v1, v1
	s_barrier
	ds_read_b128 v[2:5], v11 offset:37120
	ds_read_b128 v[6:9], v11 offset:37136
	v_mul_f32_e32 v1, 0x4f7ffffe, v1
	v_cvt_u32_f32_e32 v1, v1
	v_lshrrev_b32_e32 v14, 6, v0
	v_lshrrev_b32_e32 v15, 7, v0
	s_movk_i32 s12, 0xfe00
	v_mul_lo_u32 v10, s0, v1
	v_mul_hi_u32 v10, v1, v10
	v_add_u32_e32 v16, v1, v10
	v_lshlrev_b32_e32 v10, 2, v0
	v_lshl_add_u64 v[12:13], s[28:29], 0, v[10:11]
	s_mov_b64 s[0:1], 0x110000
	v_and_b32_e32 v1, 0x180, v0
	v_lshl_add_u64 v[12:13], v[12:13], 0, s[0:1]
	v_add_u32_e32 v11, 0, v1
	s_mov_b64 s[0:1], 0
	s_add_i32 s10, 0, 0x22000
	s_mov_b64 s[6:7], 0x800
	s_movk_i32 s13, 0x7dff
	v_mov_b32_e32 v17, 2
	v_mov_b32_e32 v18, v34
	s_add_u32 s12, s28, 0x110000
	s_addc_u32 s13, s29, 0
	s_add_u32 s16, s28, 0x150000
	s_addc_u32 s17, s29, 0
	v_lshrrev_b32_e32 v36, 7, v0
	v_mov_b32_e32 v104, 0x0
	v_mov_b32_e32 v105, 0x400
	v_mov_b32_e32 v106, 0x800
	v_mov_b32_e32 v107, 0xc00
	v_mov_b32_e32 v108, 0x1000
	v_mov_b32_e32 v109, 0x1400
	v_mov_b32_e32 v110, 0x1800
	v_mov_b32_e32 v111, 0x1c00
	global_load_dword v40, v10, s[12:13]
	v_add_u32_e32 v1, 0x800, v10
	global_load_dword v41, v1, s[12:13]
	v_add_u32_e32 v1, 0x1000, v10
	global_load_dword v42, v1, s[12:13]
	v_add_u32_e32 v1, 0x1800, v10
	global_load_dword v43, v1, s[12:13]
	v_add_u32_e32 v1, 0x2000, v10
	global_load_dword v44, v1, s[12:13]
	v_add_u32_e32 v1, 0x2800, v10
	global_load_dword v45, v1, s[12:13]
	v_add_u32_e32 v1, 0x3000, v10
	global_load_dword v46, v1, s[12:13]
	v_add_u32_e32 v1, 0x3800, v10
	global_load_dword v47, v1, s[12:13]
	v_add_u32_e32 v1, 0x4000, v10
	global_load_dword v48, v1, s[12:13]
	v_add_u32_e32 v1, 0x4800, v10
	global_load_dword v49, v1, s[12:13]
	v_add_u32_e32 v1, 0x5000, v10
	global_load_dword v50, v1, s[12:13]
	v_add_u32_e32 v1, 0x5800, v10
	global_load_dword v51, v1, s[12:13]
	v_add_u32_e32 v1, 0x6000, v10
	global_load_dword v52, v1, s[12:13]
	v_add_u32_e32 v1, 0x6800, v10
	global_load_dword v53, v1, s[12:13]
	v_add_u32_e32 v1, 0x7000, v10
	global_load_dword v54, v1, s[12:13]
	v_add_u32_e32 v1, 0x7800, v10
	global_load_dword v55, v1, s[12:13]
	v_add_u32_e32 v1, 0x8000, v10
	global_load_dword v56, v1, s[12:13]
	v_add_u32_e32 v1, 0x8800, v10
	global_load_dword v57, v1, s[12:13]
	v_add_u32_e32 v1, 0x9000, v10
	global_load_dword v58, v1, s[12:13]
	v_add_u32_e32 v1, 0x9800, v10
	global_load_dword v59, v1, s[12:13]
	v_add_u32_e32 v1, 0xa000, v10
	global_load_dword v60, v1, s[12:13]
	v_add_u32_e32 v1, 0xa800, v10
	global_load_dword v61, v1, s[12:13]
	v_add_u32_e32 v1, 0xb000, v10
	global_load_dword v62, v1, s[12:13]
	v_add_u32_e32 v1, 0xb800, v10
	global_load_dword v63, v1, s[12:13]
	v_add_u32_e32 v1, 0xc000, v10
	global_load_dword v64, v1, s[12:13]
	v_add_u32_e32 v1, 0xc800, v10
	global_load_dword v65, v1, s[12:13]
	v_add_u32_e32 v1, 0xd000, v10
	global_load_dword v66, v1, s[12:13]
	v_add_u32_e32 v1, 0xd800, v10
	global_load_dword v67, v1, s[12:13]
	v_add_u32_e32 v1, 0xe000, v10
	global_load_dword v68, v1, s[12:13]
	v_add_u32_e32 v1, 0xe800, v10
	global_load_dword v69, v1, s[12:13]
	v_add_u32_e32 v1, 0xf000, v10
	global_load_dword v70, v1, s[12:13]
	v_add_u32_e32 v1, 0xf800, v10
	global_load_dword v71, v1, s[12:13]
	v_add_u32_e32 v1, 0x10000, v10
	global_load_dword v72, v1, s[12:13]
	v_add_u32_e32 v1, 0x10800, v10
	global_load_dword v73, v1, s[12:13]
	v_add_u32_e32 v1, 0x11000, v10
	global_load_dword v74, v1, s[12:13]
	v_add_u32_e32 v1, 0x11800, v10
	global_load_dword v75, v1, s[12:13]
	v_add_u32_e32 v1, 0x12000, v10
	global_load_dword v76, v1, s[12:13]
	v_add_u32_e32 v1, 0x12800, v10
	global_load_dword v77, v1, s[12:13]
	v_add_u32_e32 v1, 0x13000, v10
	global_load_dword v78, v1, s[12:13]
	v_add_u32_e32 v1, 0x13800, v10
	global_load_dword v79, v1, s[12:13]
	v_add_u32_e32 v1, 0x14000, v10
	global_load_dword v80, v1, s[12:13]
	v_add_u32_e32 v1, 0x14800, v10
	global_load_dword v81, v1, s[12:13]
	v_add_u32_e32 v1, 0x15000, v10
	global_load_dword v82, v1, s[12:13]
	v_add_u32_e32 v1, 0x15800, v10
	global_load_dword v83, v1, s[12:13]
	v_add_u32_e32 v1, 0x16000, v10
	global_load_dword v84, v1, s[12:13]
	v_add_u32_e32 v1, 0x16800, v10
	global_load_dword v85, v1, s[12:13]
	v_add_u32_e32 v1, 0x17000, v10
	global_load_dword v86, v1, s[12:13]
	v_add_u32_e32 v1, 0x17800, v10
	global_load_dword v87, v1, s[12:13]
	s_waitcnt vmcnt(32)
	v_add_u32_e32 v1, 0x18000, v10
	global_load_dword v88, v1, s[12:13]
	v_add_u32_e32 v1, 0x18800, v10
	global_load_dword v89, v1, s[12:13]
	v_add_u32_e32 v1, 0x19000, v10
	global_load_dword v90, v1, s[12:13]
	v_add_u32_e32 v1, 0x19800, v10
	global_load_dword v91, v1, s[12:13]
	v_add_u32_e32 v1, 0x1a000, v10
	global_load_dword v92, v1, s[12:13]
	v_add_u32_e32 v1, 0x1a800, v10
	global_load_dword v93, v1, s[12:13]
	v_add_u32_e32 v1, 0x1b000, v10
	global_load_dword v94, v1, s[12:13]
	v_add_u32_e32 v1, 0x1b800, v10
	global_load_dword v95, v1, s[12:13]
	v_add_u32_e32 v1, 0x1c000, v10
	global_load_dword v96, v1, s[12:13]
	v_add_u32_e32 v1, 0x1c800, v10
	global_load_dword v97, v1, s[12:13]
	v_add_u32_e32 v1, 0x1d000, v10
	global_load_dword v98, v1, s[12:13]
	v_add_u32_e32 v1, 0x1d800, v10
	global_load_dword v99, v1, s[12:13]
	v_add_u32_e32 v1, 0x1e000, v10
	global_load_dword v100, v1, s[12:13]
	v_add_u32_e32 v1, 0x1e800, v10
	global_load_dword v101, v1, s[12:13]
	v_add_u32_e32 v1, 0x1f000, v10
	global_load_dword v102, v1, s[12:13]
	v_add_u32_e32 v1, 0x1f800, v10
	global_load_dword v103, v1, s[12:13]
	s_waitcnt lgkmcnt(0)
	s_waitcnt vmcnt(0)
	v_and_b32_e32 v112, 0xff, v40
	v_and_b32_e32 v120, 0xff, v41
	v_and_b32_e32 v128, 0xff, v42
	v_and_b32_e32 v136, 0xff, v43
	v_lshlrev_b32_e32 v112, 2, v112
	v_lshlrev_b32_e32 v120, 2, v120
	v_lshlrev_b32_e32 v128, 2, v128
	v_lshlrev_b32_e32 v136, 2, v136
	v_add_u32_e32 v118, v112, v11
	v_add_u32_e32 v126, v120, v11
	v_add_u32_e32 v134, v128, v11
	v_add_u32_e32 v142, v136, v11
	ds_read_b32 v113, v112 offset:36864
	ds_read_b32 v114, v112 offset:34816
	ds_read_b32 v115, v118
	ds_read_b32 v121, v120 offset:36864
	ds_read_b32 v122, v120 offset:34816
	ds_read_b32 v123, v126 offset:512
	ds_read_b32 v129, v128 offset:36864
	ds_read_b32 v130, v128 offset:34816
	ds_read_b32 v131, v134 offset:1024
	ds_read_b32 v137, v136 offset:36864
	ds_read_b32 v138, v136 offset:34816
	ds_read_b32 v139, v142 offset:1536
	v_mov_b32_e32 v117, v36
	v_add_u32_e32 v125, 4, v36
	v_add_u32_e32 v133, 8, v36
	v_add_u32_e32 v141, 12, v36
	v_mul_hi_u32 v118, v117, v16
	v_mul_hi_u32 v126, v125, v16
	v_mul_hi_u32 v134, v133, v16
	v_mul_hi_u32 v142, v141, v16
	v_mul_lo_u32 v118, v118, s11
	v_mul_lo_u32 v126, v126, s11
	v_mul_lo_u32 v134, v134, s11
	v_mul_lo_u32 v142, v142, s11
	v_sub_u32_e32 v117, v117, v118
	v_sub_u32_e32 v125, v125, v126
	v_sub_u32_e32 v133, v133, v134
	v_sub_u32_e32 v141, v141, v142
	v_subrev_u32_e32 v118, s11, v117
	v_subrev_u32_e32 v126, s11, v125
	v_subrev_u32_e32 v134, s11, v133
	v_subrev_u32_e32 v142, s11, v141
	v_cmp_le_u32_e32 vcc, s11, v117
	v_cmp_le_u32_e64 s[0:1], s11, v125
	v_cmp_le_u32_e64 s[6:7], s11, v133
	v_cmp_le_u32_e64 s[8:9], s11, v141
	v_cndmask_b32_e32 v117, v117, v118, vcc
	v_cndmask_b32_e64 v125, v125, v126, s[0:1]
	v_cndmask_b32_e64 v133, v133, v134, s[6:7]
	v_cndmask_b32_e64 v141, v141, v142, s[8:9]
	v_subrev_u32_e32 v118, s11, v117
	v_subrev_u32_e32 v126, s11, v125
	v_subrev_u32_e32 v134, s11, v133
	v_subrev_u32_e32 v142, s11, v141
	v_cmp_le_u32_e32 vcc, s11, v117
	v_cmp_le_u32_e64 s[0:1], s11, v125
	v_cmp_le_u32_e64 s[6:7], s11, v133
	v_cmp_le_u32_e64 s[8:9], s11, v141
	v_cndmask_b32_e32 v117, v117, v118, vcc
	v_cndmask_b32_e64 v125, v125, v126, s[0:1]
	v_cndmask_b32_e64 v133, v133, v134, s[6:7]
	v_cndmask_b32_e64 v141, v141, v142, s[8:9]
	v_ashrrev_i32_e32 v116, 8, v40
	v_ashrrev_i32_e32 v124, 8, v41
	v_ashrrev_i32_e32 v132, 8, v42
	v_ashrrev_i32_e32 v140, 8, v43
	s_waitcnt lgkmcnt(0)
	v_add_u32_e32 v116, v116, v113
	v_add_u32_e32 v124, v124, v121
	v_add_u32_e32 v132, v132, v129
	v_add_u32_e32 v140, v140, v137
	v_add3_u32 v116, v116, v114, v115
	v_add3_u32 v124, v124, v122, v123
	v_add3_u32 v132, v132, v130, v131
	v_add3_u32 v140, v140, v138, v139
	v_cmp_eq_u32_e32 vcc, s93, v117
	v_mov_b32_e32 v1, v10
	s_and_saveexec_b64 s[24:25], vcc
	global_store_dword v1, v116, s[16:17]
	s_mov_b64 exec, s[24:25]
	v_cmp_eq_u32_e32 vcc, s93, v125
	v_add_u32_e32 v1, 0x800, v10
	s_and_saveexec_b64 s[24:25], vcc
	global_store_dword v1, v124, s[16:17]
	s_mov_b64 exec, s[24:25]
	v_cmp_eq_u32_e32 vcc, s93, v133
	v_add_u32_e32 v1, 0x1000, v10
	s_and_saveexec_b64 s[24:25], vcc
	global_store_dword v1, v132, s[16:17]
	s_mov_b64 exec, s[24:25]
	v_cmp_eq_u32_e32 vcc, s93, v141
	v_add_u32_e32 v1, 0x1800, v10
	s_and_saveexec_b64 s[24:25], vcc
	global_store_dword v1, v140, s[16:17]
	s_mov_b64 exec, s[24:25]
	v_ashrrev_i32_e32 v113, 8, v116
	v_ashrrev_i32_e32 v121, 8, v124
	v_ashrrev_i32_e32 v129, 8, v132
	v_ashrrev_i32_e32 v137, 8, v140
	v_and_b32_e32 v112, 0xff, v116
	v_and_b32_e32 v120, 0xff, v124
	v_and_b32_e32 v128, 0xff, v132
	v_and_b32_e32 v136, 0xff, v140
	v_lshl_add_u32 v112, v112, 2, s10
	v_lshl_add_u32 v120, v120, 2, s10
	v_lshl_add_u32 v128, v128, 2, s10
	v_lshl_add_u32 v136, v136, 2, s10
	v_mov_b32_e32 v114, v34
	v_add_u32_e32 v122, 0x100, v34
	v_add_u32_e32 v130, 0x200, v34
	v_add_u32_e32 v138, 0x300, v34
	v_mov_b32_e32 v119, -1
	v_mov_b32_e32 v127, -1
	v_mov_b32_e32 v135, -1
	v_mov_b32_e32 v143, -1
	v_cmp_eq_u32_e32 vcc, v113, v2
	v_cmp_eq_u32_e64 s[0:1], v121, v2
	v_cmp_eq_u32_e64 s[6:7], v129, v2
	v_cmp_eq_u32_e64 s[8:9], v137, v2
	v_cndmask_b32_e32 v119, v119, v104, vcc
	v_cndmask_b32_e64 v127, v127, v104, s[0:1]
	v_cndmask_b32_e64 v135, v135, v104, s[6:7]
	v_cndmask_b32_e64 v143, v143, v104, s[8:9]
	v_cmp_eq_u32_e32 vcc, v113, v3
	v_cmp_eq_u32_e64 s[0:1], v121, v3
	v_cmp_eq_u32_e64 s[6:7], v129, v3
	v_cmp_eq_u32_e64 s[8:9], v137, v3
	v_cndmask_b32_e32 v119, v119, v105, vcc
	v_cndmask_b32_e64 v127, v127, v105, s[0:1]
	v_cndmask_b32_e64 v135, v135, v105, s[6:7]
	v_cndmask_b32_e64 v143, v143, v105, s[8:9]
	v_cmp_eq_u32_e32 vcc, v113, v4
	v_cmp_eq_u32_e64 s[0:1], v121, v4
	v_cmp_eq_u32_e64 s[6:7], v129, v4
	v_cmp_eq_u32_e64 s[8:9], v137, v4
	v_cndmask_b32_e32 v119, v119, v106, vcc
	v_cndmask_b32_e64 v127, v127, v106, s[0:1]
	v_cndmask_b32_e64 v135, v135, v106, s[6:7]
	v_cndmask_b32_e64 v143, v143, v106, s[8:9]
	v_cmp_eq_u32_e32 vcc, v113, v5
	v_cmp_eq_u32_e64 s[0:1], v121, v5
	v_cmp_eq_u32_e64 s[6:7], v129, v5
	v_cmp_eq_u32_e64 s[8:9], v137, v5
	v_cndmask_b32_e32 v119, v119, v107, vcc
	v_cndmask_b32_e64 v127, v127, v107, s[0:1]
	v_cndmask_b32_e64 v135, v135, v107, s[6:7]
	v_cndmask_b32_e64 v143, v143, v107, s[8:9]
	v_cmp_eq_u32_e32 vcc, v113, v6
	v_cmp_eq_u32_e64 s[0:1], v121, v6
	v_cmp_eq_u32_e64 s[6:7], v129, v6
	v_cmp_eq_u32_e64 s[8:9], v137, v6
	v_cndmask_b32_e32 v119, v119, v108, vcc
	v_cndmask_b32_e64 v127, v127, v108, s[0:1]
	v_cndmask_b32_e64 v135, v135, v108, s[6:7]
	v_cndmask_b32_e64 v143, v143, v108, s[8:9]
	v_cmp_eq_u32_e32 vcc, v113, v7
	v_cmp_eq_u32_e64 s[0:1], v121, v7
	v_cmp_eq_u32_e64 s[6:7], v129, v7
	v_cmp_eq_u32_e64 s[8:9], v137, v7
	v_cndmask_b32_e32 v119, v119, v109, vcc
	v_cndmask_b32_e64 v127, v127, v109, s[0:1]
	v_cndmask_b32_e64 v135, v135, v109, s[6:7]
	v_cndmask_b32_e64 v143, v143, v109, s[8:9]
	v_cmp_eq_u32_e32 vcc, v113, v8
	v_cmp_eq_u32_e64 s[0:1], v121, v8
	v_cmp_eq_u32_e64 s[6:7], v129, v8
	v_cmp_eq_u32_e64 s[8:9], v137, v8
	v_cndmask_b32_e32 v119, v119, v110, vcc
	v_cndmask_b32_e64 v127, v127, v110, s[0:1]
	v_cndmask_b32_e64 v135, v135, v110, s[6:7]
	v_cndmask_b32_e64 v143, v143, v110, s[8:9]
	v_cmp_eq_u32_e32 vcc, v113, v9
	v_cmp_eq_u32_e64 s[0:1], v121, v9
	v_cmp_eq_u32_e64 s[6:7], v129, v9
	v_cmp_eq_u32_e64 s[8:9], v137, v9
	v_cndmask_b32_e32 v119, v119, v111, vcc
	v_cndmask_b32_e64 v127, v127, v111, s[0:1]
	v_cndmask_b32_e64 v135, v135, v111, s[6:7]
	v_cndmask_b32_e64 v143, v143, v111, s[8:9]
	v_add_u32_e32 v112, v112, v119
	v_add_u32_e32 v120, v120, v127
	v_add_u32_e32 v128, v128, v135
	v_add_u32_e32 v136, v136, v143
	v_cmp_ne_u32_e32 vcc, -1, v119
	s_and_saveexec_b64 s[24:25], vcc
	ds_write_b32 v112, v114
	s_mov_b64 exec, s[24:25]
	v_cmp_ne_u32_e32 vcc, -1, v127
	s_and_saveexec_b64 s[24:25], vcc
	ds_write_b32 v120, v122
	s_mov_b64 exec, s[24:25]
	v_cmp_ne_u32_e32 vcc, -1, v135
	s_and_saveexec_b64 s[24:25], vcc
	ds_write_b32 v128, v130
	s_mov_b64 exec, s[24:25]
	v_cmp_ne_u32_e32 vcc, -1, v143
	s_and_saveexec_b64 s[24:25], vcc
	ds_write_b32 v136, v138
	s_mov_b64 exec, s[24:25]
	v_and_b32_e32 v112, 0xff, v44
	v_and_b32_e32 v120, 0xff, v45
	v_and_b32_e32 v128, 0xff, v46
	v_and_b32_e32 v136, 0xff, v47
	v_lshlrev_b32_e32 v112, 2, v112
	v_lshlrev_b32_e32 v120, 2, v120
	v_lshlrev_b32_e32 v128, 2, v128
	v_lshlrev_b32_e32 v136, 2, v136
	v_add_u32_e32 v118, v112, v11
	v_add_u32_e32 v126, v120, v11
	v_add_u32_e32 v134, v128, v11
	v_add_u32_e32 v142, v136, v11
	ds_read_b32 v113, v112 offset:36864
	ds_read_b32 v114, v112 offset:34944
	ds_read_b32 v115, v118 offset:2048
	ds_read_b32 v121, v120 offset:36864
	ds_read_b32 v122, v120 offset:34944
	ds_read_b32 v123, v126 offset:2560
	ds_read_b32 v129, v128 offset:36864
	ds_read_b32 v130, v128 offset:34944
	ds_read_b32 v131, v134 offset:3072
	ds_read_b32 v137, v136 offset:36864
	ds_read_b32 v138, v136 offset:34944
	ds_read_b32 v139, v142 offset:3584
	v_add_u32_e32 v117, 16, v36
	v_add_u32_e32 v125, 20, v36
	v_add_u32_e32 v133, 24, v36
	v_add_u32_e32 v141, 28, v36
	v_mul_hi_u32 v118, v117, v16
	v_mul_hi_u32 v126, v125, v16
	v_mul_hi_u32 v134, v133, v16
	v_mul_hi_u32 v142, v141, v16
	v_mul_lo_u32 v118, v118, s11
	v_mul_lo_u32 v126, v126, s11
	v_mul_lo_u32 v134, v134, s11
	v_mul_lo_u32 v142, v142, s11
	v_sub_u32_e32 v117, v117, v118
	v_sub_u32_e32 v125, v125, v126
	v_sub_u32_e32 v133, v133, v134
	v_sub_u32_e32 v141, v141, v142
	v_subrev_u32_e32 v118, s11, v117
	v_subrev_u32_e32 v126, s11, v125
	v_subrev_u32_e32 v134, s11, v133
	v_subrev_u32_e32 v142, s11, v141
	v_cmp_le_u32_e32 vcc, s11, v117
	v_cmp_le_u32_e64 s[0:1], s11, v125
	v_cmp_le_u32_e64 s[6:7], s11, v133
	v_cmp_le_u32_e64 s[8:9], s11, v141
	v_cndmask_b32_e32 v117, v117, v118, vcc
	v_cndmask_b32_e64 v125, v125, v126, s[0:1]
	v_cndmask_b32_e64 v133, v133, v134, s[6:7]
	v_cndmask_b32_e64 v141, v141, v142, s[8:9]
	v_subrev_u32_e32 v118, s11, v117
	v_subrev_u32_e32 v126, s11, v125
	v_subrev_u32_e32 v134, s11, v133
	v_subrev_u32_e32 v142, s11, v141
	v_cmp_le_u32_e32 vcc, s11, v117
	v_cmp_le_u32_e64 s[0:1], s11, v125
	v_cmp_le_u32_e64 s[6:7], s11, v133
	v_cmp_le_u32_e64 s[8:9], s11, v141
	v_cndmask_b32_e32 v117, v117, v118, vcc
	v_cndmask_b32_e64 v125, v125, v126, s[0:1]
	v_cndmask_b32_e64 v133, v133, v134, s[6:7]
	v_cndmask_b32_e64 v141, v141, v142, s[8:9]
	v_ashrrev_i32_e32 v116, 8, v44
	v_ashrrev_i32_e32 v124, 8, v45
	v_ashrrev_i32_e32 v132, 8, v46
	v_ashrrev_i32_e32 v140, 8, v47
	s_waitcnt lgkmcnt(0)
	v_add_u32_e32 v116, v116, v113
	v_add_u32_e32 v124, v124, v121
	v_add_u32_e32 v132, v132, v129
	v_add_u32_e32 v140, v140, v137
	v_add3_u32 v116, v116, v114, v115
	v_add3_u32 v124, v124, v122, v123
	v_add3_u32 v132, v132, v130, v131
	v_add3_u32 v140, v140, v138, v139
	v_cmp_eq_u32_e32 vcc, s93, v117
	v_add_u32_e32 v1, 0x2000, v10
	s_and_saveexec_b64 s[24:25], vcc
	global_store_dword v1, v116, s[16:17]
	s_mov_b64 exec, s[24:25]
	v_cmp_eq_u32_e32 vcc, s93, v125
	v_add_u32_e32 v1, 0x2800, v10
	s_and_saveexec_b64 s[24:25], vcc
	global_store_dword v1, v124, s[16:17]
	s_mov_b64 exec, s[24:25]
	v_cmp_eq_u32_e32 vcc, s93, v133
	v_add_u32_e32 v1, 0x3000, v10
	s_and_saveexec_b64 s[24:25], vcc
	global_store_dword v1, v132, s[16:17]
	s_mov_b64 exec, s[24:25]
	v_cmp_eq_u32_e32 vcc, s93, v141
	v_add_u32_e32 v1, 0x3800, v10
	s_and_saveexec_b64 s[24:25], vcc
	global_store_dword v1, v140, s[16:17]
	s_mov_b64 exec, s[24:25]
	v_ashrrev_i32_e32 v113, 8, v116
	v_ashrrev_i32_e32 v121, 8, v124
	v_ashrrev_i32_e32 v129, 8, v132
	v_ashrrev_i32_e32 v137, 8, v140
	v_and_b32_e32 v112, 0xff, v116
	v_and_b32_e32 v120, 0xff, v124
	v_and_b32_e32 v128, 0xff, v132
	v_and_b32_e32 v136, 0xff, v140
	v_lshl_add_u32 v112, v112, 2, s10
	v_lshl_add_u32 v120, v120, 2, s10
	v_lshl_add_u32 v128, v128, 2, s10
	v_lshl_add_u32 v136, v136, 2, s10
	v_add_u32_e32 v114, 0x400, v34
	v_add_u32_e32 v122, 0x500, v34
	v_add_u32_e32 v130, 0x600, v34
	v_add_u32_e32 v138, 0x700, v34
	v_mov_b32_e32 v119, -1
	v_mov_b32_e32 v127, -1
	v_mov_b32_e32 v135, -1
	v_mov_b32_e32 v143, -1
	v_cmp_eq_u32_e32 vcc, v113, v2
	v_cmp_eq_u32_e64 s[0:1], v121, v2
	v_cmp_eq_u32_e64 s[6:7], v129, v2
	v_cmp_eq_u32_e64 s[8:9], v137, v2
	v_cndmask_b32_e32 v119, v119, v104, vcc
	v_cndmask_b32_e64 v127, v127, v104, s[0:1]
	v_cndmask_b32_e64 v135, v135, v104, s[6:7]
	v_cndmask_b32_e64 v143, v143, v104, s[8:9]
	v_cmp_eq_u32_e32 vcc, v113, v3
	v_cmp_eq_u32_e64 s[0:1], v121, v3
	v_cmp_eq_u32_e64 s[6:7], v129, v3
	v_cmp_eq_u32_e64 s[8:9], v137, v3
	v_cndmask_b32_e32 v119, v119, v105, vcc
	v_cndmask_b32_e64 v127, v127, v105, s[0:1]
	v_cndmask_b32_e64 v135, v135, v105, s[6:7]
	v_cndmask_b32_e64 v143, v143, v105, s[8:9]
	v_cmp_eq_u32_e32 vcc, v113, v4
	v_cmp_eq_u32_e64 s[0:1], v121, v4
	v_cmp_eq_u32_e64 s[6:7], v129, v4
	v_cmp_eq_u32_e64 s[8:9], v137, v4
	v_cndmask_b32_e32 v119, v119, v106, vcc
	v_cndmask_b32_e64 v127, v127, v106, s[0:1]
	v_cndmask_b32_e64 v135, v135, v106, s[6:7]
	v_cndmask_b32_e64 v143, v143, v106, s[8:9]
	v_cmp_eq_u32_e32 vcc, v113, v5
	v_cmp_eq_u32_e64 s[0:1], v121, v5
	v_cmp_eq_u32_e64 s[6:7], v129, v5
	v_cmp_eq_u32_e64 s[8:9], v137, v5
	v_cndmask_b32_e32 v119, v119, v107, vcc
	v_cndmask_b32_e64 v127, v127, v107, s[0:1]
	v_cndmask_b32_e64 v135, v135, v107, s[6:7]
	v_cndmask_b32_e64 v143, v143, v107, s[8:9]
	v_cmp_eq_u32_e32 vcc, v113, v6
	v_cmp_eq_u32_e64 s[0:1], v121, v6
	v_cmp_eq_u32_e64 s[6:7], v129, v6
	v_cmp_eq_u32_e64 s[8:9], v137, v6
	v_cndmask_b32_e32 v119, v119, v108, vcc
	v_cndmask_b32_e64 v127, v127, v108, s[0:1]
	v_cndmask_b32_e64 v135, v135, v108, s[6:7]
	v_cndmask_b32_e64 v143, v143, v108, s[8:9]
	v_cmp_eq_u32_e32 vcc, v113, v7
	v_cmp_eq_u32_e64 s[0:1], v121, v7
	v_cmp_eq_u32_e64 s[6:7], v129, v7
	v_cmp_eq_u32_e64 s[8:9], v137, v7
	v_cndmask_b32_e32 v119, v119, v109, vcc
	v_cndmask_b32_e64 v127, v127, v109, s[0:1]
	v_cndmask_b32_e64 v135, v135, v109, s[6:7]
	v_cndmask_b32_e64 v143, v143, v109, s[8:9]
	v_cmp_eq_u32_e32 vcc, v113, v8
	v_cmp_eq_u32_e64 s[0:1], v121, v8
	v_cmp_eq_u32_e64 s[6:7], v129, v8
	v_cmp_eq_u32_e64 s[8:9], v137, v8
	v_cndmask_b32_e32 v119, v119, v110, vcc
	v_cndmask_b32_e64 v127, v127, v110, s[0:1]
	v_cndmask_b32_e64 v135, v135, v110, s[6:7]
	v_cndmask_b32_e64 v143, v143, v110, s[8:9]
	v_cmp_eq_u32_e32 vcc, v113, v9
	v_cmp_eq_u32_e64 s[0:1], v121, v9
	v_cmp_eq_u32_e64 s[6:7], v129, v9
	v_cmp_eq_u32_e64 s[8:9], v137, v9
	v_cndmask_b32_e32 v119, v119, v111, vcc
	v_cndmask_b32_e64 v127, v127, v111, s[0:1]
	v_cndmask_b32_e64 v135, v135, v111, s[6:7]
	v_cndmask_b32_e64 v143, v143, v111, s[8:9]
	v_add_u32_e32 v112, v112, v119
	v_add_u32_e32 v120, v120, v127
	v_add_u32_e32 v128, v128, v135
	v_add_u32_e32 v136, v136, v143
	v_cmp_ne_u32_e32 vcc, -1, v119
	s_and_saveexec_b64 s[24:25], vcc
	ds_write_b32 v112, v114
	s_mov_b64 exec, s[24:25]
	v_cmp_ne_u32_e32 vcc, -1, v127
	s_and_saveexec_b64 s[24:25], vcc
	ds_write_b32 v120, v122
	s_mov_b64 exec, s[24:25]
	v_cmp_ne_u32_e32 vcc, -1, v135
	s_and_saveexec_b64 s[24:25], vcc
	ds_write_b32 v128, v130
	s_mov_b64 exec, s[24:25]
	v_cmp_ne_u32_e32 vcc, -1, v143
	s_and_saveexec_b64 s[24:25], vcc
	ds_write_b32 v136, v138
	s_mov_b64 exec, s[24:25]
	v_and_b32_e32 v112, 0xff, v48
	v_and_b32_e32 v120, 0xff, v49
	v_and_b32_e32 v128, 0xff, v50
	v_and_b32_e32 v136, 0xff, v51
	v_lshlrev_b32_e32 v112, 2, v112
	v_lshlrev_b32_e32 v120, 2, v120
	v_lshlrev_b32_e32 v128, 2, v128
	v_lshlrev_b32_e32 v136, 2, v136
	v_add_u32_e32 v118, v112, v11
	v_add_u32_e32 v126, v120, v11
	v_add_u32_e32 v134, v128, v11
	v_add_u32_e32 v142, v136, v11
	ds_read_b32 v113, v112 offset:36864
	ds_read_b32 v114, v112 offset:35072
	ds_read_b32 v115, v118 offset:4096
	ds_read_b32 v121, v120 offset:36864
	ds_read_b32 v122, v120 offset:35072
	ds_read_b32 v123, v126 offset:4608
	ds_read_b32 v129, v128 offset:36864
	ds_read_b32 v130, v128 offset:35072
	ds_read_b32 v131, v134 offset:5120
	ds_read_b32 v137, v136 offset:36864
	ds_read_b32 v138, v136 offset:35072
	ds_read_b32 v139, v142 offset:5632
	v_add_u32_e32 v117, 32, v36
	v_add_u32_e32 v125, 36, v36
	v_add_u32_e32 v133, 40, v36
	v_add_u32_e32 v141, 44, v36
	v_mul_hi_u32 v118, v117, v16
	v_mul_hi_u32 v126, v125, v16
	v_mul_hi_u32 v134, v133, v16
	v_mul_hi_u32 v142, v141, v16
	v_mul_lo_u32 v118, v118, s11
	v_mul_lo_u32 v126, v126, s11
	v_mul_lo_u32 v134, v134, s11
	v_mul_lo_u32 v142, v142, s11
	v_sub_u32_e32 v117, v117, v118
	v_sub_u32_e32 v125, v125, v126
	v_sub_u32_e32 v133, v133, v134
	v_sub_u32_e32 v141, v141, v142
	v_subrev_u32_e32 v118, s11, v117
	v_subrev_u32_e32 v126, s11, v125
	v_subrev_u32_e32 v134, s11, v133
	v_subrev_u32_e32 v142, s11, v141
	v_cmp_le_u32_e32 vcc, s11, v117
	v_cmp_le_u32_e64 s[0:1], s11, v125
	v_cmp_le_u32_e64 s[6:7], s11, v133
	v_cmp_le_u32_e64 s[8:9], s11, v141
	v_cndmask_b32_e32 v117, v117, v118, vcc
	v_cndmask_b32_e64 v125, v125, v126, s[0:1]
	v_cndmask_b32_e64 v133, v133, v134, s[6:7]
	v_cndmask_b32_e64 v141, v141, v142, s[8:9]
	v_subrev_u32_e32 v118, s11, v117
	v_subrev_u32_e32 v126, s11, v125
	v_subrev_u32_e32 v134, s11, v133
	v_subrev_u32_e32 v142, s11, v141
	v_cmp_le_u32_e32 vcc, s11, v117
	v_cmp_le_u32_e64 s[0:1], s11, v125
	v_cmp_le_u32_e64 s[6:7], s11, v133
	v_cmp_le_u32_e64 s[8:9], s11, v141
	v_cndmask_b32_e32 v117, v117, v118, vcc
	v_cndmask_b32_e64 v125, v125, v126, s[0:1]
	v_cndmask_b32_e64 v133, v133, v134, s[6:7]
	v_cndmask_b32_e64 v141, v141, v142, s[8:9]
	v_ashrrev_i32_e32 v116, 8, v48
	v_ashrrev_i32_e32 v124, 8, v49
	v_ashrrev_i32_e32 v132, 8, v50
	v_ashrrev_i32_e32 v140, 8, v51
	s_waitcnt lgkmcnt(0)
	v_add_u32_e32 v116, v116, v113
	v_add_u32_e32 v124, v124, v121
	v_add_u32_e32 v132, v132, v129
	v_add_u32_e32 v140, v140, v137
	v_add3_u32 v116, v116, v114, v115
	v_add3_u32 v124, v124, v122, v123
	v_add3_u32 v132, v132, v130, v131
	v_add3_u32 v140, v140, v138, v139
	v_cmp_eq_u32_e32 vcc, s93, v117
	v_add_u32_e32 v1, 0x4000, v10
	s_and_saveexec_b64 s[24:25], vcc
	global_store_dword v1, v116, s[16:17]
	s_mov_b64 exec, s[24:25]
	v_cmp_eq_u32_e32 vcc, s93, v125
	v_add_u32_e32 v1, 0x4800, v10
	s_and_saveexec_b64 s[24:25], vcc
	global_store_dword v1, v124, s[16:17]
	s_mov_b64 exec, s[24:25]
	v_cmp_eq_u32_e32 vcc, s93, v133
	v_add_u32_e32 v1, 0x5000, v10
	s_and_saveexec_b64 s[24:25], vcc
	global_store_dword v1, v132, s[16:17]
	s_mov_b64 exec, s[24:25]
	v_cmp_eq_u32_e32 vcc, s93, v141
	v_add_u32_e32 v1, 0x5800, v10
	s_and_saveexec_b64 s[24:25], vcc
	global_store_dword v1, v140, s[16:17]
	s_mov_b64 exec, s[24:25]
	v_ashrrev_i32_e32 v113, 8, v116
	v_ashrrev_i32_e32 v121, 8, v124
	v_ashrrev_i32_e32 v129, 8, v132
	v_ashrrev_i32_e32 v137, 8, v140
	v_and_b32_e32 v112, 0xff, v116
	v_and_b32_e32 v120, 0xff, v124
	v_and_b32_e32 v128, 0xff, v132
	v_and_b32_e32 v136, 0xff, v140
	v_lshl_add_u32 v112, v112, 2, s10
	v_lshl_add_u32 v120, v120, 2, s10
	v_lshl_add_u32 v128, v128, 2, s10
	v_lshl_add_u32 v136, v136, 2, s10
	v_add_u32_e32 v114, 0x800, v34
	v_add_u32_e32 v122, 0x900, v34
	v_add_u32_e32 v130, 0xa00, v34
	v_add_u32_e32 v138, 0xb00, v34
	v_mov_b32_e32 v119, -1
	v_mov_b32_e32 v127, -1
	v_mov_b32_e32 v135, -1
	v_mov_b32_e32 v143, -1
	v_cmp_eq_u32_e32 vcc, v113, v2
	v_cmp_eq_u32_e64 s[0:1], v121, v2
	v_cmp_eq_u32_e64 s[6:7], v129, v2
	v_cmp_eq_u32_e64 s[8:9], v137, v2
	v_cndmask_b32_e32 v119, v119, v104, vcc
	v_cndmask_b32_e64 v127, v127, v104, s[0:1]
	v_cndmask_b32_e64 v135, v135, v104, s[6:7]
	v_cndmask_b32_e64 v143, v143, v104, s[8:9]
	v_cmp_eq_u32_e32 vcc, v113, v3
	v_cmp_eq_u32_e64 s[0:1], v121, v3
	v_cmp_eq_u32_e64 s[6:7], v129, v3
	v_cmp_eq_u32_e64 s[8:9], v137, v3
	v_cndmask_b32_e32 v119, v119, v105, vcc
	v_cndmask_b32_e64 v127, v127, v105, s[0:1]
	v_cndmask_b32_e64 v135, v135, v105, s[6:7]
	v_cndmask_b32_e64 v143, v143, v105, s[8:9]
	v_cmp_eq_u32_e32 vcc, v113, v4
	v_cmp_eq_u32_e64 s[0:1], v121, v4
	v_cmp_eq_u32_e64 s[6:7], v129, v4
	v_cmp_eq_u32_e64 s[8:9], v137, v4
	v_cndmask_b32_e32 v119, v119, v106, vcc
	v_cndmask_b32_e64 v127, v127, v106, s[0:1]
	v_cndmask_b32_e64 v135, v135, v106, s[6:7]
	v_cndmask_b32_e64 v143, v143, v106, s[8:9]
	v_cmp_eq_u32_e32 vcc, v113, v5
	v_cmp_eq_u32_e64 s[0:1], v121, v5
	v_cmp_eq_u32_e64 s[6:7], v129, v5
	v_cmp_eq_u32_e64 s[8:9], v137, v5
	v_cndmask_b32_e32 v119, v119, v107, vcc
	v_cndmask_b32_e64 v127, v127, v107, s[0:1]
	v_cndmask_b32_e64 v135, v135, v107, s[6:7]
	v_cndmask_b32_e64 v143, v143, v107, s[8:9]
	v_cmp_eq_u32_e32 vcc, v113, v6
	v_cmp_eq_u32_e64 s[0:1], v121, v6
	v_cmp_eq_u32_e64 s[6:7], v129, v6
	v_cmp_eq_u32_e64 s[8:9], v137, v6
	v_cndmask_b32_e32 v119, v119, v108, vcc
	v_cndmask_b32_e64 v127, v127, v108, s[0:1]
	v_cndmask_b32_e64 v135, v135, v108, s[6:7]
	v_cndmask_b32_e64 v143, v143, v108, s[8:9]
	v_cmp_eq_u32_e32 vcc, v113, v7
	v_cmp_eq_u32_e64 s[0:1], v121, v7
	v_cmp_eq_u32_e64 s[6:7], v129, v7
	v_cmp_eq_u32_e64 s[8:9], v137, v7
	v_cndmask_b32_e32 v119, v119, v109, vcc
	v_cndmask_b32_e64 v127, v127, v109, s[0:1]
	v_cndmask_b32_e64 v135, v135, v109, s[6:7]
	v_cndmask_b32_e64 v143, v143, v109, s[8:9]
	v_cmp_eq_u32_e32 vcc, v113, v8
	v_cmp_eq_u32_e64 s[0:1], v121, v8
	v_cmp_eq_u32_e64 s[6:7], v129, v8
	v_cmp_eq_u32_e64 s[8:9], v137, v8
	v_cndmask_b32_e32 v119, v119, v110, vcc
	v_cndmask_b32_e64 v127, v127, v110, s[0:1]
	v_cndmask_b32_e64 v135, v135, v110, s[6:7]
	v_cndmask_b32_e64 v143, v143, v110, s[8:9]
	v_cmp_eq_u32_e32 vcc, v113, v9
	v_cmp_eq_u32_e64 s[0:1], v121, v9
	v_cmp_eq_u32_e64 s[6:7], v129, v9
	v_cmp_eq_u32_e64 s[8:9], v137, v9
	v_cndmask_b32_e32 v119, v119, v111, vcc
	v_cndmask_b32_e64 v127, v127, v111, s[0:1]
	v_cndmask_b32_e64 v135, v135, v111, s[6:7]
	v_cndmask_b32_e64 v143, v143, v111, s[8:9]
	v_add_u32_e32 v112, v112, v119
	v_add_u32_e32 v120, v120, v127
	v_add_u32_e32 v128, v128, v135
	v_add_u32_e32 v136, v136, v143
	v_cmp_ne_u32_e32 vcc, -1, v119
	s_and_saveexec_b64 s[24:25], vcc
	ds_write_b32 v112, v114
	s_mov_b64 exec, s[24:25]
	v_cmp_ne_u32_e32 vcc, -1, v127
	s_and_saveexec_b64 s[24:25], vcc
	ds_write_b32 v120, v122
	s_mov_b64 exec, s[24:25]
	v_cmp_ne_u32_e32 vcc, -1, v135
	s_and_saveexec_b64 s[24:25], vcc
	ds_write_b32 v128, v130
	s_mov_b64 exec, s[24:25]
	v_cmp_ne_u32_e32 vcc, -1, v143
	s_and_saveexec_b64 s[24:25], vcc
	ds_write_b32 v136, v138
	s_mov_b64 exec, s[24:25]
	v_and_b32_e32 v112, 0xff, v52
	v_and_b32_e32 v120, 0xff, v53
	v_and_b32_e32 v128, 0xff, v54
	v_and_b32_e32 v136, 0xff, v55
	v_lshlrev_b32_e32 v112, 2, v112
	v_lshlrev_b32_e32 v120, 2, v120
	v_lshlrev_b32_e32 v128, 2, v128
	v_lshlrev_b32_e32 v136, 2, v136
	v_add_u32_e32 v118, v112, v11
	v_add_u32_e32 v126, v120, v11
	v_add_u32_e32 v134, v128, v11
	v_add_u32_e32 v142, v136, v11
	ds_read_b32 v113, v112 offset:36864
	ds_read_b32 v114, v112 offset:35200
	ds_read_b32 v115, v118 offset:6144
	ds_read_b32 v121, v120 offset:36864
	ds_read_b32 v122, v120 offset:35200
	ds_read_b32 v123, v126 offset:6656
	ds_read_b32 v129, v128 offset:36864
	ds_read_b32 v130, v128 offset:35200
	ds_read_b32 v131, v134 offset:7168
	ds_read_b32 v137, v136 offset:36864
	ds_read_b32 v138, v136 offset:35200
	ds_read_b32 v139, v142 offset:7680
	v_add_u32_e32 v117, 48, v36
	v_add_u32_e32 v125, 52, v36
	v_add_u32_e32 v133, 56, v36
	v_add_u32_e32 v141, 60, v36
	v_mul_hi_u32 v118, v117, v16
	v_mul_hi_u32 v126, v125, v16
	v_mul_hi_u32 v134, v133, v16
	v_mul_hi_u32 v142, v141, v16
	v_mul_lo_u32 v118, v118, s11
	v_mul_lo_u32 v126, v126, s11
	v_mul_lo_u32 v134, v134, s11
	v_mul_lo_u32 v142, v142, s11
	v_sub_u32_e32 v117, v117, v118
	v_sub_u32_e32 v125, v125, v126
	v_sub_u32_e32 v133, v133, v134
	v_sub_u32_e32 v141, v141, v142
	v_subrev_u32_e32 v118, s11, v117
	v_subrev_u32_e32 v126, s11, v125
	v_subrev_u32_e32 v134, s11, v133
	v_subrev_u32_e32 v142, s11, v141
	v_cmp_le_u32_e32 vcc, s11, v117
	v_cmp_le_u32_e64 s[0:1], s11, v125
	v_cmp_le_u32_e64 s[6:7], s11, v133
	v_cmp_le_u32_e64 s[8:9], s11, v141
	v_cndmask_b32_e32 v117, v117, v118, vcc
	v_cndmask_b32_e64 v125, v125, v126, s[0:1]
	v_cndmask_b32_e64 v133, v133, v134, s[6:7]
	v_cndmask_b32_e64 v141, v141, v142, s[8:9]
	v_subrev_u32_e32 v118, s11, v117
	v_subrev_u32_e32 v126, s11, v125
	v_subrev_u32_e32 v134, s11, v133
	v_subrev_u32_e32 v142, s11, v141
	v_cmp_le_u32_e32 vcc, s11, v117
	v_cmp_le_u32_e64 s[0:1], s11, v125
	v_cmp_le_u32_e64 s[6:7], s11, v133
	v_cmp_le_u32_e64 s[8:9], s11, v141
	v_cndmask_b32_e32 v117, v117, v118, vcc
	v_cndmask_b32_e64 v125, v125, v126, s[0:1]
	v_cndmask_b32_e64 v133, v133, v134, s[6:7]
	v_cndmask_b32_e64 v141, v141, v142, s[8:9]
	v_ashrrev_i32_e32 v116, 8, v52
	v_ashrrev_i32_e32 v124, 8, v53
	v_ashrrev_i32_e32 v132, 8, v54
	v_ashrrev_i32_e32 v140, 8, v55
	s_waitcnt lgkmcnt(0)
	v_add_u32_e32 v116, v116, v113
	v_add_u32_e32 v124, v124, v121
	v_add_u32_e32 v132, v132, v129
	v_add_u32_e32 v140, v140, v137
	v_add3_u32 v116, v116, v114, v115
	v_add3_u32 v124, v124, v122, v123
	v_add3_u32 v132, v132, v130, v131
	v_add3_u32 v140, v140, v138, v139
	v_cmp_eq_u32_e32 vcc, s93, v117
	v_add_u32_e32 v1, 0x6000, v10
	s_and_saveexec_b64 s[24:25], vcc
	global_store_dword v1, v116, s[16:17]
	s_mov_b64 exec, s[24:25]
	v_cmp_eq_u32_e32 vcc, s93, v125
	v_add_u32_e32 v1, 0x6800, v10
	s_and_saveexec_b64 s[24:25], vcc
	global_store_dword v1, v124, s[16:17]
	s_mov_b64 exec, s[24:25]
	v_cmp_eq_u32_e32 vcc, s93, v133
	v_add_u32_e32 v1, 0x7000, v10
	s_and_saveexec_b64 s[24:25], vcc
	global_store_dword v1, v132, s[16:17]
	s_mov_b64 exec, s[24:25]
	v_cmp_eq_u32_e32 vcc, s93, v141
	v_add_u32_e32 v1, 0x7800, v10
	s_and_saveexec_b64 s[24:25], vcc
	global_store_dword v1, v140, s[16:17]
	s_mov_b64 exec, s[24:25]
	v_ashrrev_i32_e32 v113, 8, v116
	v_ashrrev_i32_e32 v121, 8, v124
	v_ashrrev_i32_e32 v129, 8, v132
	v_ashrrev_i32_e32 v137, 8, v140
	v_and_b32_e32 v112, 0xff, v116
	v_and_b32_e32 v120, 0xff, v124
	v_and_b32_e32 v128, 0xff, v132
	v_and_b32_e32 v136, 0xff, v140
	v_lshl_add_u32 v112, v112, 2, s10
	v_lshl_add_u32 v120, v120, 2, s10
	v_lshl_add_u32 v128, v128, 2, s10
	v_lshl_add_u32 v136, v136, 2, s10
	v_add_u32_e32 v114, 0xc00, v34
	v_add_u32_e32 v122, 0xd00, v34
	v_add_u32_e32 v130, 0xe00, v34
	v_add_u32_e32 v138, 0xf00, v34
	v_mov_b32_e32 v119, -1
	v_mov_b32_e32 v127, -1
	v_mov_b32_e32 v135, -1
	v_mov_b32_e32 v143, -1
	v_cmp_eq_u32_e32 vcc, v113, v2
	v_cmp_eq_u32_e64 s[0:1], v121, v2
	v_cmp_eq_u32_e64 s[6:7], v129, v2
	v_cmp_eq_u32_e64 s[8:9], v137, v2
	v_cndmask_b32_e32 v119, v119, v104, vcc
	v_cndmask_b32_e64 v127, v127, v104, s[0:1]
	v_cndmask_b32_e64 v135, v135, v104, s[6:7]
	v_cndmask_b32_e64 v143, v143, v104, s[8:9]
	v_cmp_eq_u32_e32 vcc, v113, v3
	v_cmp_eq_u32_e64 s[0:1], v121, v3
	v_cmp_eq_u32_e64 s[6:7], v129, v3
	v_cmp_eq_u32_e64 s[8:9], v137, v3
	v_cndmask_b32_e32 v119, v119, v105, vcc
	v_cndmask_b32_e64 v127, v127, v105, s[0:1]
	v_cndmask_b32_e64 v135, v135, v105, s[6:7]
	v_cndmask_b32_e64 v143, v143, v105, s[8:9]
	v_cmp_eq_u32_e32 vcc, v113, v4
	v_cmp_eq_u32_e64 s[0:1], v121, v4
	v_cmp_eq_u32_e64 s[6:7], v129, v4
	v_cmp_eq_u32_e64 s[8:9], v137, v4
	v_cndmask_b32_e32 v119, v119, v106, vcc
	v_cndmask_b32_e64 v127, v127, v106, s[0:1]
	v_cndmask_b32_e64 v135, v135, v106, s[6:7]
	v_cndmask_b32_e64 v143, v143, v106, s[8:9]
	v_cmp_eq_u32_e32 vcc, v113, v5
	v_cmp_eq_u32_e64 s[0:1], v121, v5
	v_cmp_eq_u32_e64 s[6:7], v129, v5
	v_cmp_eq_u32_e64 s[8:9], v137, v5
	v_cndmask_b32_e32 v119, v119, v107, vcc
	v_cndmask_b32_e64 v127, v127, v107, s[0:1]
	v_cndmask_b32_e64 v135, v135, v107, s[6:7]
	v_cndmask_b32_e64 v143, v143, v107, s[8:9]
	v_cmp_eq_u32_e32 vcc, v113, v6
	v_cmp_eq_u32_e64 s[0:1], v121, v6
	v_cmp_eq_u32_e64 s[6:7], v129, v6
	v_cmp_eq_u32_e64 s[8:9], v137, v6
	v_cndmask_b32_e32 v119, v119, v108, vcc
	v_cndmask_b32_e64 v127, v127, v108, s[0:1]
	v_cndmask_b32_e64 v135, v135, v108, s[6:7]
	v_cndmask_b32_e64 v143, v143, v108, s[8:9]
	v_cmp_eq_u32_e32 vcc, v113, v7
	v_cmp_eq_u32_e64 s[0:1], v121, v7
	v_cmp_eq_u32_e64 s[6:7], v129, v7
	v_cmp_eq_u32_e64 s[8:9], v137, v7
	v_cndmask_b32_e32 v119, v119, v109, vcc
	v_cndmask_b32_e64 v127, v127, v109, s[0:1]
	v_cndmask_b32_e64 v135, v135, v109, s[6:7]
	v_cndmask_b32_e64 v143, v143, v109, s[8:9]
	v_cmp_eq_u32_e32 vcc, v113, v8
	v_cmp_eq_u32_e64 s[0:1], v121, v8
	v_cmp_eq_u32_e64 s[6:7], v129, v8
	v_cmp_eq_u32_e64 s[8:9], v137, v8
	v_cndmask_b32_e32 v119, v119, v110, vcc
	v_cndmask_b32_e64 v127, v127, v110, s[0:1]
	v_cndmask_b32_e64 v135, v135, v110, s[6:7]
	v_cndmask_b32_e64 v143, v143, v110, s[8:9]
	v_cmp_eq_u32_e32 vcc, v113, v9
	v_cmp_eq_u32_e64 s[0:1], v121, v9
	v_cmp_eq_u32_e64 s[6:7], v129, v9
	v_cmp_eq_u32_e64 s[8:9], v137, v9
	v_cndmask_b32_e32 v119, v119, v111, vcc
	v_cndmask_b32_e64 v127, v127, v111, s[0:1]
	v_cndmask_b32_e64 v135, v135, v111, s[6:7]
	v_cndmask_b32_e64 v143, v143, v111, s[8:9]
	v_add_u32_e32 v112, v112, v119
	v_add_u32_e32 v120, v120, v127
	v_add_u32_e32 v128, v128, v135
	v_add_u32_e32 v136, v136, v143
	v_cmp_ne_u32_e32 vcc, -1, v119
	s_and_saveexec_b64 s[24:25], vcc
	ds_write_b32 v112, v114
	s_mov_b64 exec, s[24:25]
	v_cmp_ne_u32_e32 vcc, -1, v127
	s_and_saveexec_b64 s[24:25], vcc
	ds_write_b32 v120, v122
	s_mov_b64 exec, s[24:25]
	v_cmp_ne_u32_e32 vcc, -1, v135
	s_and_saveexec_b64 s[24:25], vcc
	ds_write_b32 v128, v130
	s_mov_b64 exec, s[24:25]
	v_cmp_ne_u32_e32 vcc, -1, v143
	s_and_saveexec_b64 s[24:25], vcc
	ds_write_b32 v136, v138
	s_mov_b64 exec, s[24:25]
	v_and_b32_e32 v112, 0xff, v56
	v_and_b32_e32 v120, 0xff, v57
	v_and_b32_e32 v128, 0xff, v58
	v_and_b32_e32 v136, 0xff, v59
	v_lshlrev_b32_e32 v112, 2, v112
	v_lshlrev_b32_e32 v120, 2, v120
	v_lshlrev_b32_e32 v128, 2, v128
	v_lshlrev_b32_e32 v136, 2, v136
	v_add_u32_e32 v118, v112, v11
	v_add_u32_e32 v126, v120, v11
	v_add_u32_e32 v134, v128, v11
	v_add_u32_e32 v142, v136, v11
	ds_read_b32 v113, v112 offset:36864
	ds_read_b32 v114, v112 offset:35328
	ds_read_b32 v115, v118 offset:8192
	ds_read_b32 v121, v120 offset:36864
	ds_read_b32 v122, v120 offset:35328
	ds_read_b32 v123, v126 offset:8704
	ds_read_b32 v129, v128 offset:36864
	ds_read_b32 v130, v128 offset:35328
	ds_read_b32 v131, v134 offset:9216
	ds_read_b32 v137, v136 offset:36864
	ds_read_b32 v138, v136 offset:35328
	ds_read_b32 v139, v142 offset:9728
	v_add_u32_e32 v117, 64, v36
	v_add_u32_e32 v125, 68, v36
	v_add_u32_e32 v133, 72, v36
	v_add_u32_e32 v141, 76, v36
	v_mul_hi_u32 v118, v117, v16
	v_mul_hi_u32 v126, v125, v16
	v_mul_hi_u32 v134, v133, v16
	v_mul_hi_u32 v142, v141, v16
	v_mul_lo_u32 v118, v118, s11
	v_mul_lo_u32 v126, v126, s11
	v_mul_lo_u32 v134, v134, s11
	v_mul_lo_u32 v142, v142, s11
	v_sub_u32_e32 v117, v117, v118
	v_sub_u32_e32 v125, v125, v126
	v_sub_u32_e32 v133, v133, v134
	v_sub_u32_e32 v141, v141, v142
	v_subrev_u32_e32 v118, s11, v117
	v_subrev_u32_e32 v126, s11, v125
	v_subrev_u32_e32 v134, s11, v133
	v_subrev_u32_e32 v142, s11, v141
	v_cmp_le_u32_e32 vcc, s11, v117
	v_cmp_le_u32_e64 s[0:1], s11, v125
	v_cmp_le_u32_e64 s[6:7], s11, v133
	v_cmp_le_u32_e64 s[8:9], s11, v141
	v_cndmask_b32_e32 v117, v117, v118, vcc
	v_cndmask_b32_e64 v125, v125, v126, s[0:1]
	v_cndmask_b32_e64 v133, v133, v134, s[6:7]
	v_cndmask_b32_e64 v141, v141, v142, s[8:9]
	v_subrev_u32_e32 v118, s11, v117
	v_subrev_u32_e32 v126, s11, v125
	v_subrev_u32_e32 v134, s11, v133
	v_subrev_u32_e32 v142, s11, v141
	v_cmp_le_u32_e32 vcc, s11, v117
	v_cmp_le_u32_e64 s[0:1], s11, v125
	v_cmp_le_u32_e64 s[6:7], s11, v133
	v_cmp_le_u32_e64 s[8:9], s11, v141
	v_cndmask_b32_e32 v117, v117, v118, vcc
	v_cndmask_b32_e64 v125, v125, v126, s[0:1]
	v_cndmask_b32_e64 v133, v133, v134, s[6:7]
	v_cndmask_b32_e64 v141, v141, v142, s[8:9]
	v_ashrrev_i32_e32 v116, 8, v56
	v_ashrrev_i32_e32 v124, 8, v57
	v_ashrrev_i32_e32 v132, 8, v58
	v_ashrrev_i32_e32 v140, 8, v59
	s_waitcnt lgkmcnt(0)
	v_add_u32_e32 v116, v116, v113
	v_add_u32_e32 v124, v124, v121
	v_add_u32_e32 v132, v132, v129
	v_add_u32_e32 v140, v140, v137
	v_add3_u32 v116, v116, v114, v115
	v_add3_u32 v124, v124, v122, v123
	v_add3_u32 v132, v132, v130, v131
	v_add3_u32 v140, v140, v138, v139
	v_cmp_eq_u32_e32 vcc, s93, v117
	v_add_u32_e32 v1, 0x8000, v10
	s_and_saveexec_b64 s[24:25], vcc
	global_store_dword v1, v116, s[16:17]
	s_mov_b64 exec, s[24:25]
	v_cmp_eq_u32_e32 vcc, s93, v125
	v_add_u32_e32 v1, 0x8800, v10
	s_and_saveexec_b64 s[24:25], vcc
	global_store_dword v1, v124, s[16:17]
	s_mov_b64 exec, s[24:25]
	v_cmp_eq_u32_e32 vcc, s93, v133
	v_add_u32_e32 v1, 0x9000, v10
	s_and_saveexec_b64 s[24:25], vcc
	global_store_dword v1, v132, s[16:17]
	s_mov_b64 exec, s[24:25]
	v_cmp_eq_u32_e32 vcc, s93, v141
	v_add_u32_e32 v1, 0x9800, v10
	s_and_saveexec_b64 s[24:25], vcc
	global_store_dword v1, v140, s[16:17]
	s_mov_b64 exec, s[24:25]
	v_ashrrev_i32_e32 v113, 8, v116
	v_ashrrev_i32_e32 v121, 8, v124
	v_ashrrev_i32_e32 v129, 8, v132
	v_ashrrev_i32_e32 v137, 8, v140
	v_and_b32_e32 v112, 0xff, v116
	v_and_b32_e32 v120, 0xff, v124
	v_and_b32_e32 v128, 0xff, v132
	v_and_b32_e32 v136, 0xff, v140
	v_lshl_add_u32 v112, v112, 2, s10
	v_lshl_add_u32 v120, v120, 2, s10
	v_lshl_add_u32 v128, v128, 2, s10
	v_lshl_add_u32 v136, v136, 2, s10
	v_add_u32_e32 v114, 0x1000, v34
	v_add_u32_e32 v122, 0x1100, v34
	v_add_u32_e32 v130, 0x1200, v34
	v_add_u32_e32 v138, 0x1300, v34
	v_mov_b32_e32 v119, -1
	v_mov_b32_e32 v127, -1
	v_mov_b32_e32 v135, -1
	v_mov_b32_e32 v143, -1
	v_cmp_eq_u32_e32 vcc, v113, v2
	v_cmp_eq_u32_e64 s[0:1], v121, v2
	v_cmp_eq_u32_e64 s[6:7], v129, v2
	v_cmp_eq_u32_e64 s[8:9], v137, v2
	v_cndmask_b32_e32 v119, v119, v104, vcc
	v_cndmask_b32_e64 v127, v127, v104, s[0:1]
	v_cndmask_b32_e64 v135, v135, v104, s[6:7]
	v_cndmask_b32_e64 v143, v143, v104, s[8:9]
	v_cmp_eq_u32_e32 vcc, v113, v3
	v_cmp_eq_u32_e64 s[0:1], v121, v3
	v_cmp_eq_u32_e64 s[6:7], v129, v3
	v_cmp_eq_u32_e64 s[8:9], v137, v3
	v_cndmask_b32_e32 v119, v119, v105, vcc
	v_cndmask_b32_e64 v127, v127, v105, s[0:1]
	v_cndmask_b32_e64 v135, v135, v105, s[6:7]
	v_cndmask_b32_e64 v143, v143, v105, s[8:9]
	v_cmp_eq_u32_e32 vcc, v113, v4
	v_cmp_eq_u32_e64 s[0:1], v121, v4
	v_cmp_eq_u32_e64 s[6:7], v129, v4
	v_cmp_eq_u32_e64 s[8:9], v137, v4
	v_cndmask_b32_e32 v119, v119, v106, vcc
	v_cndmask_b32_e64 v127, v127, v106, s[0:1]
	v_cndmask_b32_e64 v135, v135, v106, s[6:7]
	v_cndmask_b32_e64 v143, v143, v106, s[8:9]
	v_cmp_eq_u32_e32 vcc, v113, v5
	v_cmp_eq_u32_e64 s[0:1], v121, v5
	v_cmp_eq_u32_e64 s[6:7], v129, v5
	v_cmp_eq_u32_e64 s[8:9], v137, v5
	v_cndmask_b32_e32 v119, v119, v107, vcc
	v_cndmask_b32_e64 v127, v127, v107, s[0:1]
	v_cndmask_b32_e64 v135, v135, v107, s[6:7]
	v_cndmask_b32_e64 v143, v143, v107, s[8:9]
	v_cmp_eq_u32_e32 vcc, v113, v6
	v_cmp_eq_u32_e64 s[0:1], v121, v6
	v_cmp_eq_u32_e64 s[6:7], v129, v6
	v_cmp_eq_u32_e64 s[8:9], v137, v6
	v_cndmask_b32_e32 v119, v119, v108, vcc
	v_cndmask_b32_e64 v127, v127, v108, s[0:1]
	v_cndmask_b32_e64 v135, v135, v108, s[6:7]
	v_cndmask_b32_e64 v143, v143, v108, s[8:9]
	v_cmp_eq_u32_e32 vcc, v113, v7
	v_cmp_eq_u32_e64 s[0:1], v121, v7
	v_cmp_eq_u32_e64 s[6:7], v129, v7
	v_cmp_eq_u32_e64 s[8:9], v137, v7
	v_cndmask_b32_e32 v119, v119, v109, vcc
	v_cndmask_b32_e64 v127, v127, v109, s[0:1]
	v_cndmask_b32_e64 v135, v135, v109, s[6:7]
	v_cndmask_b32_e64 v143, v143, v109, s[8:9]
	v_cmp_eq_u32_e32 vcc, v113, v8
	v_cmp_eq_u32_e64 s[0:1], v121, v8
	v_cmp_eq_u32_e64 s[6:7], v129, v8
	v_cmp_eq_u32_e64 s[8:9], v137, v8
	v_cndmask_b32_e32 v119, v119, v110, vcc
	v_cndmask_b32_e64 v127, v127, v110, s[0:1]
	v_cndmask_b32_e64 v135, v135, v110, s[6:7]
	v_cndmask_b32_e64 v143, v143, v110, s[8:9]
	v_cmp_eq_u32_e32 vcc, v113, v9
	v_cmp_eq_u32_e64 s[0:1], v121, v9
	v_cmp_eq_u32_e64 s[6:7], v129, v9
	v_cmp_eq_u32_e64 s[8:9], v137, v9
	v_cndmask_b32_e32 v119, v119, v111, vcc
	v_cndmask_b32_e64 v127, v127, v111, s[0:1]
	v_cndmask_b32_e64 v135, v135, v111, s[6:7]
	v_cndmask_b32_e64 v143, v143, v111, s[8:9]
	v_add_u32_e32 v112, v112, v119
	v_add_u32_e32 v120, v120, v127
	v_add_u32_e32 v128, v128, v135
	v_add_u32_e32 v136, v136, v143
	v_cmp_ne_u32_e32 vcc, -1, v119
	s_and_saveexec_b64 s[24:25], vcc
	ds_write_b32 v112, v114
	s_mov_b64 exec, s[24:25]
	v_cmp_ne_u32_e32 vcc, -1, v127
	s_and_saveexec_b64 s[24:25], vcc
	ds_write_b32 v120, v122
	s_mov_b64 exec, s[24:25]
	v_cmp_ne_u32_e32 vcc, -1, v135
	s_and_saveexec_b64 s[24:25], vcc
	ds_write_b32 v128, v130
	s_mov_b64 exec, s[24:25]
	v_cmp_ne_u32_e32 vcc, -1, v143
	s_and_saveexec_b64 s[24:25], vcc
	ds_write_b32 v136, v138
	s_mov_b64 exec, s[24:25]
	v_and_b32_e32 v112, 0xff, v60
	v_and_b32_e32 v120, 0xff, v61
	v_and_b32_e32 v128, 0xff, v62
	v_and_b32_e32 v136, 0xff, v63
	v_lshlrev_b32_e32 v112, 2, v112
	v_lshlrev_b32_e32 v120, 2, v120
	v_lshlrev_b32_e32 v128, 2, v128
	v_lshlrev_b32_e32 v136, 2, v136
	v_add_u32_e32 v118, v112, v11
	v_add_u32_e32 v126, v120, v11
	v_add_u32_e32 v134, v128, v11
	v_add_u32_e32 v142, v136, v11
	ds_read_b32 v113, v112 offset:36864
	ds_read_b32 v114, v112 offset:35456
	ds_read_b32 v115, v118 offset:10240
	ds_read_b32 v121, v120 offset:36864
	ds_read_b32 v122, v120 offset:35456
	ds_read_b32 v123, v126 offset:10752
	ds_read_b32 v129, v128 offset:36864
	ds_read_b32 v130, v128 offset:35456
	ds_read_b32 v131, v134 offset:11264
	ds_read_b32 v137, v136 offset:36864
	ds_read_b32 v138, v136 offset:35456
	ds_read_b32 v139, v142 offset:11776
	v_add_u32_e32 v117, 80, v36
	v_add_u32_e32 v125, 84, v36
	v_add_u32_e32 v133, 88, v36
	v_add_u32_e32 v141, 92, v36
	v_mul_hi_u32 v118, v117, v16
	v_mul_hi_u32 v126, v125, v16
	v_mul_hi_u32 v134, v133, v16
	v_mul_hi_u32 v142, v141, v16
	v_mul_lo_u32 v118, v118, s11
	v_mul_lo_u32 v126, v126, s11
	v_mul_lo_u32 v134, v134, s11
	v_mul_lo_u32 v142, v142, s11
	v_sub_u32_e32 v117, v117, v118
	v_sub_u32_e32 v125, v125, v126
	v_sub_u32_e32 v133, v133, v134
	v_sub_u32_e32 v141, v141, v142
	v_subrev_u32_e32 v118, s11, v117
	v_subrev_u32_e32 v126, s11, v125
	v_subrev_u32_e32 v134, s11, v133
	v_subrev_u32_e32 v142, s11, v141
	v_cmp_le_u32_e32 vcc, s11, v117
	v_cmp_le_u32_e64 s[0:1], s11, v125
	v_cmp_le_u32_e64 s[6:7], s11, v133
	v_cmp_le_u32_e64 s[8:9], s11, v141
	v_cndmask_b32_e32 v117, v117, v118, vcc
	v_cndmask_b32_e64 v125, v125, v126, s[0:1]
	v_cndmask_b32_e64 v133, v133, v134, s[6:7]
	v_cndmask_b32_e64 v141, v141, v142, s[8:9]
	v_subrev_u32_e32 v118, s11, v117
	v_subrev_u32_e32 v126, s11, v125
	v_subrev_u32_e32 v134, s11, v133
	v_subrev_u32_e32 v142, s11, v141
	v_cmp_le_u32_e32 vcc, s11, v117
	v_cmp_le_u32_e64 s[0:1], s11, v125
	v_cmp_le_u32_e64 s[6:7], s11, v133
	v_cmp_le_u32_e64 s[8:9], s11, v141
	v_cndmask_b32_e32 v117, v117, v118, vcc
	v_cndmask_b32_e64 v125, v125, v126, s[0:1]
	v_cndmask_b32_e64 v133, v133, v134, s[6:7]
	v_cndmask_b32_e64 v141, v141, v142, s[8:9]
	v_ashrrev_i32_e32 v116, 8, v60
	v_ashrrev_i32_e32 v124, 8, v61
	v_ashrrev_i32_e32 v132, 8, v62
	v_ashrrev_i32_e32 v140, 8, v63
	s_waitcnt lgkmcnt(0)
	v_add_u32_e32 v116, v116, v113
	v_add_u32_e32 v124, v124, v121
	v_add_u32_e32 v132, v132, v129
	v_add_u32_e32 v140, v140, v137
	v_add3_u32 v116, v116, v114, v115
	v_add3_u32 v124, v124, v122, v123
	v_add3_u32 v132, v132, v130, v131
	v_add3_u32 v140, v140, v138, v139
	v_cmp_eq_u32_e32 vcc, s93, v117
	v_add_u32_e32 v1, 0xa000, v10
	s_and_saveexec_b64 s[24:25], vcc
	global_store_dword v1, v116, s[16:17]
	s_mov_b64 exec, s[24:25]
	v_cmp_eq_u32_e32 vcc, s93, v125
	v_add_u32_e32 v1, 0xa800, v10
	s_and_saveexec_b64 s[24:25], vcc
	global_store_dword v1, v124, s[16:17]
	s_mov_b64 exec, s[24:25]
	v_cmp_eq_u32_e32 vcc, s93, v133
	v_add_u32_e32 v1, 0xb000, v10
	s_and_saveexec_b64 s[24:25], vcc
	global_store_dword v1, v132, s[16:17]
	s_mov_b64 exec, s[24:25]
	v_cmp_eq_u32_e32 vcc, s93, v141
	v_add_u32_e32 v1, 0xb800, v10
	s_and_saveexec_b64 s[24:25], vcc
	global_store_dword v1, v140, s[16:17]
	s_mov_b64 exec, s[24:25]
	v_ashrrev_i32_e32 v113, 8, v116
	v_ashrrev_i32_e32 v121, 8, v124
	v_ashrrev_i32_e32 v129, 8, v132
	v_ashrrev_i32_e32 v137, 8, v140
	v_and_b32_e32 v112, 0xff, v116
	v_and_b32_e32 v120, 0xff, v124
	v_and_b32_e32 v128, 0xff, v132
	v_and_b32_e32 v136, 0xff, v140
	v_lshl_add_u32 v112, v112, 2, s10
	v_lshl_add_u32 v120, v120, 2, s10
	v_lshl_add_u32 v128, v128, 2, s10
	v_lshl_add_u32 v136, v136, 2, s10
	v_add_u32_e32 v114, 0x1400, v34
	v_add_u32_e32 v122, 0x1500, v34
	v_add_u32_e32 v130, 0x1600, v34
	v_add_u32_e32 v138, 0x1700, v34
	v_mov_b32_e32 v119, -1
	v_mov_b32_e32 v127, -1
	v_mov_b32_e32 v135, -1
	v_mov_b32_e32 v143, -1
	v_cmp_eq_u32_e32 vcc, v113, v2
	v_cmp_eq_u32_e64 s[0:1], v121, v2
	v_cmp_eq_u32_e64 s[6:7], v129, v2
	v_cmp_eq_u32_e64 s[8:9], v137, v2
	v_cndmask_b32_e32 v119, v119, v104, vcc
	v_cndmask_b32_e64 v127, v127, v104, s[0:1]
	v_cndmask_b32_e64 v135, v135, v104, s[6:7]
	v_cndmask_b32_e64 v143, v143, v104, s[8:9]
	v_cmp_eq_u32_e32 vcc, v113, v3
	v_cmp_eq_u32_e64 s[0:1], v121, v3
	v_cmp_eq_u32_e64 s[6:7], v129, v3
	v_cmp_eq_u32_e64 s[8:9], v137, v3
	v_cndmask_b32_e32 v119, v119, v105, vcc
	v_cndmask_b32_e64 v127, v127, v105, s[0:1]
	v_cndmask_b32_e64 v135, v135, v105, s[6:7]
	v_cndmask_b32_e64 v143, v143, v105, s[8:9]
	v_cmp_eq_u32_e32 vcc, v113, v4
	v_cmp_eq_u32_e64 s[0:1], v121, v4
	v_cmp_eq_u32_e64 s[6:7], v129, v4
	v_cmp_eq_u32_e64 s[8:9], v137, v4
	v_cndmask_b32_e32 v119, v119, v106, vcc
	v_cndmask_b32_e64 v127, v127, v106, s[0:1]
	v_cndmask_b32_e64 v135, v135, v106, s[6:7]
	v_cndmask_b32_e64 v143, v143, v106, s[8:9]
	v_cmp_eq_u32_e32 vcc, v113, v5
	v_cmp_eq_u32_e64 s[0:1], v121, v5
	v_cmp_eq_u32_e64 s[6:7], v129, v5
	v_cmp_eq_u32_e64 s[8:9], v137, v5
	v_cndmask_b32_e32 v119, v119, v107, vcc
	v_cndmask_b32_e64 v127, v127, v107, s[0:1]
	v_cndmask_b32_e64 v135, v135, v107, s[6:7]
	v_cndmask_b32_e64 v143, v143, v107, s[8:9]
	v_cmp_eq_u32_e32 vcc, v113, v6
	v_cmp_eq_u32_e64 s[0:1], v121, v6
	v_cmp_eq_u32_e64 s[6:7], v129, v6
	v_cmp_eq_u32_e64 s[8:9], v137, v6
	v_cndmask_b32_e32 v119, v119, v108, vcc
	v_cndmask_b32_e64 v127, v127, v108, s[0:1]
	v_cndmask_b32_e64 v135, v135, v108, s[6:7]
	v_cndmask_b32_e64 v143, v143, v108, s[8:9]
	v_cmp_eq_u32_e32 vcc, v113, v7
	v_cmp_eq_u32_e64 s[0:1], v121, v7
	v_cmp_eq_u32_e64 s[6:7], v129, v7
	v_cmp_eq_u32_e64 s[8:9], v137, v7
	v_cndmask_b32_e32 v119, v119, v109, vcc
	v_cndmask_b32_e64 v127, v127, v109, s[0:1]
	v_cndmask_b32_e64 v135, v135, v109, s[6:7]
	v_cndmask_b32_e64 v143, v143, v109, s[8:9]
	v_cmp_eq_u32_e32 vcc, v113, v8
	v_cmp_eq_u32_e64 s[0:1], v121, v8
	v_cmp_eq_u32_e64 s[6:7], v129, v8
	v_cmp_eq_u32_e64 s[8:9], v137, v8
	v_cndmask_b32_e32 v119, v119, v110, vcc
	v_cndmask_b32_e64 v127, v127, v110, s[0:1]
	v_cndmask_b32_e64 v135, v135, v110, s[6:7]
	v_cndmask_b32_e64 v143, v143, v110, s[8:9]
	v_cmp_eq_u32_e32 vcc, v113, v9
	v_cmp_eq_u32_e64 s[0:1], v121, v9
	v_cmp_eq_u32_e64 s[6:7], v129, v9
	v_cmp_eq_u32_e64 s[8:9], v137, v9
	v_cndmask_b32_e32 v119, v119, v111, vcc
	v_cndmask_b32_e64 v127, v127, v111, s[0:1]
	v_cndmask_b32_e64 v135, v135, v111, s[6:7]
	v_cndmask_b32_e64 v143, v143, v111, s[8:9]
	v_add_u32_e32 v112, v112, v119
	v_add_u32_e32 v120, v120, v127
	v_add_u32_e32 v128, v128, v135
	v_add_u32_e32 v136, v136, v143
	v_cmp_ne_u32_e32 vcc, -1, v119
	s_and_saveexec_b64 s[24:25], vcc
	ds_write_b32 v112, v114
	s_mov_b64 exec, s[24:25]
	v_cmp_ne_u32_e32 vcc, -1, v127
	s_and_saveexec_b64 s[24:25], vcc
	ds_write_b32 v120, v122
	s_mov_b64 exec, s[24:25]
	v_cmp_ne_u32_e32 vcc, -1, v135
	s_and_saveexec_b64 s[24:25], vcc
	ds_write_b32 v128, v130
	s_mov_b64 exec, s[24:25]
	v_cmp_ne_u32_e32 vcc, -1, v143
	s_and_saveexec_b64 s[24:25], vcc
	ds_write_b32 v136, v138
	s_mov_b64 exec, s[24:25]
	v_and_b32_e32 v112, 0xff, v64
	v_and_b32_e32 v120, 0xff, v65
	v_and_b32_e32 v128, 0xff, v66
	v_and_b32_e32 v136, 0xff, v67
	v_lshlrev_b32_e32 v112, 2, v112
	v_lshlrev_b32_e32 v120, 2, v120
	v_lshlrev_b32_e32 v128, 2, v128
	v_lshlrev_b32_e32 v136, 2, v136
	v_add_u32_e32 v118, v112, v11
	v_add_u32_e32 v126, v120, v11
	v_add_u32_e32 v134, v128, v11
	v_add_u32_e32 v142, v136, v11
	ds_read_b32 v113, v112 offset:36864
	ds_read_b32 v114, v112 offset:35584
	ds_read_b32 v115, v118 offset:12288
	ds_read_b32 v121, v120 offset:36864
	ds_read_b32 v122, v120 offset:35584
	ds_read_b32 v123, v126 offset:12800
	ds_read_b32 v129, v128 offset:36864
	ds_read_b32 v130, v128 offset:35584
	ds_read_b32 v131, v134 offset:13312
	ds_read_b32 v137, v136 offset:36864
	ds_read_b32 v138, v136 offset:35584
	ds_read_b32 v139, v142 offset:13824
	v_add_u32_e32 v117, 96, v36
	v_add_u32_e32 v125, 100, v36
	v_add_u32_e32 v133, 104, v36
	v_add_u32_e32 v141, 108, v36
	v_mul_hi_u32 v118, v117, v16
	v_mul_hi_u32 v126, v125, v16
	v_mul_hi_u32 v134, v133, v16
	v_mul_hi_u32 v142, v141, v16
	v_mul_lo_u32 v118, v118, s11
	v_mul_lo_u32 v126, v126, s11
	v_mul_lo_u32 v134, v134, s11
	v_mul_lo_u32 v142, v142, s11
	v_sub_u32_e32 v117, v117, v118
	v_sub_u32_e32 v125, v125, v126
	v_sub_u32_e32 v133, v133, v134
	v_sub_u32_e32 v141, v141, v142
	v_subrev_u32_e32 v118, s11, v117
	v_subrev_u32_e32 v126, s11, v125
	v_subrev_u32_e32 v134, s11, v133
	v_subrev_u32_e32 v142, s11, v141
	v_cmp_le_u32_e32 vcc, s11, v117
	v_cmp_le_u32_e64 s[0:1], s11, v125
	v_cmp_le_u32_e64 s[6:7], s11, v133
	v_cmp_le_u32_e64 s[8:9], s11, v141
	v_cndmask_b32_e32 v117, v117, v118, vcc
	v_cndmask_b32_e64 v125, v125, v126, s[0:1]
	v_cndmask_b32_e64 v133, v133, v134, s[6:7]
	v_cndmask_b32_e64 v141, v141, v142, s[8:9]
	v_subrev_u32_e32 v118, s11, v117
	v_subrev_u32_e32 v126, s11, v125
	v_subrev_u32_e32 v134, s11, v133
	v_subrev_u32_e32 v142, s11, v141
	v_cmp_le_u32_e32 vcc, s11, v117
	v_cmp_le_u32_e64 s[0:1], s11, v125
	v_cmp_le_u32_e64 s[6:7], s11, v133
	v_cmp_le_u32_e64 s[8:9], s11, v141
	v_cndmask_b32_e32 v117, v117, v118, vcc
	v_cndmask_b32_e64 v125, v125, v126, s[0:1]
	v_cndmask_b32_e64 v133, v133, v134, s[6:7]
	v_cndmask_b32_e64 v141, v141, v142, s[8:9]
	v_ashrrev_i32_e32 v116, 8, v64
	v_ashrrev_i32_e32 v124, 8, v65
	v_ashrrev_i32_e32 v132, 8, v66
	v_ashrrev_i32_e32 v140, 8, v67
	s_waitcnt lgkmcnt(0)
	v_add_u32_e32 v116, v116, v113
	v_add_u32_e32 v124, v124, v121
	v_add_u32_e32 v132, v132, v129
	v_add_u32_e32 v140, v140, v137
	v_add3_u32 v116, v116, v114, v115
	v_add3_u32 v124, v124, v122, v123
	v_add3_u32 v132, v132, v130, v131
	v_add3_u32 v140, v140, v138, v139
	v_cmp_eq_u32_e32 vcc, s93, v117
	v_add_u32_e32 v1, 0xc000, v10
	s_and_saveexec_b64 s[24:25], vcc
	global_store_dword v1, v116, s[16:17]
	s_mov_b64 exec, s[24:25]
	v_cmp_eq_u32_e32 vcc, s93, v125
	v_add_u32_e32 v1, 0xc800, v10
	s_and_saveexec_b64 s[24:25], vcc
	global_store_dword v1, v124, s[16:17]
	s_mov_b64 exec, s[24:25]
	v_cmp_eq_u32_e32 vcc, s93, v133
	v_add_u32_e32 v1, 0xd000, v10
	s_and_saveexec_b64 s[24:25], vcc
	global_store_dword v1, v132, s[16:17]
	s_mov_b64 exec, s[24:25]
	v_cmp_eq_u32_e32 vcc, s93, v141
	v_add_u32_e32 v1, 0xd800, v10
	s_and_saveexec_b64 s[24:25], vcc
	global_store_dword v1, v140, s[16:17]
	s_mov_b64 exec, s[24:25]
	v_ashrrev_i32_e32 v113, 8, v116
	v_ashrrev_i32_e32 v121, 8, v124
	v_ashrrev_i32_e32 v129, 8, v132
	v_ashrrev_i32_e32 v137, 8, v140
	v_and_b32_e32 v112, 0xff, v116
	v_and_b32_e32 v120, 0xff, v124
	v_and_b32_e32 v128, 0xff, v132
	v_and_b32_e32 v136, 0xff, v140
	v_lshl_add_u32 v112, v112, 2, s10
	v_lshl_add_u32 v120, v120, 2, s10
	v_lshl_add_u32 v128, v128, 2, s10
	v_lshl_add_u32 v136, v136, 2, s10
	v_add_u32_e32 v114, 0x1800, v34
	v_add_u32_e32 v122, 0x1900, v34
	v_add_u32_e32 v130, 0x1a00, v34
	v_add_u32_e32 v138, 0x1b00, v34
	v_mov_b32_e32 v119, -1
	v_mov_b32_e32 v127, -1
	v_mov_b32_e32 v135, -1
	v_mov_b32_e32 v143, -1
	v_cmp_eq_u32_e32 vcc, v113, v2
	v_cmp_eq_u32_e64 s[0:1], v121, v2
	v_cmp_eq_u32_e64 s[6:7], v129, v2
	v_cmp_eq_u32_e64 s[8:9], v137, v2
	v_cndmask_b32_e32 v119, v119, v104, vcc
	v_cndmask_b32_e64 v127, v127, v104, s[0:1]
	v_cndmask_b32_e64 v135, v135, v104, s[6:7]
	v_cndmask_b32_e64 v143, v143, v104, s[8:9]
	v_cmp_eq_u32_e32 vcc, v113, v3
	v_cmp_eq_u32_e64 s[0:1], v121, v3
	v_cmp_eq_u32_e64 s[6:7], v129, v3
	v_cmp_eq_u32_e64 s[8:9], v137, v3
	v_cndmask_b32_e32 v119, v119, v105, vcc
	v_cndmask_b32_e64 v127, v127, v105, s[0:1]
	v_cndmask_b32_e64 v135, v135, v105, s[6:7]
	v_cndmask_b32_e64 v143, v143, v105, s[8:9]
	v_cmp_eq_u32_e32 vcc, v113, v4
	v_cmp_eq_u32_e64 s[0:1], v121, v4
	v_cmp_eq_u32_e64 s[6:7], v129, v4
	v_cmp_eq_u32_e64 s[8:9], v137, v4
	v_cndmask_b32_e32 v119, v119, v106, vcc
	v_cndmask_b32_e64 v127, v127, v106, s[0:1]
	v_cndmask_b32_e64 v135, v135, v106, s[6:7]
	v_cndmask_b32_e64 v143, v143, v106, s[8:9]
	v_cmp_eq_u32_e32 vcc, v113, v5
	v_cmp_eq_u32_e64 s[0:1], v121, v5
	v_cmp_eq_u32_e64 s[6:7], v129, v5
	v_cmp_eq_u32_e64 s[8:9], v137, v5
	v_cndmask_b32_e32 v119, v119, v107, vcc
	v_cndmask_b32_e64 v127, v127, v107, s[0:1]
	v_cndmask_b32_e64 v135, v135, v107, s[6:7]
	v_cndmask_b32_e64 v143, v143, v107, s[8:9]
	v_cmp_eq_u32_e32 vcc, v113, v6
	v_cmp_eq_u32_e64 s[0:1], v121, v6
	v_cmp_eq_u32_e64 s[6:7], v129, v6
	v_cmp_eq_u32_e64 s[8:9], v137, v6
	v_cndmask_b32_e32 v119, v119, v108, vcc
	v_cndmask_b32_e64 v127, v127, v108, s[0:1]
	v_cndmask_b32_e64 v135, v135, v108, s[6:7]
	v_cndmask_b32_e64 v143, v143, v108, s[8:9]
	v_cmp_eq_u32_e32 vcc, v113, v7
	v_cmp_eq_u32_e64 s[0:1], v121, v7
	v_cmp_eq_u32_e64 s[6:7], v129, v7
	v_cmp_eq_u32_e64 s[8:9], v137, v7
	v_cndmask_b32_e32 v119, v119, v109, vcc
	v_cndmask_b32_e64 v127, v127, v109, s[0:1]
	v_cndmask_b32_e64 v135, v135, v109, s[6:7]
	v_cndmask_b32_e64 v143, v143, v109, s[8:9]
	v_cmp_eq_u32_e32 vcc, v113, v8
	v_cmp_eq_u32_e64 s[0:1], v121, v8
	v_cmp_eq_u32_e64 s[6:7], v129, v8
	v_cmp_eq_u32_e64 s[8:9], v137, v8
	v_cndmask_b32_e32 v119, v119, v110, vcc
	v_cndmask_b32_e64 v127, v127, v110, s[0:1]
	v_cndmask_b32_e64 v135, v135, v110, s[6:7]
	v_cndmask_b32_e64 v143, v143, v110, s[8:9]
	v_cmp_eq_u32_e32 vcc, v113, v9
	v_cmp_eq_u32_e64 s[0:1], v121, v9
	v_cmp_eq_u32_e64 s[6:7], v129, v9
	v_cmp_eq_u32_e64 s[8:9], v137, v9
	v_cndmask_b32_e32 v119, v119, v111, vcc
	v_cndmask_b32_e64 v127, v127, v111, s[0:1]
	v_cndmask_b32_e64 v135, v135, v111, s[6:7]
	v_cndmask_b32_e64 v143, v143, v111, s[8:9]
	v_add_u32_e32 v112, v112, v119
	v_add_u32_e32 v120, v120, v127
	v_add_u32_e32 v128, v128, v135
	v_add_u32_e32 v136, v136, v143
	v_cmp_ne_u32_e32 vcc, -1, v119
	s_and_saveexec_b64 s[24:25], vcc
	ds_write_b32 v112, v114
	s_mov_b64 exec, s[24:25]
	v_cmp_ne_u32_e32 vcc, -1, v127
	s_and_saveexec_b64 s[24:25], vcc
	ds_write_b32 v120, v122
	s_mov_b64 exec, s[24:25]
	v_cmp_ne_u32_e32 vcc, -1, v135
	s_and_saveexec_b64 s[24:25], vcc
	ds_write_b32 v128, v130
	s_mov_b64 exec, s[24:25]
	v_cmp_ne_u32_e32 vcc, -1, v143
	s_and_saveexec_b64 s[24:25], vcc
	ds_write_b32 v136, v138
	s_mov_b64 exec, s[24:25]
	v_and_b32_e32 v112, 0xff, v68
	v_and_b32_e32 v120, 0xff, v69
	v_and_b32_e32 v128, 0xff, v70
	v_and_b32_e32 v136, 0xff, v71
	v_lshlrev_b32_e32 v112, 2, v112
	v_lshlrev_b32_e32 v120, 2, v120
	v_lshlrev_b32_e32 v128, 2, v128
	v_lshlrev_b32_e32 v136, 2, v136
	v_add_u32_e32 v118, v112, v11
	v_add_u32_e32 v126, v120, v11
	v_add_u32_e32 v134, v128, v11
	v_add_u32_e32 v142, v136, v11
	ds_read_b32 v113, v112 offset:36864
	ds_read_b32 v114, v112 offset:35712
	ds_read_b32 v115, v118 offset:14336
	ds_read_b32 v121, v120 offset:36864
	ds_read_b32 v122, v120 offset:35712
	ds_read_b32 v123, v126 offset:14848
	ds_read_b32 v129, v128 offset:36864
	ds_read_b32 v130, v128 offset:35712
	ds_read_b32 v131, v134 offset:15360
	ds_read_b32 v137, v136 offset:36864
	ds_read_b32 v138, v136 offset:35712
	ds_read_b32 v139, v142 offset:15872
	v_add_u32_e32 v117, 112, v36
	v_add_u32_e32 v125, 116, v36
	v_add_u32_e32 v133, 120, v36
	v_add_u32_e32 v141, 124, v36
	v_mul_hi_u32 v118, v117, v16
	v_mul_hi_u32 v126, v125, v16
	v_mul_hi_u32 v134, v133, v16
	v_mul_hi_u32 v142, v141, v16
	v_mul_lo_u32 v118, v118, s11
	v_mul_lo_u32 v126, v126, s11
	v_mul_lo_u32 v134, v134, s11
	v_mul_lo_u32 v142, v142, s11
	v_sub_u32_e32 v117, v117, v118
	v_sub_u32_e32 v125, v125, v126
	v_sub_u32_e32 v133, v133, v134
	v_sub_u32_e32 v141, v141, v142
	v_subrev_u32_e32 v118, s11, v117
	v_subrev_u32_e32 v126, s11, v125
	v_subrev_u32_e32 v134, s11, v133
	v_subrev_u32_e32 v142, s11, v141
	v_cmp_le_u32_e32 vcc, s11, v117
	v_cmp_le_u32_e64 s[0:1], s11, v125
	v_cmp_le_u32_e64 s[6:7], s11, v133
	v_cmp_le_u32_e64 s[8:9], s11, v141
	v_cndmask_b32_e32 v117, v117, v118, vcc
	v_cndmask_b32_e64 v125, v125, v126, s[0:1]
	v_cndmask_b32_e64 v133, v133, v134, s[6:7]
	v_cndmask_b32_e64 v141, v141, v142, s[8:9]
	v_subrev_u32_e32 v118, s11, v117
	v_subrev_u32_e32 v126, s11, v125
	v_subrev_u32_e32 v134, s11, v133
	v_subrev_u32_e32 v142, s11, v141
	v_cmp_le_u32_e32 vcc, s11, v117
	v_cmp_le_u32_e64 s[0:1], s11, v125
	v_cmp_le_u32_e64 s[6:7], s11, v133
	v_cmp_le_u32_e64 s[8:9], s11, v141
	v_cndmask_b32_e32 v117, v117, v118, vcc
	v_cndmask_b32_e64 v125, v125, v126, s[0:1]
	v_cndmask_b32_e64 v133, v133, v134, s[6:7]
	v_cndmask_b32_e64 v141, v141, v142, s[8:9]
	v_ashrrev_i32_e32 v116, 8, v68
	v_ashrrev_i32_e32 v124, 8, v69
	v_ashrrev_i32_e32 v132, 8, v70
	v_ashrrev_i32_e32 v140, 8, v71
	s_waitcnt lgkmcnt(0)
	v_add_u32_e32 v116, v116, v113
	v_add_u32_e32 v124, v124, v121
	v_add_u32_e32 v132, v132, v129
	v_add_u32_e32 v140, v140, v137
	v_add3_u32 v116, v116, v114, v115
	v_add3_u32 v124, v124, v122, v123
	v_add3_u32 v132, v132, v130, v131
	v_add3_u32 v140, v140, v138, v139
	v_cmp_eq_u32_e32 vcc, s93, v117
	v_add_u32_e32 v1, 0xe000, v10
	s_and_saveexec_b64 s[24:25], vcc
	global_store_dword v1, v116, s[16:17]
	s_mov_b64 exec, s[24:25]
	v_cmp_eq_u32_e32 vcc, s93, v125
	v_add_u32_e32 v1, 0xe800, v10
	s_and_saveexec_b64 s[24:25], vcc
	global_store_dword v1, v124, s[16:17]
	s_mov_b64 exec, s[24:25]
	v_cmp_eq_u32_e32 vcc, s93, v133
	v_add_u32_e32 v1, 0xf000, v10
	s_and_saveexec_b64 s[24:25], vcc
	global_store_dword v1, v132, s[16:17]
	s_mov_b64 exec, s[24:25]
	v_cmp_eq_u32_e32 vcc, s93, v141
	v_add_u32_e32 v1, 0xf800, v10
	s_and_saveexec_b64 s[24:25], vcc
	global_store_dword v1, v140, s[16:17]
	s_mov_b64 exec, s[24:25]
	v_ashrrev_i32_e32 v113, 8, v116
	v_ashrrev_i32_e32 v121, 8, v124
	v_ashrrev_i32_e32 v129, 8, v132
	v_ashrrev_i32_e32 v137, 8, v140
	v_and_b32_e32 v112, 0xff, v116
	v_and_b32_e32 v120, 0xff, v124
	v_and_b32_e32 v128, 0xff, v132
	v_and_b32_e32 v136, 0xff, v140
	v_lshl_add_u32 v112, v112, 2, s10
	v_lshl_add_u32 v120, v120, 2, s10
	v_lshl_add_u32 v128, v128, 2, s10
	v_lshl_add_u32 v136, v136, 2, s10
	v_add_u32_e32 v114, 0x1c00, v34
	v_add_u32_e32 v122, 0x1d00, v34
	v_add_u32_e32 v130, 0x1e00, v34
	v_add_u32_e32 v138, 0x1f00, v34
	v_mov_b32_e32 v119, -1
	v_mov_b32_e32 v127, -1
	v_mov_b32_e32 v135, -1
	v_mov_b32_e32 v143, -1
	v_cmp_eq_u32_e32 vcc, v113, v2
	v_cmp_eq_u32_e64 s[0:1], v121, v2
	v_cmp_eq_u32_e64 s[6:7], v129, v2
	v_cmp_eq_u32_e64 s[8:9], v137, v2
	v_cndmask_b32_e32 v119, v119, v104, vcc
	v_cndmask_b32_e64 v127, v127, v104, s[0:1]
	v_cndmask_b32_e64 v135, v135, v104, s[6:7]
	v_cndmask_b32_e64 v143, v143, v104, s[8:9]
	v_cmp_eq_u32_e32 vcc, v113, v3
	v_cmp_eq_u32_e64 s[0:1], v121, v3
	v_cmp_eq_u32_e64 s[6:7], v129, v3
	v_cmp_eq_u32_e64 s[8:9], v137, v3
	v_cndmask_b32_e32 v119, v119, v105, vcc
	v_cndmask_b32_e64 v127, v127, v105, s[0:1]
	v_cndmask_b32_e64 v135, v135, v105, s[6:7]
	v_cndmask_b32_e64 v143, v143, v105, s[8:9]
	v_cmp_eq_u32_e32 vcc, v113, v4
	v_cmp_eq_u32_e64 s[0:1], v121, v4
	v_cmp_eq_u32_e64 s[6:7], v129, v4
	v_cmp_eq_u32_e64 s[8:9], v137, v4
	v_cndmask_b32_e32 v119, v119, v106, vcc
	v_cndmask_b32_e64 v127, v127, v106, s[0:1]
	v_cndmask_b32_e64 v135, v135, v106, s[6:7]
	v_cndmask_b32_e64 v143, v143, v106, s[8:9]
	v_cmp_eq_u32_e32 vcc, v113, v5
	v_cmp_eq_u32_e64 s[0:1], v121, v5
	v_cmp_eq_u32_e64 s[6:7], v129, v5
	v_cmp_eq_u32_e64 s[8:9], v137, v5
	v_cndmask_b32_e32 v119, v119, v107, vcc
	v_cndmask_b32_e64 v127, v127, v107, s[0:1]
	v_cndmask_b32_e64 v135, v135, v107, s[6:7]
	v_cndmask_b32_e64 v143, v143, v107, s[8:9]
	v_cmp_eq_u32_e32 vcc, v113, v6
	v_cmp_eq_u32_e64 s[0:1], v121, v6
	v_cmp_eq_u32_e64 s[6:7], v129, v6
	v_cmp_eq_u32_e64 s[8:9], v137, v6
	v_cndmask_b32_e32 v119, v119, v108, vcc
	v_cndmask_b32_e64 v127, v127, v108, s[0:1]
	v_cndmask_b32_e64 v135, v135, v108, s[6:7]
	v_cndmask_b32_e64 v143, v143, v108, s[8:9]
	v_cmp_eq_u32_e32 vcc, v113, v7
	v_cmp_eq_u32_e64 s[0:1], v121, v7
	v_cmp_eq_u32_e64 s[6:7], v129, v7
	v_cmp_eq_u32_e64 s[8:9], v137, v7
	v_cndmask_b32_e32 v119, v119, v109, vcc
	v_cndmask_b32_e64 v127, v127, v109, s[0:1]
	v_cndmask_b32_e64 v135, v135, v109, s[6:7]
	v_cndmask_b32_e64 v143, v143, v109, s[8:9]
	v_cmp_eq_u32_e32 vcc, v113, v8
	v_cmp_eq_u32_e64 s[0:1], v121, v8
	v_cmp_eq_u32_e64 s[6:7], v129, v8
	v_cmp_eq_u32_e64 s[8:9], v137, v8
	v_cndmask_b32_e32 v119, v119, v110, vcc
	v_cndmask_b32_e64 v127, v127, v110, s[0:1]
	v_cndmask_b32_e64 v135, v135, v110, s[6:7]
	v_cndmask_b32_e64 v143, v143, v110, s[8:9]
	v_cmp_eq_u32_e32 vcc, v113, v9
	v_cmp_eq_u32_e64 s[0:1], v121, v9
	v_cmp_eq_u32_e64 s[6:7], v129, v9
	v_cmp_eq_u32_e64 s[8:9], v137, v9
	v_cndmask_b32_e32 v119, v119, v111, vcc
	v_cndmask_b32_e64 v127, v127, v111, s[0:1]
	v_cndmask_b32_e64 v135, v135, v111, s[6:7]
	v_cndmask_b32_e64 v143, v143, v111, s[8:9]
	v_add_u32_e32 v112, v112, v119
	v_add_u32_e32 v120, v120, v127
	v_add_u32_e32 v128, v128, v135
	v_add_u32_e32 v136, v136, v143
	v_cmp_ne_u32_e32 vcc, -1, v119
	s_and_saveexec_b64 s[24:25], vcc
	ds_write_b32 v112, v114
	s_mov_b64 exec, s[24:25]
	v_cmp_ne_u32_e32 vcc, -1, v127
	s_and_saveexec_b64 s[24:25], vcc
	ds_write_b32 v120, v122
	s_mov_b64 exec, s[24:25]
	v_cmp_ne_u32_e32 vcc, -1, v135
	s_and_saveexec_b64 s[24:25], vcc
	ds_write_b32 v128, v130
	s_mov_b64 exec, s[24:25]
	v_cmp_ne_u32_e32 vcc, -1, v143
	s_and_saveexec_b64 s[24:25], vcc
	ds_write_b32 v136, v138
	s_mov_b64 exec, s[24:25]
	v_and_b32_e32 v112, 0xff, v72
	v_and_b32_e32 v120, 0xff, v73
	v_and_b32_e32 v128, 0xff, v74
	v_and_b32_e32 v136, 0xff, v75
	v_lshlrev_b32_e32 v112, 2, v112
	v_lshlrev_b32_e32 v120, 2, v120
	v_lshlrev_b32_e32 v128, 2, v128
	v_lshlrev_b32_e32 v136, 2, v136
	v_add_u32_e32 v118, v112, v11
	v_add_u32_e32 v126, v120, v11
	v_add_u32_e32 v134, v128, v11
	v_add_u32_e32 v142, v136, v11
	ds_read_b32 v113, v112 offset:36864
	ds_read_b32 v114, v112 offset:35840
	ds_read_b32 v115, v118 offset:16384
	ds_read_b32 v121, v120 offset:36864
	ds_read_b32 v122, v120 offset:35840
	ds_read_b32 v123, v126 offset:16896
	ds_read_b32 v129, v128 offset:36864
	ds_read_b32 v130, v128 offset:35840
	ds_read_b32 v131, v134 offset:17408
	ds_read_b32 v137, v136 offset:36864
	ds_read_b32 v138, v136 offset:35840
	ds_read_b32 v139, v142 offset:17920
	v_add_u32_e32 v117, 128, v36
	v_add_u32_e32 v125, 132, v36
	v_add_u32_e32 v133, 136, v36
	v_add_u32_e32 v141, 140, v36
	v_mul_hi_u32 v118, v117, v16
	v_mul_hi_u32 v126, v125, v16
	v_mul_hi_u32 v134, v133, v16
	v_mul_hi_u32 v142, v141, v16
	v_mul_lo_u32 v118, v118, s11
	v_mul_lo_u32 v126, v126, s11
	v_mul_lo_u32 v134, v134, s11
	v_mul_lo_u32 v142, v142, s11
	v_sub_u32_e32 v117, v117, v118
	v_sub_u32_e32 v125, v125, v126
	v_sub_u32_e32 v133, v133, v134
	v_sub_u32_e32 v141, v141, v142
	v_subrev_u32_e32 v118, s11, v117
	v_subrev_u32_e32 v126, s11, v125
	v_subrev_u32_e32 v134, s11, v133
	v_subrev_u32_e32 v142, s11, v141
	v_cmp_le_u32_e32 vcc, s11, v117
	v_cmp_le_u32_e64 s[0:1], s11, v125
	v_cmp_le_u32_e64 s[6:7], s11, v133
	v_cmp_le_u32_e64 s[8:9], s11, v141
	v_cndmask_b32_e32 v117, v117, v118, vcc
	v_cndmask_b32_e64 v125, v125, v126, s[0:1]
	v_cndmask_b32_e64 v133, v133, v134, s[6:7]
	v_cndmask_b32_e64 v141, v141, v142, s[8:9]
	v_subrev_u32_e32 v118, s11, v117
	v_subrev_u32_e32 v126, s11, v125
	v_subrev_u32_e32 v134, s11, v133
	v_subrev_u32_e32 v142, s11, v141
	v_cmp_le_u32_e32 vcc, s11, v117
	v_cmp_le_u32_e64 s[0:1], s11, v125
	v_cmp_le_u32_e64 s[6:7], s11, v133
	v_cmp_le_u32_e64 s[8:9], s11, v141
	v_cndmask_b32_e32 v117, v117, v118, vcc
	v_cndmask_b32_e64 v125, v125, v126, s[0:1]
	v_cndmask_b32_e64 v133, v133, v134, s[6:7]
	v_cndmask_b32_e64 v141, v141, v142, s[8:9]
	v_ashrrev_i32_e32 v116, 8, v72
	v_ashrrev_i32_e32 v124, 8, v73
	v_ashrrev_i32_e32 v132, 8, v74
	v_ashrrev_i32_e32 v140, 8, v75
	s_waitcnt lgkmcnt(0)
	v_add_u32_e32 v116, v116, v113
	v_add_u32_e32 v124, v124, v121
	v_add_u32_e32 v132, v132, v129
	v_add_u32_e32 v140, v140, v137
	v_add3_u32 v116, v116, v114, v115
	v_add3_u32 v124, v124, v122, v123
	v_add3_u32 v132, v132, v130, v131
	v_add3_u32 v140, v140, v138, v139
	v_cmp_eq_u32_e32 vcc, s93, v117
	v_add_u32_e32 v1, 0x10000, v10
	s_and_saveexec_b64 s[24:25], vcc
	global_store_dword v1, v116, s[16:17]
	s_mov_b64 exec, s[24:25]
	v_cmp_eq_u32_e32 vcc, s93, v125
	v_add_u32_e32 v1, 0x10800, v10
	s_and_saveexec_b64 s[24:25], vcc
	global_store_dword v1, v124, s[16:17]
	s_mov_b64 exec, s[24:25]
	v_cmp_eq_u32_e32 vcc, s93, v133
	v_add_u32_e32 v1, 0x11000, v10
	s_and_saveexec_b64 s[24:25], vcc
	global_store_dword v1, v132, s[16:17]
	s_mov_b64 exec, s[24:25]
	v_cmp_eq_u32_e32 vcc, s93, v141
	v_add_u32_e32 v1, 0x11800, v10
	s_and_saveexec_b64 s[24:25], vcc
	global_store_dword v1, v140, s[16:17]
	s_mov_b64 exec, s[24:25]
	v_ashrrev_i32_e32 v113, 8, v116
	v_ashrrev_i32_e32 v121, 8, v124
	v_ashrrev_i32_e32 v129, 8, v132
	v_ashrrev_i32_e32 v137, 8, v140
	v_and_b32_e32 v112, 0xff, v116
	v_and_b32_e32 v120, 0xff, v124
	v_and_b32_e32 v128, 0xff, v132
	v_and_b32_e32 v136, 0xff, v140
	v_lshl_add_u32 v112, v112, 2, s10
	v_lshl_add_u32 v120, v120, 2, s10
	v_lshl_add_u32 v128, v128, 2, s10
	v_lshl_add_u32 v136, v136, 2, s10
	v_add_u32_e32 v114, 0x2000, v34
	v_add_u32_e32 v122, 0x2100, v34
	v_add_u32_e32 v130, 0x2200, v34
	v_add_u32_e32 v138, 0x2300, v34
	v_mov_b32_e32 v119, -1
	v_mov_b32_e32 v127, -1
	v_mov_b32_e32 v135, -1
	v_mov_b32_e32 v143, -1
	v_cmp_eq_u32_e32 vcc, v113, v2
	v_cmp_eq_u32_e64 s[0:1], v121, v2
	v_cmp_eq_u32_e64 s[6:7], v129, v2
	v_cmp_eq_u32_e64 s[8:9], v137, v2
	v_cndmask_b32_e32 v119, v119, v104, vcc
	v_cndmask_b32_e64 v127, v127, v104, s[0:1]
	v_cndmask_b32_e64 v135, v135, v104, s[6:7]
	v_cndmask_b32_e64 v143, v143, v104, s[8:9]
	v_cmp_eq_u32_e32 vcc, v113, v3
	v_cmp_eq_u32_e64 s[0:1], v121, v3
	v_cmp_eq_u32_e64 s[6:7], v129, v3
	v_cmp_eq_u32_e64 s[8:9], v137, v3
	v_cndmask_b32_e32 v119, v119, v105, vcc
	v_cndmask_b32_e64 v127, v127, v105, s[0:1]
	v_cndmask_b32_e64 v135, v135, v105, s[6:7]
	v_cndmask_b32_e64 v143, v143, v105, s[8:9]
	v_cmp_eq_u32_e32 vcc, v113, v4
	v_cmp_eq_u32_e64 s[0:1], v121, v4
	v_cmp_eq_u32_e64 s[6:7], v129, v4
	v_cmp_eq_u32_e64 s[8:9], v137, v4
	v_cndmask_b32_e32 v119, v119, v106, vcc
	v_cndmask_b32_e64 v127, v127, v106, s[0:1]
	v_cndmask_b32_e64 v135, v135, v106, s[6:7]
	v_cndmask_b32_e64 v143, v143, v106, s[8:9]
	v_cmp_eq_u32_e32 vcc, v113, v5
	v_cmp_eq_u32_e64 s[0:1], v121, v5
	v_cmp_eq_u32_e64 s[6:7], v129, v5
	v_cmp_eq_u32_e64 s[8:9], v137, v5
	v_cndmask_b32_e32 v119, v119, v107, vcc
	v_cndmask_b32_e64 v127, v127, v107, s[0:1]
	v_cndmask_b32_e64 v135, v135, v107, s[6:7]
	v_cndmask_b32_e64 v143, v143, v107, s[8:9]
	v_cmp_eq_u32_e32 vcc, v113, v6
	v_cmp_eq_u32_e64 s[0:1], v121, v6
	v_cmp_eq_u32_e64 s[6:7], v129, v6
	v_cmp_eq_u32_e64 s[8:9], v137, v6
	v_cndmask_b32_e32 v119, v119, v108, vcc
	v_cndmask_b32_e64 v127, v127, v108, s[0:1]
	v_cndmask_b32_e64 v135, v135, v108, s[6:7]
	v_cndmask_b32_e64 v143, v143, v108, s[8:9]
	v_cmp_eq_u32_e32 vcc, v113, v7
	v_cmp_eq_u32_e64 s[0:1], v121, v7
	v_cmp_eq_u32_e64 s[6:7], v129, v7
	v_cmp_eq_u32_e64 s[8:9], v137, v7
	v_cndmask_b32_e32 v119, v119, v109, vcc
	v_cndmask_b32_e64 v127, v127, v109, s[0:1]
	v_cndmask_b32_e64 v135, v135, v109, s[6:7]
	v_cndmask_b32_e64 v143, v143, v109, s[8:9]
	v_cmp_eq_u32_e32 vcc, v113, v8
	v_cmp_eq_u32_e64 s[0:1], v121, v8
	v_cmp_eq_u32_e64 s[6:7], v129, v8
	v_cmp_eq_u32_e64 s[8:9], v137, v8
	v_cndmask_b32_e32 v119, v119, v110, vcc
	v_cndmask_b32_e64 v127, v127, v110, s[0:1]
	v_cndmask_b32_e64 v135, v135, v110, s[6:7]
	v_cndmask_b32_e64 v143, v143, v110, s[8:9]
	v_cmp_eq_u32_e32 vcc, v113, v9
	v_cmp_eq_u32_e64 s[0:1], v121, v9
	v_cmp_eq_u32_e64 s[6:7], v129, v9
	v_cmp_eq_u32_e64 s[8:9], v137, v9
	v_cndmask_b32_e32 v119, v119, v111, vcc
	v_cndmask_b32_e64 v127, v127, v111, s[0:1]
	v_cndmask_b32_e64 v135, v135, v111, s[6:7]
	v_cndmask_b32_e64 v143, v143, v111, s[8:9]
	v_add_u32_e32 v112, v112, v119
	v_add_u32_e32 v120, v120, v127
	v_add_u32_e32 v128, v128, v135
	v_add_u32_e32 v136, v136, v143
	v_cmp_ne_u32_e32 vcc, -1, v119
	s_and_saveexec_b64 s[24:25], vcc
	ds_write_b32 v112, v114
	s_mov_b64 exec, s[24:25]
	v_cmp_ne_u32_e32 vcc, -1, v127
	s_and_saveexec_b64 s[24:25], vcc
	ds_write_b32 v120, v122
	s_mov_b64 exec, s[24:25]
	v_cmp_ne_u32_e32 vcc, -1, v135
	s_and_saveexec_b64 s[24:25], vcc
	ds_write_b32 v128, v130
	s_mov_b64 exec, s[24:25]
	v_cmp_ne_u32_e32 vcc, -1, v143
	s_and_saveexec_b64 s[24:25], vcc
	ds_write_b32 v136, v138
	s_mov_b64 exec, s[24:25]
	v_and_b32_e32 v112, 0xff, v76
	v_and_b32_e32 v120, 0xff, v77
	v_and_b32_e32 v128, 0xff, v78
	v_and_b32_e32 v136, 0xff, v79
	v_lshlrev_b32_e32 v112, 2, v112
	v_lshlrev_b32_e32 v120, 2, v120
	v_lshlrev_b32_e32 v128, 2, v128
	v_lshlrev_b32_e32 v136, 2, v136
	v_add_u32_e32 v118, v112, v11
	v_add_u32_e32 v126, v120, v11
	v_add_u32_e32 v134, v128, v11
	v_add_u32_e32 v142, v136, v11
	ds_read_b32 v113, v112 offset:36864
	ds_read_b32 v114, v112 offset:35968
	ds_read_b32 v115, v118 offset:18432
	ds_read_b32 v121, v120 offset:36864
	ds_read_b32 v122, v120 offset:35968
	ds_read_b32 v123, v126 offset:18944
	ds_read_b32 v129, v128 offset:36864
	ds_read_b32 v130, v128 offset:35968
	ds_read_b32 v131, v134 offset:19456
	ds_read_b32 v137, v136 offset:36864
	ds_read_b32 v138, v136 offset:35968
	ds_read_b32 v139, v142 offset:19968
	v_add_u32_e32 v117, 144, v36
	v_add_u32_e32 v125, 148, v36
	v_add_u32_e32 v133, 152, v36
	v_add_u32_e32 v141, 156, v36
	v_mul_hi_u32 v118, v117, v16
	v_mul_hi_u32 v126, v125, v16
	v_mul_hi_u32 v134, v133, v16
	v_mul_hi_u32 v142, v141, v16
	v_mul_lo_u32 v118, v118, s11
	v_mul_lo_u32 v126, v126, s11
	v_mul_lo_u32 v134, v134, s11
	v_mul_lo_u32 v142, v142, s11
	v_sub_u32_e32 v117, v117, v118
	v_sub_u32_e32 v125, v125, v126
	v_sub_u32_e32 v133, v133, v134
	v_sub_u32_e32 v141, v141, v142
	v_subrev_u32_e32 v118, s11, v117
	v_subrev_u32_e32 v126, s11, v125
	v_subrev_u32_e32 v134, s11, v133
	v_subrev_u32_e32 v142, s11, v141
	v_cmp_le_u32_e32 vcc, s11, v117
	v_cmp_le_u32_e64 s[0:1], s11, v125
	v_cmp_le_u32_e64 s[6:7], s11, v133
	v_cmp_le_u32_e64 s[8:9], s11, v141
	v_cndmask_b32_e32 v117, v117, v118, vcc
	v_cndmask_b32_e64 v125, v125, v126, s[0:1]
	v_cndmask_b32_e64 v133, v133, v134, s[6:7]
	v_cndmask_b32_e64 v141, v141, v142, s[8:9]
	v_subrev_u32_e32 v118, s11, v117
	v_subrev_u32_e32 v126, s11, v125
	v_subrev_u32_e32 v134, s11, v133
	v_subrev_u32_e32 v142, s11, v141
	v_cmp_le_u32_e32 vcc, s11, v117
	v_cmp_le_u32_e64 s[0:1], s11, v125
	v_cmp_le_u32_e64 s[6:7], s11, v133
	v_cmp_le_u32_e64 s[8:9], s11, v141
	v_cndmask_b32_e32 v117, v117, v118, vcc
	v_cndmask_b32_e64 v125, v125, v126, s[0:1]
	v_cndmask_b32_e64 v133, v133, v134, s[6:7]
	v_cndmask_b32_e64 v141, v141, v142, s[8:9]
	v_ashrrev_i32_e32 v116, 8, v76
	v_ashrrev_i32_e32 v124, 8, v77
	v_ashrrev_i32_e32 v132, 8, v78
	v_ashrrev_i32_e32 v140, 8, v79
	s_waitcnt lgkmcnt(0)
	v_add_u32_e32 v116, v116, v113
	v_add_u32_e32 v124, v124, v121
	v_add_u32_e32 v132, v132, v129
	v_add_u32_e32 v140, v140, v137
	v_add3_u32 v116, v116, v114, v115
	v_add3_u32 v124, v124, v122, v123
	v_add3_u32 v132, v132, v130, v131
	v_add3_u32 v140, v140, v138, v139
	v_cmp_eq_u32_e32 vcc, s93, v117
	v_add_u32_e32 v1, 0x12000, v10
	s_and_saveexec_b64 s[24:25], vcc
	global_store_dword v1, v116, s[16:17]
	s_mov_b64 exec, s[24:25]
	v_cmp_eq_u32_e32 vcc, s93, v125
	v_add_u32_e32 v1, 0x12800, v10
	s_and_saveexec_b64 s[24:25], vcc
	global_store_dword v1, v124, s[16:17]
	s_mov_b64 exec, s[24:25]
	v_cmp_eq_u32_e32 vcc, s93, v133
	v_add_u32_e32 v1, 0x13000, v10
	s_and_saveexec_b64 s[24:25], vcc
	global_store_dword v1, v132, s[16:17]
	s_mov_b64 exec, s[24:25]
	v_cmp_eq_u32_e32 vcc, s93, v141
	v_add_u32_e32 v1, 0x13800, v10
	s_and_saveexec_b64 s[24:25], vcc
	global_store_dword v1, v140, s[16:17]
	s_mov_b64 exec, s[24:25]
	v_ashrrev_i32_e32 v113, 8, v116
	v_ashrrev_i32_e32 v121, 8, v124
	v_ashrrev_i32_e32 v129, 8, v132
	v_ashrrev_i32_e32 v137, 8, v140
	v_and_b32_e32 v112, 0xff, v116
	v_and_b32_e32 v120, 0xff, v124
	v_and_b32_e32 v128, 0xff, v132
	v_and_b32_e32 v136, 0xff, v140
	v_lshl_add_u32 v112, v112, 2, s10
	v_lshl_add_u32 v120, v120, 2, s10
	v_lshl_add_u32 v128, v128, 2, s10
	v_lshl_add_u32 v136, v136, 2, s10
	v_add_u32_e32 v114, 0x2400, v34
	v_add_u32_e32 v122, 0x2500, v34
	v_add_u32_e32 v130, 0x2600, v34
	v_add_u32_e32 v138, 0x2700, v34
	v_mov_b32_e32 v119, -1
	v_mov_b32_e32 v127, -1
	v_mov_b32_e32 v135, -1
	v_mov_b32_e32 v143, -1
	v_cmp_eq_u32_e32 vcc, v113, v2
	v_cmp_eq_u32_e64 s[0:1], v121, v2
	v_cmp_eq_u32_e64 s[6:7], v129, v2
	v_cmp_eq_u32_e64 s[8:9], v137, v2
	v_cndmask_b32_e32 v119, v119, v104, vcc
	v_cndmask_b32_e64 v127, v127, v104, s[0:1]
	v_cndmask_b32_e64 v135, v135, v104, s[6:7]
	v_cndmask_b32_e64 v143, v143, v104, s[8:9]
	v_cmp_eq_u32_e32 vcc, v113, v3
	v_cmp_eq_u32_e64 s[0:1], v121, v3
	v_cmp_eq_u32_e64 s[6:7], v129, v3
	v_cmp_eq_u32_e64 s[8:9], v137, v3
	v_cndmask_b32_e32 v119, v119, v105, vcc
	v_cndmask_b32_e64 v127, v127, v105, s[0:1]
	v_cndmask_b32_e64 v135, v135, v105, s[6:7]
	v_cndmask_b32_e64 v143, v143, v105, s[8:9]
	v_cmp_eq_u32_e32 vcc, v113, v4
	v_cmp_eq_u32_e64 s[0:1], v121, v4
	v_cmp_eq_u32_e64 s[6:7], v129, v4
	v_cmp_eq_u32_e64 s[8:9], v137, v4
	v_cndmask_b32_e32 v119, v119, v106, vcc
	v_cndmask_b32_e64 v127, v127, v106, s[0:1]
	v_cndmask_b32_e64 v135, v135, v106, s[6:7]
	v_cndmask_b32_e64 v143, v143, v106, s[8:9]
	v_cmp_eq_u32_e32 vcc, v113, v5
	v_cmp_eq_u32_e64 s[0:1], v121, v5
	v_cmp_eq_u32_e64 s[6:7], v129, v5
	v_cmp_eq_u32_e64 s[8:9], v137, v5
	v_cndmask_b32_e32 v119, v119, v107, vcc
	v_cndmask_b32_e64 v127, v127, v107, s[0:1]
	v_cndmask_b32_e64 v135, v135, v107, s[6:7]
	v_cndmask_b32_e64 v143, v143, v107, s[8:9]
	v_cmp_eq_u32_e32 vcc, v113, v6
	v_cmp_eq_u32_e64 s[0:1], v121, v6
	v_cmp_eq_u32_e64 s[6:7], v129, v6
	v_cmp_eq_u32_e64 s[8:9], v137, v6
	v_cndmask_b32_e32 v119, v119, v108, vcc
	v_cndmask_b32_e64 v127, v127, v108, s[0:1]
	v_cndmask_b32_e64 v135, v135, v108, s[6:7]
	v_cndmask_b32_e64 v143, v143, v108, s[8:9]
	v_cmp_eq_u32_e32 vcc, v113, v7
	v_cmp_eq_u32_e64 s[0:1], v121, v7
	v_cmp_eq_u32_e64 s[6:7], v129, v7
	v_cmp_eq_u32_e64 s[8:9], v137, v7
	v_cndmask_b32_e32 v119, v119, v109, vcc
	v_cndmask_b32_e64 v127, v127, v109, s[0:1]
	v_cndmask_b32_e64 v135, v135, v109, s[6:7]
	v_cndmask_b32_e64 v143, v143, v109, s[8:9]
	v_cmp_eq_u32_e32 vcc, v113, v8
	v_cmp_eq_u32_e64 s[0:1], v121, v8
	v_cmp_eq_u32_e64 s[6:7], v129, v8
	v_cmp_eq_u32_e64 s[8:9], v137, v8
	v_cndmask_b32_e32 v119, v119, v110, vcc
	v_cndmask_b32_e64 v127, v127, v110, s[0:1]
	v_cndmask_b32_e64 v135, v135, v110, s[6:7]
	v_cndmask_b32_e64 v143, v143, v110, s[8:9]
	v_cmp_eq_u32_e32 vcc, v113, v9
	v_cmp_eq_u32_e64 s[0:1], v121, v9
	v_cmp_eq_u32_e64 s[6:7], v129, v9
	v_cmp_eq_u32_e64 s[8:9], v137, v9
	v_cndmask_b32_e32 v119, v119, v111, vcc
	v_cndmask_b32_e64 v127, v127, v111, s[0:1]
	v_cndmask_b32_e64 v135, v135, v111, s[6:7]
	v_cndmask_b32_e64 v143, v143, v111, s[8:9]
	v_add_u32_e32 v112, v112, v119
	v_add_u32_e32 v120, v120, v127
	v_add_u32_e32 v128, v128, v135
	v_add_u32_e32 v136, v136, v143
	v_cmp_ne_u32_e32 vcc, -1, v119
	s_and_saveexec_b64 s[24:25], vcc
	ds_write_b32 v112, v114
	s_mov_b64 exec, s[24:25]
	v_cmp_ne_u32_e32 vcc, -1, v127
	s_and_saveexec_b64 s[24:25], vcc
	ds_write_b32 v120, v122
	s_mov_b64 exec, s[24:25]
	v_cmp_ne_u32_e32 vcc, -1, v135
	s_and_saveexec_b64 s[24:25], vcc
	ds_write_b32 v128, v130
	s_mov_b64 exec, s[24:25]
	v_cmp_ne_u32_e32 vcc, -1, v143
	s_and_saveexec_b64 s[24:25], vcc
	ds_write_b32 v136, v138
	s_mov_b64 exec, s[24:25]
	v_and_b32_e32 v112, 0xff, v80
	v_and_b32_e32 v120, 0xff, v81
	v_and_b32_e32 v128, 0xff, v82
	v_and_b32_e32 v136, 0xff, v83
	v_lshlrev_b32_e32 v112, 2, v112
	v_lshlrev_b32_e32 v120, 2, v120
	v_lshlrev_b32_e32 v128, 2, v128
	v_lshlrev_b32_e32 v136, 2, v136
	v_add_u32_e32 v118, v112, v11
	v_add_u32_e32 v126, v120, v11
	v_add_u32_e32 v134, v128, v11
	v_add_u32_e32 v142, v136, v11
	ds_read_b32 v113, v112 offset:36864
	ds_read_b32 v114, v112 offset:36096
	ds_read_b32 v115, v118 offset:20480
	ds_read_b32 v121, v120 offset:36864
	ds_read_b32 v122, v120 offset:36096
	ds_read_b32 v123, v126 offset:20992
	ds_read_b32 v129, v128 offset:36864
	ds_read_b32 v130, v128 offset:36096
	ds_read_b32 v131, v134 offset:21504
	ds_read_b32 v137, v136 offset:36864
	ds_read_b32 v138, v136 offset:36096
	ds_read_b32 v139, v142 offset:22016
	v_add_u32_e32 v117, 160, v36
	v_add_u32_e32 v125, 164, v36
	v_add_u32_e32 v133, 168, v36
	v_add_u32_e32 v141, 172, v36
	v_mul_hi_u32 v118, v117, v16
	v_mul_hi_u32 v126, v125, v16
	v_mul_hi_u32 v134, v133, v16
	v_mul_hi_u32 v142, v141, v16
	v_mul_lo_u32 v118, v118, s11
	v_mul_lo_u32 v126, v126, s11
	v_mul_lo_u32 v134, v134, s11
	v_mul_lo_u32 v142, v142, s11
	v_sub_u32_e32 v117, v117, v118
	v_sub_u32_e32 v125, v125, v126
	v_sub_u32_e32 v133, v133, v134
	v_sub_u32_e32 v141, v141, v142
	v_subrev_u32_e32 v118, s11, v117
	v_subrev_u32_e32 v126, s11, v125
	v_subrev_u32_e32 v134, s11, v133
	v_subrev_u32_e32 v142, s11, v141
	v_cmp_le_u32_e32 vcc, s11, v117
	v_cmp_le_u32_e64 s[0:1], s11, v125
	v_cmp_le_u32_e64 s[6:7], s11, v133
	v_cmp_le_u32_e64 s[8:9], s11, v141
	v_cndmask_b32_e32 v117, v117, v118, vcc
	v_cndmask_b32_e64 v125, v125, v126, s[0:1]
	v_cndmask_b32_e64 v133, v133, v134, s[6:7]
	v_cndmask_b32_e64 v141, v141, v142, s[8:9]
	v_subrev_u32_e32 v118, s11, v117
	v_subrev_u32_e32 v126, s11, v125
	v_subrev_u32_e32 v134, s11, v133
	v_subrev_u32_e32 v142, s11, v141
	v_cmp_le_u32_e32 vcc, s11, v117
	v_cmp_le_u32_e64 s[0:1], s11, v125
	v_cmp_le_u32_e64 s[6:7], s11, v133
	v_cmp_le_u32_e64 s[8:9], s11, v141
	v_cndmask_b32_e32 v117, v117, v118, vcc
	v_cndmask_b32_e64 v125, v125, v126, s[0:1]
	v_cndmask_b32_e64 v133, v133, v134, s[6:7]
	v_cndmask_b32_e64 v141, v141, v142, s[8:9]
	v_ashrrev_i32_e32 v116, 8, v80
	v_ashrrev_i32_e32 v124, 8, v81
	v_ashrrev_i32_e32 v132, 8, v82
	v_ashrrev_i32_e32 v140, 8, v83
	s_waitcnt lgkmcnt(0)
	v_add_u32_e32 v116, v116, v113
	v_add_u32_e32 v124, v124, v121
	v_add_u32_e32 v132, v132, v129
	v_add_u32_e32 v140, v140, v137
	v_add3_u32 v116, v116, v114, v115
	v_add3_u32 v124, v124, v122, v123
	v_add3_u32 v132, v132, v130, v131
	v_add3_u32 v140, v140, v138, v139
	v_cmp_eq_u32_e32 vcc, s93, v117
	v_add_u32_e32 v1, 0x14000, v10
	s_and_saveexec_b64 s[24:25], vcc
	global_store_dword v1, v116, s[16:17]
	s_mov_b64 exec, s[24:25]
	v_cmp_eq_u32_e32 vcc, s93, v125
	v_add_u32_e32 v1, 0x14800, v10
	s_and_saveexec_b64 s[24:25], vcc
	global_store_dword v1, v124, s[16:17]
	s_mov_b64 exec, s[24:25]
	v_cmp_eq_u32_e32 vcc, s93, v133
	v_add_u32_e32 v1, 0x15000, v10
	s_and_saveexec_b64 s[24:25], vcc
	global_store_dword v1, v132, s[16:17]
	s_mov_b64 exec, s[24:25]
	v_cmp_eq_u32_e32 vcc, s93, v141
	v_add_u32_e32 v1, 0x15800, v10
	s_and_saveexec_b64 s[24:25], vcc
	global_store_dword v1, v140, s[16:17]
	s_mov_b64 exec, s[24:25]
	v_ashrrev_i32_e32 v113, 8, v116
	v_ashrrev_i32_e32 v121, 8, v124
	v_ashrrev_i32_e32 v129, 8, v132
	v_ashrrev_i32_e32 v137, 8, v140
	v_and_b32_e32 v112, 0xff, v116
	v_and_b32_e32 v120, 0xff, v124
	v_and_b32_e32 v128, 0xff, v132
	v_and_b32_e32 v136, 0xff, v140
	v_lshl_add_u32 v112, v112, 2, s10
	v_lshl_add_u32 v120, v120, 2, s10
	v_lshl_add_u32 v128, v128, 2, s10
	v_lshl_add_u32 v136, v136, 2, s10
	v_add_u32_e32 v114, 0x2800, v34
	v_add_u32_e32 v122, 0x2900, v34
	v_add_u32_e32 v130, 0x2a00, v34
	v_add_u32_e32 v138, 0x2b00, v34
	v_mov_b32_e32 v119, -1
	v_mov_b32_e32 v127, -1
	v_mov_b32_e32 v135, -1
	v_mov_b32_e32 v143, -1
	v_cmp_eq_u32_e32 vcc, v113, v2
	v_cmp_eq_u32_e64 s[0:1], v121, v2
	v_cmp_eq_u32_e64 s[6:7], v129, v2
	v_cmp_eq_u32_e64 s[8:9], v137, v2
	v_cndmask_b32_e32 v119, v119, v104, vcc
	v_cndmask_b32_e64 v127, v127, v104, s[0:1]
	v_cndmask_b32_e64 v135, v135, v104, s[6:7]
	v_cndmask_b32_e64 v143, v143, v104, s[8:9]
	v_cmp_eq_u32_e32 vcc, v113, v3
	v_cmp_eq_u32_e64 s[0:1], v121, v3
	v_cmp_eq_u32_e64 s[6:7], v129, v3
	v_cmp_eq_u32_e64 s[8:9], v137, v3
	v_cndmask_b32_e32 v119, v119, v105, vcc
	v_cndmask_b32_e64 v127, v127, v105, s[0:1]
	v_cndmask_b32_e64 v135, v135, v105, s[6:7]
	v_cndmask_b32_e64 v143, v143, v105, s[8:9]
	v_cmp_eq_u32_e32 vcc, v113, v4
	v_cmp_eq_u32_e64 s[0:1], v121, v4
	v_cmp_eq_u32_e64 s[6:7], v129, v4
	v_cmp_eq_u32_e64 s[8:9], v137, v4
	v_cndmask_b32_e32 v119, v119, v106, vcc
	v_cndmask_b32_e64 v127, v127, v106, s[0:1]
	v_cndmask_b32_e64 v135, v135, v106, s[6:7]
	v_cndmask_b32_e64 v143, v143, v106, s[8:9]
	v_cmp_eq_u32_e32 vcc, v113, v5
	v_cmp_eq_u32_e64 s[0:1], v121, v5
	v_cmp_eq_u32_e64 s[6:7], v129, v5
	v_cmp_eq_u32_e64 s[8:9], v137, v5
	v_cndmask_b32_e32 v119, v119, v107, vcc
	v_cndmask_b32_e64 v127, v127, v107, s[0:1]
	v_cndmask_b32_e64 v135, v135, v107, s[6:7]
	v_cndmask_b32_e64 v143, v143, v107, s[8:9]
	v_cmp_eq_u32_e32 vcc, v113, v6
	v_cmp_eq_u32_e64 s[0:1], v121, v6
	v_cmp_eq_u32_e64 s[6:7], v129, v6
	v_cmp_eq_u32_e64 s[8:9], v137, v6
	v_cndmask_b32_e32 v119, v119, v108, vcc
	v_cndmask_b32_e64 v127, v127, v108, s[0:1]
	v_cndmask_b32_e64 v135, v135, v108, s[6:7]
	v_cndmask_b32_e64 v143, v143, v108, s[8:9]
	v_cmp_eq_u32_e32 vcc, v113, v7
	v_cmp_eq_u32_e64 s[0:1], v121, v7
	v_cmp_eq_u32_e64 s[6:7], v129, v7
	v_cmp_eq_u32_e64 s[8:9], v137, v7
	v_cndmask_b32_e32 v119, v119, v109, vcc
	v_cndmask_b32_e64 v127, v127, v109, s[0:1]
	v_cndmask_b32_e64 v135, v135, v109, s[6:7]
	v_cndmask_b32_e64 v143, v143, v109, s[8:9]
	v_cmp_eq_u32_e32 vcc, v113, v8
	v_cmp_eq_u32_e64 s[0:1], v121, v8
	v_cmp_eq_u32_e64 s[6:7], v129, v8
	v_cmp_eq_u32_e64 s[8:9], v137, v8
	v_cndmask_b32_e32 v119, v119, v110, vcc
	v_cndmask_b32_e64 v127, v127, v110, s[0:1]
	v_cndmask_b32_e64 v135, v135, v110, s[6:7]
	v_cndmask_b32_e64 v143, v143, v110, s[8:9]
	v_cmp_eq_u32_e32 vcc, v113, v9
	v_cmp_eq_u32_e64 s[0:1], v121, v9
	v_cmp_eq_u32_e64 s[6:7], v129, v9
	v_cmp_eq_u32_e64 s[8:9], v137, v9
	v_cndmask_b32_e32 v119, v119, v111, vcc
	v_cndmask_b32_e64 v127, v127, v111, s[0:1]
	v_cndmask_b32_e64 v135, v135, v111, s[6:7]
	v_cndmask_b32_e64 v143, v143, v111, s[8:9]
	v_add_u32_e32 v112, v112, v119
	v_add_u32_e32 v120, v120, v127
	v_add_u32_e32 v128, v128, v135
	v_add_u32_e32 v136, v136, v143
	v_cmp_ne_u32_e32 vcc, -1, v119
	s_and_saveexec_b64 s[24:25], vcc
	ds_write_b32 v112, v114
	s_mov_b64 exec, s[24:25]
	v_cmp_ne_u32_e32 vcc, -1, v127
	s_and_saveexec_b64 s[24:25], vcc
	ds_write_b32 v120, v122
	s_mov_b64 exec, s[24:25]
	v_cmp_ne_u32_e32 vcc, -1, v135
	s_and_saveexec_b64 s[24:25], vcc
	ds_write_b32 v128, v130
	s_mov_b64 exec, s[24:25]
	v_cmp_ne_u32_e32 vcc, -1, v143
	s_and_saveexec_b64 s[24:25], vcc
	ds_write_b32 v136, v138
	s_mov_b64 exec, s[24:25]
	v_and_b32_e32 v112, 0xff, v84
	v_and_b32_e32 v120, 0xff, v85
	v_and_b32_e32 v128, 0xff, v86
	v_and_b32_e32 v136, 0xff, v87
	v_lshlrev_b32_e32 v112, 2, v112
	v_lshlrev_b32_e32 v120, 2, v120
	v_lshlrev_b32_e32 v128, 2, v128
	v_lshlrev_b32_e32 v136, 2, v136
	v_add_u32_e32 v118, v112, v11
	v_add_u32_e32 v126, v120, v11
	v_add_u32_e32 v134, v128, v11
	v_add_u32_e32 v142, v136, v11
	ds_read_b32 v113, v112 offset:36864
	ds_read_b32 v114, v112 offset:36224
	ds_read_b32 v115, v118 offset:22528
	ds_read_b32 v121, v120 offset:36864
	ds_read_b32 v122, v120 offset:36224
	ds_read_b32 v123, v126 offset:23040
	ds_read_b32 v129, v128 offset:36864
	ds_read_b32 v130, v128 offset:36224
	ds_read_b32 v131, v134 offset:23552
	ds_read_b32 v137, v136 offset:36864
	ds_read_b32 v138, v136 offset:36224
	ds_read_b32 v139, v142 offset:24064
	v_add_u32_e32 v117, 176, v36
	v_add_u32_e32 v125, 180, v36
	v_add_u32_e32 v133, 184, v36
	v_add_u32_e32 v141, 188, v36
	v_mul_hi_u32 v118, v117, v16
	v_mul_hi_u32 v126, v125, v16
	v_mul_hi_u32 v134, v133, v16
	v_mul_hi_u32 v142, v141, v16
	v_mul_lo_u32 v118, v118, s11
	v_mul_lo_u32 v126, v126, s11
	v_mul_lo_u32 v134, v134, s11
	v_mul_lo_u32 v142, v142, s11
	v_sub_u32_e32 v117, v117, v118
	v_sub_u32_e32 v125, v125, v126
	v_sub_u32_e32 v133, v133, v134
	v_sub_u32_e32 v141, v141, v142
	v_subrev_u32_e32 v118, s11, v117
	v_subrev_u32_e32 v126, s11, v125
	v_subrev_u32_e32 v134, s11, v133
	v_subrev_u32_e32 v142, s11, v141
	v_cmp_le_u32_e32 vcc, s11, v117
	v_cmp_le_u32_e64 s[0:1], s11, v125
	v_cmp_le_u32_e64 s[6:7], s11, v133
	v_cmp_le_u32_e64 s[8:9], s11, v141
	v_cndmask_b32_e32 v117, v117, v118, vcc
	v_cndmask_b32_e64 v125, v125, v126, s[0:1]
	v_cndmask_b32_e64 v133, v133, v134, s[6:7]
	v_cndmask_b32_e64 v141, v141, v142, s[8:9]
	v_subrev_u32_e32 v118, s11, v117
	v_subrev_u32_e32 v126, s11, v125
	v_subrev_u32_e32 v134, s11, v133
	v_subrev_u32_e32 v142, s11, v141
	v_cmp_le_u32_e32 vcc, s11, v117
	v_cmp_le_u32_e64 s[0:1], s11, v125
	v_cmp_le_u32_e64 s[6:7], s11, v133
	v_cmp_le_u32_e64 s[8:9], s11, v141
	v_cndmask_b32_e32 v117, v117, v118, vcc
	v_cndmask_b32_e64 v125, v125, v126, s[0:1]
	v_cndmask_b32_e64 v133, v133, v134, s[6:7]
	v_cndmask_b32_e64 v141, v141, v142, s[8:9]
	v_ashrrev_i32_e32 v116, 8, v84
	v_ashrrev_i32_e32 v124, 8, v85
	v_ashrrev_i32_e32 v132, 8, v86
	v_ashrrev_i32_e32 v140, 8, v87
	s_waitcnt lgkmcnt(0)
	v_add_u32_e32 v116, v116, v113
	v_add_u32_e32 v124, v124, v121
	v_add_u32_e32 v132, v132, v129
	v_add_u32_e32 v140, v140, v137
	v_add3_u32 v116, v116, v114, v115
	v_add3_u32 v124, v124, v122, v123
	v_add3_u32 v132, v132, v130, v131
	v_add3_u32 v140, v140, v138, v139
	v_cmp_eq_u32_e32 vcc, s93, v117
	v_add_u32_e32 v1, 0x16000, v10
	s_and_saveexec_b64 s[24:25], vcc
	global_store_dword v1, v116, s[16:17]
	s_mov_b64 exec, s[24:25]
	v_cmp_eq_u32_e32 vcc, s93, v125
	v_add_u32_e32 v1, 0x16800, v10
	s_and_saveexec_b64 s[24:25], vcc
	global_store_dword v1, v124, s[16:17]
	s_mov_b64 exec, s[24:25]
	v_cmp_eq_u32_e32 vcc, s93, v133
	v_add_u32_e32 v1, 0x17000, v10
	s_and_saveexec_b64 s[24:25], vcc
	global_store_dword v1, v132, s[16:17]
	s_mov_b64 exec, s[24:25]
	v_cmp_eq_u32_e32 vcc, s93, v141
	v_add_u32_e32 v1, 0x17800, v10
	s_and_saveexec_b64 s[24:25], vcc
	global_store_dword v1, v140, s[16:17]
	s_mov_b64 exec, s[24:25]
	v_ashrrev_i32_e32 v113, 8, v116
	v_ashrrev_i32_e32 v121, 8, v124
	v_ashrrev_i32_e32 v129, 8, v132
	v_ashrrev_i32_e32 v137, 8, v140
	v_and_b32_e32 v112, 0xff, v116
	v_and_b32_e32 v120, 0xff, v124
	v_and_b32_e32 v128, 0xff, v132
	v_and_b32_e32 v136, 0xff, v140
	v_lshl_add_u32 v112, v112, 2, s10
	v_lshl_add_u32 v120, v120, 2, s10
	v_lshl_add_u32 v128, v128, 2, s10
	v_lshl_add_u32 v136, v136, 2, s10
	v_add_u32_e32 v114, 0x2c00, v34
	v_add_u32_e32 v122, 0x2d00, v34
	v_add_u32_e32 v130, 0x2e00, v34
	v_add_u32_e32 v138, 0x2f00, v34
	v_mov_b32_e32 v119, -1
	v_mov_b32_e32 v127, -1
	v_mov_b32_e32 v135, -1
	v_mov_b32_e32 v143, -1
	v_cmp_eq_u32_e32 vcc, v113, v2
	v_cmp_eq_u32_e64 s[0:1], v121, v2
	v_cmp_eq_u32_e64 s[6:7], v129, v2
	v_cmp_eq_u32_e64 s[8:9], v137, v2
	v_cndmask_b32_e32 v119, v119, v104, vcc
	v_cndmask_b32_e64 v127, v127, v104, s[0:1]
	v_cndmask_b32_e64 v135, v135, v104, s[6:7]
	v_cndmask_b32_e64 v143, v143, v104, s[8:9]
	v_cmp_eq_u32_e32 vcc, v113, v3
	v_cmp_eq_u32_e64 s[0:1], v121, v3
	v_cmp_eq_u32_e64 s[6:7], v129, v3
	v_cmp_eq_u32_e64 s[8:9], v137, v3
	v_cndmask_b32_e32 v119, v119, v105, vcc
	v_cndmask_b32_e64 v127, v127, v105, s[0:1]
	v_cndmask_b32_e64 v135, v135, v105, s[6:7]
	v_cndmask_b32_e64 v143, v143, v105, s[8:9]
	v_cmp_eq_u32_e32 vcc, v113, v4
	v_cmp_eq_u32_e64 s[0:1], v121, v4
	v_cmp_eq_u32_e64 s[6:7], v129, v4
	v_cmp_eq_u32_e64 s[8:9], v137, v4
	v_cndmask_b32_e32 v119, v119, v106, vcc
	v_cndmask_b32_e64 v127, v127, v106, s[0:1]
	v_cndmask_b32_e64 v135, v135, v106, s[6:7]
	v_cndmask_b32_e64 v143, v143, v106, s[8:9]
	v_cmp_eq_u32_e32 vcc, v113, v5
	v_cmp_eq_u32_e64 s[0:1], v121, v5
	v_cmp_eq_u32_e64 s[6:7], v129, v5
	v_cmp_eq_u32_e64 s[8:9], v137, v5
	v_cndmask_b32_e32 v119, v119, v107, vcc
	v_cndmask_b32_e64 v127, v127, v107, s[0:1]
	v_cndmask_b32_e64 v135, v135, v107, s[6:7]
	v_cndmask_b32_e64 v143, v143, v107, s[8:9]
	v_cmp_eq_u32_e32 vcc, v113, v6
	v_cmp_eq_u32_e64 s[0:1], v121, v6
	v_cmp_eq_u32_e64 s[6:7], v129, v6
	v_cmp_eq_u32_e64 s[8:9], v137, v6
	v_cndmask_b32_e32 v119, v119, v108, vcc
	v_cndmask_b32_e64 v127, v127, v108, s[0:1]
	v_cndmask_b32_e64 v135, v135, v108, s[6:7]
	v_cndmask_b32_e64 v143, v143, v108, s[8:9]
	v_cmp_eq_u32_e32 vcc, v113, v7
	v_cmp_eq_u32_e64 s[0:1], v121, v7
	v_cmp_eq_u32_e64 s[6:7], v129, v7
	v_cmp_eq_u32_e64 s[8:9], v137, v7
	v_cndmask_b32_e32 v119, v119, v109, vcc
	v_cndmask_b32_e64 v127, v127, v109, s[0:1]
	v_cndmask_b32_e64 v135, v135, v109, s[6:7]
	v_cndmask_b32_e64 v143, v143, v109, s[8:9]
	v_cmp_eq_u32_e32 vcc, v113, v8
	v_cmp_eq_u32_e64 s[0:1], v121, v8
	v_cmp_eq_u32_e64 s[6:7], v129, v8
	v_cmp_eq_u32_e64 s[8:9], v137, v8
	v_cndmask_b32_e32 v119, v119, v110, vcc
	v_cndmask_b32_e64 v127, v127, v110, s[0:1]
	v_cndmask_b32_e64 v135, v135, v110, s[6:7]
	v_cndmask_b32_e64 v143, v143, v110, s[8:9]
	v_cmp_eq_u32_e32 vcc, v113, v9
	v_cmp_eq_u32_e64 s[0:1], v121, v9
	v_cmp_eq_u32_e64 s[6:7], v129, v9
	v_cmp_eq_u32_e64 s[8:9], v137, v9
	v_cndmask_b32_e32 v119, v119, v111, vcc
	v_cndmask_b32_e64 v127, v127, v111, s[0:1]
	v_cndmask_b32_e64 v135, v135, v111, s[6:7]
	v_cndmask_b32_e64 v143, v143, v111, s[8:9]
	v_add_u32_e32 v112, v112, v119
	v_add_u32_e32 v120, v120, v127
	v_add_u32_e32 v128, v128, v135
	v_add_u32_e32 v136, v136, v143
	v_cmp_ne_u32_e32 vcc, -1, v119
	s_and_saveexec_b64 s[24:25], vcc
	ds_write_b32 v112, v114
	s_mov_b64 exec, s[24:25]
	v_cmp_ne_u32_e32 vcc, -1, v127
	s_and_saveexec_b64 s[24:25], vcc
	ds_write_b32 v120, v122
	s_mov_b64 exec, s[24:25]
	v_cmp_ne_u32_e32 vcc, -1, v135
	s_and_saveexec_b64 s[24:25], vcc
	ds_write_b32 v128, v130
	s_mov_b64 exec, s[24:25]
	v_cmp_ne_u32_e32 vcc, -1, v143
	s_and_saveexec_b64 s[24:25], vcc
	ds_write_b32 v136, v138
	s_mov_b64 exec, s[24:25]
	v_and_b32_e32 v112, 0xff, v88
	v_and_b32_e32 v120, 0xff, v89
	v_and_b32_e32 v128, 0xff, v90
	v_and_b32_e32 v136, 0xff, v91
	v_lshlrev_b32_e32 v112, 2, v112
	v_lshlrev_b32_e32 v120, 2, v120
	v_lshlrev_b32_e32 v128, 2, v128
	v_lshlrev_b32_e32 v136, 2, v136
	v_add_u32_e32 v118, v112, v11
	v_add_u32_e32 v126, v120, v11
	v_add_u32_e32 v134, v128, v11
	v_add_u32_e32 v142, v136, v11
	ds_read_b32 v113, v112 offset:36864
	ds_read_b32 v114, v112 offset:36352
	ds_read_b32 v115, v118 offset:24576
	ds_read_b32 v121, v120 offset:36864
	ds_read_b32 v122, v120 offset:36352
	ds_read_b32 v123, v126 offset:25088
	ds_read_b32 v129, v128 offset:36864
	ds_read_b32 v130, v128 offset:36352
	ds_read_b32 v131, v134 offset:25600
	ds_read_b32 v137, v136 offset:36864
	ds_read_b32 v138, v136 offset:36352
	ds_read_b32 v139, v142 offset:26112
	v_add_u32_e32 v117, 192, v36
	v_add_u32_e32 v125, 196, v36
	v_add_u32_e32 v133, 200, v36
	v_add_u32_e32 v141, 204, v36
	v_mul_hi_u32 v118, v117, v16
	v_mul_hi_u32 v126, v125, v16
	v_mul_hi_u32 v134, v133, v16
	v_mul_hi_u32 v142, v141, v16
	v_mul_lo_u32 v118, v118, s11
	v_mul_lo_u32 v126, v126, s11
	v_mul_lo_u32 v134, v134, s11
	v_mul_lo_u32 v142, v142, s11
	v_sub_u32_e32 v117, v117, v118
	v_sub_u32_e32 v125, v125, v126
	v_sub_u32_e32 v133, v133, v134
	v_sub_u32_e32 v141, v141, v142
	v_subrev_u32_e32 v118, s11, v117
	v_subrev_u32_e32 v126, s11, v125
	v_subrev_u32_e32 v134, s11, v133
	v_subrev_u32_e32 v142, s11, v141
	v_cmp_le_u32_e32 vcc, s11, v117
	v_cmp_le_u32_e64 s[0:1], s11, v125
	v_cmp_le_u32_e64 s[6:7], s11, v133
	v_cmp_le_u32_e64 s[8:9], s11, v141
	v_cndmask_b32_e32 v117, v117, v118, vcc
	v_cndmask_b32_e64 v125, v125, v126, s[0:1]
	v_cndmask_b32_e64 v133, v133, v134, s[6:7]
	v_cndmask_b32_e64 v141, v141, v142, s[8:9]
	v_subrev_u32_e32 v118, s11, v117
	v_subrev_u32_e32 v126, s11, v125
	v_subrev_u32_e32 v134, s11, v133
	v_subrev_u32_e32 v142, s11, v141
	v_cmp_le_u32_e32 vcc, s11, v117
	v_cmp_le_u32_e64 s[0:1], s11, v125
	v_cmp_le_u32_e64 s[6:7], s11, v133
	v_cmp_le_u32_e64 s[8:9], s11, v141
	v_cndmask_b32_e32 v117, v117, v118, vcc
	v_cndmask_b32_e64 v125, v125, v126, s[0:1]
	v_cndmask_b32_e64 v133, v133, v134, s[6:7]
	v_cndmask_b32_e64 v141, v141, v142, s[8:9]
	v_ashrrev_i32_e32 v116, 8, v88
	v_ashrrev_i32_e32 v124, 8, v89
	v_ashrrev_i32_e32 v132, 8, v90
	v_ashrrev_i32_e32 v140, 8, v91
	s_waitcnt lgkmcnt(0)
	v_add_u32_e32 v116, v116, v113
	v_add_u32_e32 v124, v124, v121
	v_add_u32_e32 v132, v132, v129
	v_add_u32_e32 v140, v140, v137
	v_add3_u32 v116, v116, v114, v115
	v_add3_u32 v124, v124, v122, v123
	v_add3_u32 v132, v132, v130, v131
	v_add3_u32 v140, v140, v138, v139
	v_cmp_eq_u32_e32 vcc, s93, v117
	v_add_u32_e32 v1, 0x18000, v10
	s_and_saveexec_b64 s[24:25], vcc
	global_store_dword v1, v116, s[16:17]
	s_mov_b64 exec, s[24:25]
	v_cmp_eq_u32_e32 vcc, s93, v125
	v_add_u32_e32 v1, 0x18800, v10
	s_and_saveexec_b64 s[24:25], vcc
	global_store_dword v1, v124, s[16:17]
	s_mov_b64 exec, s[24:25]
	v_cmp_eq_u32_e32 vcc, s93, v133
	v_add_u32_e32 v1, 0x19000, v10
	s_and_saveexec_b64 s[24:25], vcc
	global_store_dword v1, v132, s[16:17]
	s_mov_b64 exec, s[24:25]
	v_cmp_eq_u32_e32 vcc, s93, v141
	v_add_u32_e32 v1, 0x19800, v10
	s_and_saveexec_b64 s[24:25], vcc
	global_store_dword v1, v140, s[16:17]
	s_mov_b64 exec, s[24:25]
	v_ashrrev_i32_e32 v113, 8, v116
	v_ashrrev_i32_e32 v121, 8, v124
	v_ashrrev_i32_e32 v129, 8, v132
	v_ashrrev_i32_e32 v137, 8, v140
	v_and_b32_e32 v112, 0xff, v116
	v_and_b32_e32 v120, 0xff, v124
	v_and_b32_e32 v128, 0xff, v132
	v_and_b32_e32 v136, 0xff, v140
	v_lshl_add_u32 v112, v112, 2, s10
	v_lshl_add_u32 v120, v120, 2, s10
	v_lshl_add_u32 v128, v128, 2, s10
	v_lshl_add_u32 v136, v136, 2, s10
	v_add_u32_e32 v114, 0x3000, v34
	v_add_u32_e32 v122, 0x3100, v34
	v_add_u32_e32 v130, 0x3200, v34
	v_add_u32_e32 v138, 0x3300, v34
	v_mov_b32_e32 v119, -1
	v_mov_b32_e32 v127, -1
	v_mov_b32_e32 v135, -1
	v_mov_b32_e32 v143, -1
	v_cmp_eq_u32_e32 vcc, v113, v2
	v_cmp_eq_u32_e64 s[0:1], v121, v2
	v_cmp_eq_u32_e64 s[6:7], v129, v2
	v_cmp_eq_u32_e64 s[8:9], v137, v2
	v_cndmask_b32_e32 v119, v119, v104, vcc
	v_cndmask_b32_e64 v127, v127, v104, s[0:1]
	v_cndmask_b32_e64 v135, v135, v104, s[6:7]
	v_cndmask_b32_e64 v143, v143, v104, s[8:9]
	v_cmp_eq_u32_e32 vcc, v113, v3
	v_cmp_eq_u32_e64 s[0:1], v121, v3
	v_cmp_eq_u32_e64 s[6:7], v129, v3
	v_cmp_eq_u32_e64 s[8:9], v137, v3
	v_cndmask_b32_e32 v119, v119, v105, vcc
	v_cndmask_b32_e64 v127, v127, v105, s[0:1]
	v_cndmask_b32_e64 v135, v135, v105, s[6:7]
	v_cndmask_b32_e64 v143, v143, v105, s[8:9]
	v_cmp_eq_u32_e32 vcc, v113, v4
	v_cmp_eq_u32_e64 s[0:1], v121, v4
	v_cmp_eq_u32_e64 s[6:7], v129, v4
	v_cmp_eq_u32_e64 s[8:9], v137, v4
	v_cndmask_b32_e32 v119, v119, v106, vcc
	v_cndmask_b32_e64 v127, v127, v106, s[0:1]
	v_cndmask_b32_e64 v135, v135, v106, s[6:7]
	v_cndmask_b32_e64 v143, v143, v106, s[8:9]
	v_cmp_eq_u32_e32 vcc, v113, v5
	v_cmp_eq_u32_e64 s[0:1], v121, v5
	v_cmp_eq_u32_e64 s[6:7], v129, v5
	v_cmp_eq_u32_e64 s[8:9], v137, v5
	v_cndmask_b32_e32 v119, v119, v107, vcc
	v_cndmask_b32_e64 v127, v127, v107, s[0:1]
	v_cndmask_b32_e64 v135, v135, v107, s[6:7]
	v_cndmask_b32_e64 v143, v143, v107, s[8:9]
	v_cmp_eq_u32_e32 vcc, v113, v6
	v_cmp_eq_u32_e64 s[0:1], v121, v6
	v_cmp_eq_u32_e64 s[6:7], v129, v6
	v_cmp_eq_u32_e64 s[8:9], v137, v6
	v_cndmask_b32_e32 v119, v119, v108, vcc
	v_cndmask_b32_e64 v127, v127, v108, s[0:1]
	v_cndmask_b32_e64 v135, v135, v108, s[6:7]
	v_cndmask_b32_e64 v143, v143, v108, s[8:9]
	v_cmp_eq_u32_e32 vcc, v113, v7
	v_cmp_eq_u32_e64 s[0:1], v121, v7
	v_cmp_eq_u32_e64 s[6:7], v129, v7
	v_cmp_eq_u32_e64 s[8:9], v137, v7
	v_cndmask_b32_e32 v119, v119, v109, vcc
	v_cndmask_b32_e64 v127, v127, v109, s[0:1]
	v_cndmask_b32_e64 v135, v135, v109, s[6:7]
	v_cndmask_b32_e64 v143, v143, v109, s[8:9]
	v_cmp_eq_u32_e32 vcc, v113, v8
	v_cmp_eq_u32_e64 s[0:1], v121, v8
	v_cmp_eq_u32_e64 s[6:7], v129, v8
	v_cmp_eq_u32_e64 s[8:9], v137, v8
	v_cndmask_b32_e32 v119, v119, v110, vcc
	v_cndmask_b32_e64 v127, v127, v110, s[0:1]
	v_cndmask_b32_e64 v135, v135, v110, s[6:7]
	v_cndmask_b32_e64 v143, v143, v110, s[8:9]
	v_cmp_eq_u32_e32 vcc, v113, v9
	v_cmp_eq_u32_e64 s[0:1], v121, v9
	v_cmp_eq_u32_e64 s[6:7], v129, v9
	v_cmp_eq_u32_e64 s[8:9], v137, v9
	v_cndmask_b32_e32 v119, v119, v111, vcc
	v_cndmask_b32_e64 v127, v127, v111, s[0:1]
	v_cndmask_b32_e64 v135, v135, v111, s[6:7]
	v_cndmask_b32_e64 v143, v143, v111, s[8:9]
	v_add_u32_e32 v112, v112, v119
	v_add_u32_e32 v120, v120, v127
	v_add_u32_e32 v128, v128, v135
	v_add_u32_e32 v136, v136, v143
	v_cmp_ne_u32_e32 vcc, -1, v119
	s_and_saveexec_b64 s[24:25], vcc
	ds_write_b32 v112, v114
	s_mov_b64 exec, s[24:25]
	v_cmp_ne_u32_e32 vcc, -1, v127
	s_and_saveexec_b64 s[24:25], vcc
	ds_write_b32 v120, v122
	s_mov_b64 exec, s[24:25]
	v_cmp_ne_u32_e32 vcc, -1, v135
	s_and_saveexec_b64 s[24:25], vcc
	ds_write_b32 v128, v130
	s_mov_b64 exec, s[24:25]
	v_cmp_ne_u32_e32 vcc, -1, v143
	s_and_saveexec_b64 s[24:25], vcc
	ds_write_b32 v136, v138
	s_mov_b64 exec, s[24:25]
	v_and_b32_e32 v112, 0xff, v92
	v_and_b32_e32 v120, 0xff, v93
	v_and_b32_e32 v128, 0xff, v94
	v_and_b32_e32 v136, 0xff, v95
	v_lshlrev_b32_e32 v112, 2, v112
	v_lshlrev_b32_e32 v120, 2, v120
	v_lshlrev_b32_e32 v128, 2, v128
	v_lshlrev_b32_e32 v136, 2, v136
	v_add_u32_e32 v118, v112, v11
	v_add_u32_e32 v126, v120, v11
	v_add_u32_e32 v134, v128, v11
	v_add_u32_e32 v142, v136, v11
	ds_read_b32 v113, v112 offset:36864
	ds_read_b32 v114, v112 offset:36480
	ds_read_b32 v115, v118 offset:26624
	ds_read_b32 v121, v120 offset:36864
	ds_read_b32 v122, v120 offset:36480
	ds_read_b32 v123, v126 offset:27136
	ds_read_b32 v129, v128 offset:36864
	ds_read_b32 v130, v128 offset:36480
	ds_read_b32 v131, v134 offset:27648
	ds_read_b32 v137, v136 offset:36864
	ds_read_b32 v138, v136 offset:36480
	ds_read_b32 v139, v142 offset:28160
	v_add_u32_e32 v117, 208, v36
	v_add_u32_e32 v125, 212, v36
	v_add_u32_e32 v133, 216, v36
	v_add_u32_e32 v141, 220, v36
	v_mul_hi_u32 v118, v117, v16
	v_mul_hi_u32 v126, v125, v16
	v_mul_hi_u32 v134, v133, v16
	v_mul_hi_u32 v142, v141, v16
	v_mul_lo_u32 v118, v118, s11
	v_mul_lo_u32 v126, v126, s11
	v_mul_lo_u32 v134, v134, s11
	v_mul_lo_u32 v142, v142, s11
	v_sub_u32_e32 v117, v117, v118
	v_sub_u32_e32 v125, v125, v126
	v_sub_u32_e32 v133, v133, v134
	v_sub_u32_e32 v141, v141, v142
	v_subrev_u32_e32 v118, s11, v117
	v_subrev_u32_e32 v126, s11, v125
	v_subrev_u32_e32 v134, s11, v133
	v_subrev_u32_e32 v142, s11, v141
	v_cmp_le_u32_e32 vcc, s11, v117
	v_cmp_le_u32_e64 s[0:1], s11, v125
	v_cmp_le_u32_e64 s[6:7], s11, v133
	v_cmp_le_u32_e64 s[8:9], s11, v141
	v_cndmask_b32_e32 v117, v117, v118, vcc
	v_cndmask_b32_e64 v125, v125, v126, s[0:1]
	v_cndmask_b32_e64 v133, v133, v134, s[6:7]
	v_cndmask_b32_e64 v141, v141, v142, s[8:9]
	v_subrev_u32_e32 v118, s11, v117
	v_subrev_u32_e32 v126, s11, v125
	v_subrev_u32_e32 v134, s11, v133
	v_subrev_u32_e32 v142, s11, v141
	v_cmp_le_u32_e32 vcc, s11, v117
	v_cmp_le_u32_e64 s[0:1], s11, v125
	v_cmp_le_u32_e64 s[6:7], s11, v133
	v_cmp_le_u32_e64 s[8:9], s11, v141
	v_cndmask_b32_e32 v117, v117, v118, vcc
	v_cndmask_b32_e64 v125, v125, v126, s[0:1]
	v_cndmask_b32_e64 v133, v133, v134, s[6:7]
	v_cndmask_b32_e64 v141, v141, v142, s[8:9]
	v_ashrrev_i32_e32 v116, 8, v92
	v_ashrrev_i32_e32 v124, 8, v93
	v_ashrrev_i32_e32 v132, 8, v94
	v_ashrrev_i32_e32 v140, 8, v95
	s_waitcnt lgkmcnt(0)
	v_add_u32_e32 v116, v116, v113
	v_add_u32_e32 v124, v124, v121
	v_add_u32_e32 v132, v132, v129
	v_add_u32_e32 v140, v140, v137
	v_add3_u32 v116, v116, v114, v115
	v_add3_u32 v124, v124, v122, v123
	v_add3_u32 v132, v132, v130, v131
	v_add3_u32 v140, v140, v138, v139
	v_cmp_eq_u32_e32 vcc, s93, v117
	v_add_u32_e32 v1, 0x1a000, v10
	s_and_saveexec_b64 s[24:25], vcc
	global_store_dword v1, v116, s[16:17]
	s_mov_b64 exec, s[24:25]
	v_cmp_eq_u32_e32 vcc, s93, v125
	v_add_u32_e32 v1, 0x1a800, v10
	s_and_saveexec_b64 s[24:25], vcc
	global_store_dword v1, v124, s[16:17]
	s_mov_b64 exec, s[24:25]
	v_cmp_eq_u32_e32 vcc, s93, v133
	v_add_u32_e32 v1, 0x1b000, v10
	s_and_saveexec_b64 s[24:25], vcc
	global_store_dword v1, v132, s[16:17]
	s_mov_b64 exec, s[24:25]
	v_cmp_eq_u32_e32 vcc, s93, v141
	v_add_u32_e32 v1, 0x1b800, v10
	s_and_saveexec_b64 s[24:25], vcc
	global_store_dword v1, v140, s[16:17]
	s_mov_b64 exec, s[24:25]
	v_ashrrev_i32_e32 v113, 8, v116
	v_ashrrev_i32_e32 v121, 8, v124
	v_ashrrev_i32_e32 v129, 8, v132
	v_ashrrev_i32_e32 v137, 8, v140
	v_and_b32_e32 v112, 0xff, v116
	v_and_b32_e32 v120, 0xff, v124
	v_and_b32_e32 v128, 0xff, v132
	v_and_b32_e32 v136, 0xff, v140
	v_lshl_add_u32 v112, v112, 2, s10
	v_lshl_add_u32 v120, v120, 2, s10
	v_lshl_add_u32 v128, v128, 2, s10
	v_lshl_add_u32 v136, v136, 2, s10
	v_add_u32_e32 v114, 0x3400, v34
	v_add_u32_e32 v122, 0x3500, v34
	v_add_u32_e32 v130, 0x3600, v34
	v_add_u32_e32 v138, 0x3700, v34
	v_mov_b32_e32 v119, -1
	v_mov_b32_e32 v127, -1
	v_mov_b32_e32 v135, -1
	v_mov_b32_e32 v143, -1
	v_cmp_eq_u32_e32 vcc, v113, v2
	v_cmp_eq_u32_e64 s[0:1], v121, v2
	v_cmp_eq_u32_e64 s[6:7], v129, v2
	v_cmp_eq_u32_e64 s[8:9], v137, v2
	v_cndmask_b32_e32 v119, v119, v104, vcc
	v_cndmask_b32_e64 v127, v127, v104, s[0:1]
	v_cndmask_b32_e64 v135, v135, v104, s[6:7]
	v_cndmask_b32_e64 v143, v143, v104, s[8:9]
	v_cmp_eq_u32_e32 vcc, v113, v3
	v_cmp_eq_u32_e64 s[0:1], v121, v3
	v_cmp_eq_u32_e64 s[6:7], v129, v3
	v_cmp_eq_u32_e64 s[8:9], v137, v3
	v_cndmask_b32_e32 v119, v119, v105, vcc
	v_cndmask_b32_e64 v127, v127, v105, s[0:1]
	v_cndmask_b32_e64 v135, v135, v105, s[6:7]
	v_cndmask_b32_e64 v143, v143, v105, s[8:9]
	v_cmp_eq_u32_e32 vcc, v113, v4
	v_cmp_eq_u32_e64 s[0:1], v121, v4
	v_cmp_eq_u32_e64 s[6:7], v129, v4
	v_cmp_eq_u32_e64 s[8:9], v137, v4
	v_cndmask_b32_e32 v119, v119, v106, vcc
	v_cndmask_b32_e64 v127, v127, v106, s[0:1]
	v_cndmask_b32_e64 v135, v135, v106, s[6:7]
	v_cndmask_b32_e64 v143, v143, v106, s[8:9]
	v_cmp_eq_u32_e32 vcc, v113, v5
	v_cmp_eq_u32_e64 s[0:1], v121, v5
	v_cmp_eq_u32_e64 s[6:7], v129, v5
	v_cmp_eq_u32_e64 s[8:9], v137, v5
	v_cndmask_b32_e32 v119, v119, v107, vcc
	v_cndmask_b32_e64 v127, v127, v107, s[0:1]
	v_cndmask_b32_e64 v135, v135, v107, s[6:7]
	v_cndmask_b32_e64 v143, v143, v107, s[8:9]
	v_cmp_eq_u32_e32 vcc, v113, v6
	v_cmp_eq_u32_e64 s[0:1], v121, v6
	v_cmp_eq_u32_e64 s[6:7], v129, v6
	v_cmp_eq_u32_e64 s[8:9], v137, v6
	v_cndmask_b32_e32 v119, v119, v108, vcc
	v_cndmask_b32_e64 v127, v127, v108, s[0:1]
	v_cndmask_b32_e64 v135, v135, v108, s[6:7]
	v_cndmask_b32_e64 v143, v143, v108, s[8:9]
	v_cmp_eq_u32_e32 vcc, v113, v7
	v_cmp_eq_u32_e64 s[0:1], v121, v7
	v_cmp_eq_u32_e64 s[6:7], v129, v7
	v_cmp_eq_u32_e64 s[8:9], v137, v7
	v_cndmask_b32_e32 v119, v119, v109, vcc
	v_cndmask_b32_e64 v127, v127, v109, s[0:1]
	v_cndmask_b32_e64 v135, v135, v109, s[6:7]
	v_cndmask_b32_e64 v143, v143, v109, s[8:9]
	v_cmp_eq_u32_e32 vcc, v113, v8
	v_cmp_eq_u32_e64 s[0:1], v121, v8
	v_cmp_eq_u32_e64 s[6:7], v129, v8
	v_cmp_eq_u32_e64 s[8:9], v137, v8
	v_cndmask_b32_e32 v119, v119, v110, vcc
	v_cndmask_b32_e64 v127, v127, v110, s[0:1]
	v_cndmask_b32_e64 v135, v135, v110, s[6:7]
	v_cndmask_b32_e64 v143, v143, v110, s[8:9]
	v_cmp_eq_u32_e32 vcc, v113, v9
	v_cmp_eq_u32_e64 s[0:1], v121, v9
	v_cmp_eq_u32_e64 s[6:7], v129, v9
	v_cmp_eq_u32_e64 s[8:9], v137, v9
	v_cndmask_b32_e32 v119, v119, v111, vcc
	v_cndmask_b32_e64 v127, v127, v111, s[0:1]
	v_cndmask_b32_e64 v135, v135, v111, s[6:7]
	v_cndmask_b32_e64 v143, v143, v111, s[8:9]
	v_add_u32_e32 v112, v112, v119
	v_add_u32_e32 v120, v120, v127
	v_add_u32_e32 v128, v128, v135
	v_add_u32_e32 v136, v136, v143
	v_cmp_ne_u32_e32 vcc, -1, v119
	s_and_saveexec_b64 s[24:25], vcc
	ds_write_b32 v112, v114
	s_mov_b64 exec, s[24:25]
	v_cmp_ne_u32_e32 vcc, -1, v127
	s_and_saveexec_b64 s[24:25], vcc
	ds_write_b32 v120, v122
	s_mov_b64 exec, s[24:25]
	v_cmp_ne_u32_e32 vcc, -1, v135
	s_and_saveexec_b64 s[24:25], vcc
	ds_write_b32 v128, v130
	s_mov_b64 exec, s[24:25]
	v_cmp_ne_u32_e32 vcc, -1, v143
	s_and_saveexec_b64 s[24:25], vcc
	ds_write_b32 v136, v138
	s_mov_b64 exec, s[24:25]
	v_and_b32_e32 v112, 0xff, v96
	v_and_b32_e32 v120, 0xff, v97
	v_and_b32_e32 v128, 0xff, v98
	v_and_b32_e32 v136, 0xff, v99
	v_lshlrev_b32_e32 v112, 2, v112
	v_lshlrev_b32_e32 v120, 2, v120
	v_lshlrev_b32_e32 v128, 2, v128
	v_lshlrev_b32_e32 v136, 2, v136
	v_add_u32_e32 v118, v112, v11
	v_add_u32_e32 v126, v120, v11
	v_add_u32_e32 v134, v128, v11
	v_add_u32_e32 v142, v136, v11
	ds_read_b32 v113, v112 offset:36864
	ds_read_b32 v114, v112 offset:36608
	ds_read_b32 v115, v118 offset:28672
	ds_read_b32 v121, v120 offset:36864
	ds_read_b32 v122, v120 offset:36608
	ds_read_b32 v123, v126 offset:29184
	ds_read_b32 v129, v128 offset:36864
	ds_read_b32 v130, v128 offset:36608
	ds_read_b32 v131, v134 offset:29696
	ds_read_b32 v137, v136 offset:36864
	ds_read_b32 v138, v136 offset:36608
	ds_read_b32 v139, v142 offset:30208
	v_add_u32_e32 v117, 224, v36
	v_add_u32_e32 v125, 228, v36
	v_add_u32_e32 v133, 232, v36
	v_add_u32_e32 v141, 236, v36
	v_mul_hi_u32 v118, v117, v16
	v_mul_hi_u32 v126, v125, v16
	v_mul_hi_u32 v134, v133, v16
	v_mul_hi_u32 v142, v141, v16
	v_mul_lo_u32 v118, v118, s11
	v_mul_lo_u32 v126, v126, s11
	v_mul_lo_u32 v134, v134, s11
	v_mul_lo_u32 v142, v142, s11
	v_sub_u32_e32 v117, v117, v118
	v_sub_u32_e32 v125, v125, v126
	v_sub_u32_e32 v133, v133, v134
	v_sub_u32_e32 v141, v141, v142
	v_subrev_u32_e32 v118, s11, v117
	v_subrev_u32_e32 v126, s11, v125
	v_subrev_u32_e32 v134, s11, v133
	v_subrev_u32_e32 v142, s11, v141
	v_cmp_le_u32_e32 vcc, s11, v117
	v_cmp_le_u32_e64 s[0:1], s11, v125
	v_cmp_le_u32_e64 s[6:7], s11, v133
	v_cmp_le_u32_e64 s[8:9], s11, v141
	v_cndmask_b32_e32 v117, v117, v118, vcc
	v_cndmask_b32_e64 v125, v125, v126, s[0:1]
	v_cndmask_b32_e64 v133, v133, v134, s[6:7]
	v_cndmask_b32_e64 v141, v141, v142, s[8:9]
	v_subrev_u32_e32 v118, s11, v117
	v_subrev_u32_e32 v126, s11, v125
	v_subrev_u32_e32 v134, s11, v133
	v_subrev_u32_e32 v142, s11, v141
	v_cmp_le_u32_e32 vcc, s11, v117
	v_cmp_le_u32_e64 s[0:1], s11, v125
	v_cmp_le_u32_e64 s[6:7], s11, v133
	v_cmp_le_u32_e64 s[8:9], s11, v141
	v_cndmask_b32_e32 v117, v117, v118, vcc
	v_cndmask_b32_e64 v125, v125, v126, s[0:1]
	v_cndmask_b32_e64 v133, v133, v134, s[6:7]
	v_cndmask_b32_e64 v141, v141, v142, s[8:9]
	v_ashrrev_i32_e32 v116, 8, v96
	v_ashrrev_i32_e32 v124, 8, v97
	v_ashrrev_i32_e32 v132, 8, v98
	v_ashrrev_i32_e32 v140, 8, v99
	s_waitcnt lgkmcnt(0)
	v_add_u32_e32 v116, v116, v113
	v_add_u32_e32 v124, v124, v121
	v_add_u32_e32 v132, v132, v129
	v_add_u32_e32 v140, v140, v137
	v_add3_u32 v116, v116, v114, v115
	v_add3_u32 v124, v124, v122, v123
	v_add3_u32 v132, v132, v130, v131
	v_add3_u32 v140, v140, v138, v139
	v_cmp_eq_u32_e32 vcc, s93, v117
	v_add_u32_e32 v1, 0x1c000, v10
	s_and_saveexec_b64 s[24:25], vcc
	global_store_dword v1, v116, s[16:17]
	s_mov_b64 exec, s[24:25]
	v_cmp_eq_u32_e32 vcc, s93, v125
	v_add_u32_e32 v1, 0x1c800, v10
	s_and_saveexec_b64 s[24:25], vcc
	global_store_dword v1, v124, s[16:17]
	s_mov_b64 exec, s[24:25]
	v_cmp_eq_u32_e32 vcc, s93, v133
	v_add_u32_e32 v1, 0x1d000, v10
	s_and_saveexec_b64 s[24:25], vcc
	global_store_dword v1, v132, s[16:17]
	s_mov_b64 exec, s[24:25]
	v_cmp_eq_u32_e32 vcc, s93, v141
	v_add_u32_e32 v1, 0x1d800, v10
	s_and_saveexec_b64 s[24:25], vcc
	global_store_dword v1, v140, s[16:17]
	s_mov_b64 exec, s[24:25]
	v_ashrrev_i32_e32 v113, 8, v116
	v_ashrrev_i32_e32 v121, 8, v124
	v_ashrrev_i32_e32 v129, 8, v132
	v_ashrrev_i32_e32 v137, 8, v140
	v_and_b32_e32 v112, 0xff, v116
	v_and_b32_e32 v120, 0xff, v124
	v_and_b32_e32 v128, 0xff, v132
	v_and_b32_e32 v136, 0xff, v140
	v_lshl_add_u32 v112, v112, 2, s10
	v_lshl_add_u32 v120, v120, 2, s10
	v_lshl_add_u32 v128, v128, 2, s10
	v_lshl_add_u32 v136, v136, 2, s10
	v_add_u32_e32 v114, 0x3800, v34
	v_add_u32_e32 v122, 0x3900, v34
	v_add_u32_e32 v130, 0x3a00, v34
	v_add_u32_e32 v138, 0x3b00, v34
	v_mov_b32_e32 v119, -1
	v_mov_b32_e32 v127, -1
	v_mov_b32_e32 v135, -1
	v_mov_b32_e32 v143, -1
	v_cmp_eq_u32_e32 vcc, v113, v2
	v_cmp_eq_u32_e64 s[0:1], v121, v2
	v_cmp_eq_u32_e64 s[6:7], v129, v2
	v_cmp_eq_u32_e64 s[8:9], v137, v2
	v_cndmask_b32_e32 v119, v119, v104, vcc
	v_cndmask_b32_e64 v127, v127, v104, s[0:1]
	v_cndmask_b32_e64 v135, v135, v104, s[6:7]
	v_cndmask_b32_e64 v143, v143, v104, s[8:9]
	v_cmp_eq_u32_e32 vcc, v113, v3
	v_cmp_eq_u32_e64 s[0:1], v121, v3
	v_cmp_eq_u32_e64 s[6:7], v129, v3
	v_cmp_eq_u32_e64 s[8:9], v137, v3
	v_cndmask_b32_e32 v119, v119, v105, vcc
	v_cndmask_b32_e64 v127, v127, v105, s[0:1]
	v_cndmask_b32_e64 v135, v135, v105, s[6:7]
	v_cndmask_b32_e64 v143, v143, v105, s[8:9]
	v_cmp_eq_u32_e32 vcc, v113, v4
	v_cmp_eq_u32_e64 s[0:1], v121, v4
	v_cmp_eq_u32_e64 s[6:7], v129, v4
	v_cmp_eq_u32_e64 s[8:9], v137, v4
	v_cndmask_b32_e32 v119, v119, v106, vcc
	v_cndmask_b32_e64 v127, v127, v106, s[0:1]
	v_cndmask_b32_e64 v135, v135, v106, s[6:7]
	v_cndmask_b32_e64 v143, v143, v106, s[8:9]
	v_cmp_eq_u32_e32 vcc, v113, v5
	v_cmp_eq_u32_e64 s[0:1], v121, v5
	v_cmp_eq_u32_e64 s[6:7], v129, v5
	v_cmp_eq_u32_e64 s[8:9], v137, v5
	v_cndmask_b32_e32 v119, v119, v107, vcc
	v_cndmask_b32_e64 v127, v127, v107, s[0:1]
	v_cndmask_b32_e64 v135, v135, v107, s[6:7]
	v_cndmask_b32_e64 v143, v143, v107, s[8:9]
	v_cmp_eq_u32_e32 vcc, v113, v6
	v_cmp_eq_u32_e64 s[0:1], v121, v6
	v_cmp_eq_u32_e64 s[6:7], v129, v6
	v_cmp_eq_u32_e64 s[8:9], v137, v6
	v_cndmask_b32_e32 v119, v119, v108, vcc
	v_cndmask_b32_e64 v127, v127, v108, s[0:1]
	v_cndmask_b32_e64 v135, v135, v108, s[6:7]
	v_cndmask_b32_e64 v143, v143, v108, s[8:9]
	v_cmp_eq_u32_e32 vcc, v113, v7
	v_cmp_eq_u32_e64 s[0:1], v121, v7
	v_cmp_eq_u32_e64 s[6:7], v129, v7
	v_cmp_eq_u32_e64 s[8:9], v137, v7
	v_cndmask_b32_e32 v119, v119, v109, vcc
	v_cndmask_b32_e64 v127, v127, v109, s[0:1]
	v_cndmask_b32_e64 v135, v135, v109, s[6:7]
	v_cndmask_b32_e64 v143, v143, v109, s[8:9]
	v_cmp_eq_u32_e32 vcc, v113, v8
	v_cmp_eq_u32_e64 s[0:1], v121, v8
	v_cmp_eq_u32_e64 s[6:7], v129, v8
	v_cmp_eq_u32_e64 s[8:9], v137, v8
	v_cndmask_b32_e32 v119, v119, v110, vcc
	v_cndmask_b32_e64 v127, v127, v110, s[0:1]
	v_cndmask_b32_e64 v135, v135, v110, s[6:7]
	v_cndmask_b32_e64 v143, v143, v110, s[8:9]
	v_cmp_eq_u32_e32 vcc, v113, v9
	v_cmp_eq_u32_e64 s[0:1], v121, v9
	v_cmp_eq_u32_e64 s[6:7], v129, v9
	v_cmp_eq_u32_e64 s[8:9], v137, v9
	v_cndmask_b32_e32 v119, v119, v111, vcc
	v_cndmask_b32_e64 v127, v127, v111, s[0:1]
	v_cndmask_b32_e64 v135, v135, v111, s[6:7]
	v_cndmask_b32_e64 v143, v143, v111, s[8:9]
	v_add_u32_e32 v112, v112, v119
	v_add_u32_e32 v120, v120, v127
	v_add_u32_e32 v128, v128, v135
	v_add_u32_e32 v136, v136, v143
	v_cmp_ne_u32_e32 vcc, -1, v119
	s_and_saveexec_b64 s[24:25], vcc
	ds_write_b32 v112, v114
	s_mov_b64 exec, s[24:25]
	v_cmp_ne_u32_e32 vcc, -1, v127
	s_and_saveexec_b64 s[24:25], vcc
	ds_write_b32 v120, v122
	s_mov_b64 exec, s[24:25]
	v_cmp_ne_u32_e32 vcc, -1, v135
	s_and_saveexec_b64 s[24:25], vcc
	ds_write_b32 v128, v130
	s_mov_b64 exec, s[24:25]
	v_cmp_ne_u32_e32 vcc, -1, v143
	s_and_saveexec_b64 s[24:25], vcc
	ds_write_b32 v136, v138
	s_mov_b64 exec, s[24:25]
	v_and_b32_e32 v112, 0xff, v100
	v_and_b32_e32 v120, 0xff, v101
	v_and_b32_e32 v128, 0xff, v102
	v_and_b32_e32 v136, 0xff, v103
	v_lshlrev_b32_e32 v112, 2, v112
	v_lshlrev_b32_e32 v120, 2, v120
	v_lshlrev_b32_e32 v128, 2, v128
	v_lshlrev_b32_e32 v136, 2, v136
	v_add_u32_e32 v118, v112, v11
	v_add_u32_e32 v126, v120, v11
	v_add_u32_e32 v134, v128, v11
	v_add_u32_e32 v142, v136, v11
	ds_read_b32 v113, v112 offset:36864
	ds_read_b32 v114, v112 offset:36736
	ds_read_b32 v115, v118 offset:30720
	ds_read_b32 v121, v120 offset:36864
	ds_read_b32 v122, v120 offset:36736
	ds_read_b32 v123, v126 offset:31232
	ds_read_b32 v129, v128 offset:36864
	ds_read_b32 v130, v128 offset:36736
	ds_read_b32 v131, v134 offset:31744
	ds_read_b32 v137, v136 offset:36864
	ds_read_b32 v138, v136 offset:36736
	ds_read_b32 v139, v142 offset:32256
	v_add_u32_e32 v117, 240, v36
	v_add_u32_e32 v125, 244, v36
	v_add_u32_e32 v133, 248, v36
	v_add_u32_e32 v141, 252, v36
	v_mul_hi_u32 v118, v117, v16
	v_mul_hi_u32 v126, v125, v16
	v_mul_hi_u32 v134, v133, v16
	v_mul_hi_u32 v142, v141, v16
	v_mul_lo_u32 v118, v118, s11
	v_mul_lo_u32 v126, v126, s11
	v_mul_lo_u32 v134, v134, s11
	v_mul_lo_u32 v142, v142, s11
	v_sub_u32_e32 v117, v117, v118
	v_sub_u32_e32 v125, v125, v126
	v_sub_u32_e32 v133, v133, v134
	v_sub_u32_e32 v141, v141, v142
	v_subrev_u32_e32 v118, s11, v117
	v_subrev_u32_e32 v126, s11, v125
	v_subrev_u32_e32 v134, s11, v133
	v_subrev_u32_e32 v142, s11, v141
	v_cmp_le_u32_e32 vcc, s11, v117
	v_cmp_le_u32_e64 s[0:1], s11, v125
	v_cmp_le_u32_e64 s[6:7], s11, v133
	v_cmp_le_u32_e64 s[8:9], s11, v141
	v_cndmask_b32_e32 v117, v117, v118, vcc
	v_cndmask_b32_e64 v125, v125, v126, s[0:1]
	v_cndmask_b32_e64 v133, v133, v134, s[6:7]
	v_cndmask_b32_e64 v141, v141, v142, s[8:9]
	v_subrev_u32_e32 v118, s11, v117
	v_subrev_u32_e32 v126, s11, v125
	v_subrev_u32_e32 v134, s11, v133
	v_subrev_u32_e32 v142, s11, v141
	v_cmp_le_u32_e32 vcc, s11, v117
	v_cmp_le_u32_e64 s[0:1], s11, v125
	v_cmp_le_u32_e64 s[6:7], s11, v133
	v_cmp_le_u32_e64 s[8:9], s11, v141
	v_cndmask_b32_e32 v117, v117, v118, vcc
	v_cndmask_b32_e64 v125, v125, v126, s[0:1]
	v_cndmask_b32_e64 v133, v133, v134, s[6:7]
	v_cndmask_b32_e64 v141, v141, v142, s[8:9]
	v_ashrrev_i32_e32 v116, 8, v100
	v_ashrrev_i32_e32 v124, 8, v101
	v_ashrrev_i32_e32 v132, 8, v102
	v_ashrrev_i32_e32 v140, 8, v103
	s_waitcnt lgkmcnt(0)
	v_add_u32_e32 v116, v116, v113
	v_add_u32_e32 v124, v124, v121
	v_add_u32_e32 v132, v132, v129
	v_add_u32_e32 v140, v140, v137
	v_add3_u32 v116, v116, v114, v115
	v_add3_u32 v124, v124, v122, v123
	v_add3_u32 v132, v132, v130, v131
	v_add3_u32 v140, v140, v138, v139
	v_cmp_eq_u32_e32 vcc, s93, v117
	v_add_u32_e32 v1, 0x1e000, v10
	s_and_saveexec_b64 s[24:25], vcc
	global_store_dword v1, v116, s[16:17]
	s_mov_b64 exec, s[24:25]
	v_cmp_eq_u32_e32 vcc, s93, v125
	v_add_u32_e32 v1, 0x1e800, v10
	s_and_saveexec_b64 s[24:25], vcc
	global_store_dword v1, v124, s[16:17]
	s_mov_b64 exec, s[24:25]
	v_cmp_eq_u32_e32 vcc, s93, v133
	v_add_u32_e32 v1, 0x1f000, v10
	s_and_saveexec_b64 s[24:25], vcc
	global_store_dword v1, v132, s[16:17]
	s_mov_b64 exec, s[24:25]
	v_cmp_eq_u32_e32 vcc, s93, v141
	v_add_u32_e32 v1, 0x1f800, v10
	s_and_saveexec_b64 s[24:25], vcc
	global_store_dword v1, v140, s[16:17]
	s_mov_b64 exec, s[24:25]
	v_ashrrev_i32_e32 v113, 8, v116
	v_ashrrev_i32_e32 v121, 8, v124
	v_ashrrev_i32_e32 v129, 8, v132
	v_ashrrev_i32_e32 v137, 8, v140
	v_and_b32_e32 v112, 0xff, v116
	v_and_b32_e32 v120, 0xff, v124
	v_and_b32_e32 v128, 0xff, v132
	v_and_b32_e32 v136, 0xff, v140
	v_lshl_add_u32 v112, v112, 2, s10
	v_lshl_add_u32 v120, v120, 2, s10
	v_lshl_add_u32 v128, v128, 2, s10
	v_lshl_add_u32 v136, v136, 2, s10
	v_add_u32_e32 v114, 0x3c00, v34
	v_add_u32_e32 v122, 0x3d00, v34
	v_add_u32_e32 v130, 0x3e00, v34
	v_add_u32_e32 v138, 0x3f00, v34
	v_mov_b32_e32 v119, -1
	v_mov_b32_e32 v127, -1
	v_mov_b32_e32 v135, -1
	v_mov_b32_e32 v143, -1
	v_cmp_eq_u32_e32 vcc, v113, v2
	v_cmp_eq_u32_e64 s[0:1], v121, v2
	v_cmp_eq_u32_e64 s[6:7], v129, v2
	v_cmp_eq_u32_e64 s[8:9], v137, v2
	v_cndmask_b32_e32 v119, v119, v104, vcc
	v_cndmask_b32_e64 v127, v127, v104, s[0:1]
	v_cndmask_b32_e64 v135, v135, v104, s[6:7]
	v_cndmask_b32_e64 v143, v143, v104, s[8:9]
	v_cmp_eq_u32_e32 vcc, v113, v3
	v_cmp_eq_u32_e64 s[0:1], v121, v3
	v_cmp_eq_u32_e64 s[6:7], v129, v3
	v_cmp_eq_u32_e64 s[8:9], v137, v3
	v_cndmask_b32_e32 v119, v119, v105, vcc
	v_cndmask_b32_e64 v127, v127, v105, s[0:1]
	v_cndmask_b32_e64 v135, v135, v105, s[6:7]
	v_cndmask_b32_e64 v143, v143, v105, s[8:9]
	v_cmp_eq_u32_e32 vcc, v113, v4
	v_cmp_eq_u32_e64 s[0:1], v121, v4
	v_cmp_eq_u32_e64 s[6:7], v129, v4
	v_cmp_eq_u32_e64 s[8:9], v137, v4
	v_cndmask_b32_e32 v119, v119, v106, vcc
	v_cndmask_b32_e64 v127, v127, v106, s[0:1]
	v_cndmask_b32_e64 v135, v135, v106, s[6:7]
	v_cndmask_b32_e64 v143, v143, v106, s[8:9]
	v_cmp_eq_u32_e32 vcc, v113, v5
	v_cmp_eq_u32_e64 s[0:1], v121, v5
	v_cmp_eq_u32_e64 s[6:7], v129, v5
	v_cmp_eq_u32_e64 s[8:9], v137, v5
	v_cndmask_b32_e32 v119, v119, v107, vcc
	v_cndmask_b32_e64 v127, v127, v107, s[0:1]
	v_cndmask_b32_e64 v135, v135, v107, s[6:7]
	v_cndmask_b32_e64 v143, v143, v107, s[8:9]
	v_cmp_eq_u32_e32 vcc, v113, v6
	v_cmp_eq_u32_e64 s[0:1], v121, v6
	v_cmp_eq_u32_e64 s[6:7], v129, v6
	v_cmp_eq_u32_e64 s[8:9], v137, v6
	v_cndmask_b32_e32 v119, v119, v108, vcc
	v_cndmask_b32_e64 v127, v127, v108, s[0:1]
	v_cndmask_b32_e64 v135, v135, v108, s[6:7]
	v_cndmask_b32_e64 v143, v143, v108, s[8:9]
	v_cmp_eq_u32_e32 vcc, v113, v7
	v_cmp_eq_u32_e64 s[0:1], v121, v7
	v_cmp_eq_u32_e64 s[6:7], v129, v7
	v_cmp_eq_u32_e64 s[8:9], v137, v7
	v_cndmask_b32_e32 v119, v119, v109, vcc
	v_cndmask_b32_e64 v127, v127, v109, s[0:1]
	v_cndmask_b32_e64 v135, v135, v109, s[6:7]
	v_cndmask_b32_e64 v143, v143, v109, s[8:9]
	v_cmp_eq_u32_e32 vcc, v113, v8
	v_cmp_eq_u32_e64 s[0:1], v121, v8
	v_cmp_eq_u32_e64 s[6:7], v129, v8
	v_cmp_eq_u32_e64 s[8:9], v137, v8
	v_cndmask_b32_e32 v119, v119, v110, vcc
	v_cndmask_b32_e64 v127, v127, v110, s[0:1]
	v_cndmask_b32_e64 v135, v135, v110, s[6:7]
	v_cndmask_b32_e64 v143, v143, v110, s[8:9]
	v_cmp_eq_u32_e32 vcc, v113, v9
	v_cmp_eq_u32_e64 s[0:1], v121, v9
	v_cmp_eq_u32_e64 s[6:7], v129, v9
	v_cmp_eq_u32_e64 s[8:9], v137, v9
	v_cndmask_b32_e32 v119, v119, v111, vcc
	v_cndmask_b32_e64 v127, v127, v111, s[0:1]
	v_cndmask_b32_e64 v135, v135, v111, s[6:7]
	v_cndmask_b32_e64 v143, v143, v111, s[8:9]
	v_add_u32_e32 v112, v112, v119
	v_add_u32_e32 v120, v120, v127
	v_add_u32_e32 v128, v128, v135
	v_add_u32_e32 v136, v136, v143
	v_cmp_ne_u32_e32 vcc, -1, v119
	s_and_saveexec_b64 s[24:25], vcc
	ds_write_b32 v112, v114
	s_mov_b64 exec, s[24:25]
	v_cmp_ne_u32_e32 vcc, -1, v127
	s_and_saveexec_b64 s[24:25], vcc
	ds_write_b32 v120, v122
	s_mov_b64 exec, s[24:25]
	v_cmp_ne_u32_e32 vcc, -1, v135
	s_and_saveexec_b64 s[24:25], vcc
	ds_write_b32 v128, v130
	s_mov_b64 exec, s[24:25]
	v_cmp_ne_u32_e32 vcc, -1, v143
	s_and_saveexec_b64 s[24:25], vcc
	ds_write_b32 v136, v138
	s_mov_b64 exec, s[24:25]
	s_mov_b64 s[0:1], 0

.LBB0_1473:
	s_or_b64 exec, exec, s[0:1]
	s_abs_i32 s11, s80
	v_cvt_f32_u32_e32 v1, s11
	v_mov_b32_e32 v11, 0
	s_sub_i32 s0, 0, s11
	s_waitcnt lgkmcnt(0)
	v_rcp_iflag_f32_e32 v2, v1
	s_barrier
	v_lshrrev_b32_e32 v1, 6, v0
	v_mul_f32_e32 v2, 0x4f7ffffe, v2
	v_cvt_u32_f32_e32 v10, v2
	ds_read_b128 v[2:5], v11 offset:37120
	ds_read_b128 v[6:9], v11 offset:37136
	v_lshrrev_b32_e32 v14, 7, v0
	s_movk_i32 s12, 0xfe00
	v_mul_lo_u32 v12, s0, v10
	v_mul_hi_u32 v12, v10, v12
	v_add_u32_e32 v15, v10, v12
	v_lshlrev_b32_e32 v10, 2, v0
	v_lshl_add_u64 v[12:13], s[28:29], 0, v[10:11]
	s_mov_b64 s[0:1], 0x110000
	v_and_b32_e32 v11, 0x180, v0
	v_lshl_add_u64 v[12:13], v[12:13], 0, s[0:1]
	v_add_u32_e32 v11, 0, v11
	s_mov_b64 s[0:1], 0
	s_add_i32 s10, 0, 0x22000
	s_mov_b64 s[6:7], 0x800
	s_movk_i32 s13, 0x7dff
	v_mov_b32_e32 v16, 2
	v_mov_b32_e32 v17, v34
	s_add_u32 s12, s28, 0x110000
	s_addc_u32 s13, s29, 0
	s_add_u32 s16, s28, 0x150000
	s_addc_u32 s17, s29, 0
	v_lshrrev_b32_e32 v36, 7, v0
	v_mov_b32_e32 v104, 0x0
	v_mov_b32_e32 v105, 0x400
	v_mov_b32_e32 v106, 0x800
	v_mov_b32_e32 v107, 0xc00
	v_mov_b32_e32 v108, 0x1000
	v_mov_b32_e32 v109, 0x1400
	v_mov_b32_e32 v110, 0x1800
	v_mov_b32_e32 v111, 0x1c00
	global_load_dword v40, v10, s[12:13]
	v_add_u32_e32 v1, 0x800, v10
	global_load_dword v41, v1, s[12:13]
	v_add_u32_e32 v1, 0x1000, v10
	global_load_dword v42, v1, s[12:13]
	v_add_u32_e32 v1, 0x1800, v10
	global_load_dword v43, v1, s[12:13]
	v_add_u32_e32 v1, 0x2000, v10
	global_load_dword v44, v1, s[12:13]
	v_add_u32_e32 v1, 0x2800, v10
	global_load_dword v45, v1, s[12:13]
	v_add_u32_e32 v1, 0x3000, v10
	global_load_dword v46, v1, s[12:13]
	v_add_u32_e32 v1, 0x3800, v10
	global_load_dword v47, v1, s[12:13]
	v_add_u32_e32 v1, 0x4000, v10
	global_load_dword v48, v1, s[12:13]
	v_add_u32_e32 v1, 0x4800, v10
	global_load_dword v49, v1, s[12:13]
	v_add_u32_e32 v1, 0x5000, v10
	global_load_dword v50, v1, s[12:13]
	v_add_u32_e32 v1, 0x5800, v10
	global_load_dword v51, v1, s[12:13]
	v_add_u32_e32 v1, 0x6000, v10
	global_load_dword v52, v1, s[12:13]
	v_add_u32_e32 v1, 0x6800, v10
	global_load_dword v53, v1, s[12:13]
	v_add_u32_e32 v1, 0x7000, v10
	global_load_dword v54, v1, s[12:13]
	v_add_u32_e32 v1, 0x7800, v10
	global_load_dword v55, v1, s[12:13]
	v_add_u32_e32 v1, 0x8000, v10
	global_load_dword v56, v1, s[12:13]
	v_add_u32_e32 v1, 0x8800, v10
	global_load_dword v57, v1, s[12:13]
	v_add_u32_e32 v1, 0x9000, v10
	global_load_dword v58, v1, s[12:13]
	v_add_u32_e32 v1, 0x9800, v10
	global_load_dword v59, v1, s[12:13]
	v_add_u32_e32 v1, 0xa000, v10
	global_load_dword v60, v1, s[12:13]
	v_add_u32_e32 v1, 0xa800, v10
	global_load_dword v61, v1, s[12:13]
	v_add_u32_e32 v1, 0xb000, v10
	global_load_dword v62, v1, s[12:13]
	v_add_u32_e32 v1, 0xb800, v10
	global_load_dword v63, v1, s[12:13]
	v_add_u32_e32 v1, 0xc000, v10
	global_load_dword v64, v1, s[12:13]
	v_add_u32_e32 v1, 0xc800, v10
	global_load_dword v65, v1, s[12:13]
	v_add_u32_e32 v1, 0xd000, v10
	global_load_dword v66, v1, s[12:13]
	v_add_u32_e32 v1, 0xd800, v10
	global_load_dword v67, v1, s[12:13]
	v_add_u32_e32 v1, 0xe000, v10
	global_load_dword v68, v1, s[12:13]
	v_add_u32_e32 v1, 0xe800, v10
	global_load_dword v69, v1, s[12:13]
	v_add_u32_e32 v1, 0xf000, v10
	global_load_dword v70, v1, s[12:13]
	v_add_u32_e32 v1, 0xf800, v10
	global_load_dword v71, v1, s[12:13]
	v_add_u32_e32 v1, 0x10000, v10
	global_load_dword v72, v1, s[12:13]
	v_add_u32_e32 v1, 0x10800, v10
	global_load_dword v73, v1, s[12:13]
	v_add_u32_e32 v1, 0x11000, v10
	global_load_dword v74, v1, s[12:13]
	v_add_u32_e32 v1, 0x11800, v10
	global_load_dword v75, v1, s[12:13]
	v_add_u32_e32 v1, 0x12000, v10
	global_load_dword v76, v1, s[12:13]
	v_add_u32_e32 v1, 0x12800, v10
	global_load_dword v77, v1, s[12:13]
	v_add_u32_e32 v1, 0x13000, v10
	global_load_dword v78, v1, s[12:13]
	v_add_u32_e32 v1, 0x13800, v10
	global_load_dword v79, v1, s[12:13]
	v_add_u32_e32 v1, 0x14000, v10
	global_load_dword v80, v1, s[12:13]
	v_add_u32_e32 v1, 0x14800, v10
	global_load_dword v81, v1, s[12:13]
	v_add_u32_e32 v1, 0x15000, v10
	global_load_dword v82, v1, s[12:13]
	v_add_u32_e32 v1, 0x15800, v10
	global_load_dword v83, v1, s[12:13]
	v_add_u32_e32 v1, 0x16000, v10
	global_load_dword v84, v1, s[12:13]
	v_add_u32_e32 v1, 0x16800, v10
	global_load_dword v85, v1, s[12:13]
	v_add_u32_e32 v1, 0x17000, v10
	global_load_dword v86, v1, s[12:13]
	v_add_u32_e32 v1, 0x17800, v10
	global_load_dword v87, v1, s[12:13]
	s_waitcnt vmcnt(32)
	v_add_u32_e32 v1, 0x18000, v10
	global_load_dword v88, v1, s[12:13]
	v_add_u32_e32 v1, 0x18800, v10
	global_load_dword v89, v1, s[12:13]
	v_add_u32_e32 v1, 0x19000, v10
	global_load_dword v90, v1, s[12:13]
	v_add_u32_e32 v1, 0x19800, v10
	global_load_dword v91, v1, s[12:13]
	v_add_u32_e32 v1, 0x1a000, v10
	global_load_dword v92, v1, s[12:13]
	v_add_u32_e32 v1, 0x1a800, v10
	global_load_dword v93, v1, s[12:13]
	v_add_u32_e32 v1, 0x1b000, v10
	global_load_dword v94, v1, s[12:13]
	v_add_u32_e32 v1, 0x1b800, v10
	global_load_dword v95, v1, s[12:13]
	v_add_u32_e32 v1, 0x1c000, v10
	global_load_dword v96, v1, s[12:13]
	v_add_u32_e32 v1, 0x1c800, v10
	global_load_dword v97, v1, s[12:13]
	v_add_u32_e32 v1, 0x1d000, v10
	global_load_dword v98, v1, s[12:13]
	v_add_u32_e32 v1, 0x1d800, v10
	global_load_dword v99, v1, s[12:13]
	v_add_u32_e32 v1, 0x1e000, v10
	global_load_dword v100, v1, s[12:13]
	v_add_u32_e32 v1, 0x1e800, v10
	global_load_dword v101, v1, s[12:13]
	v_add_u32_e32 v1, 0x1f000, v10
	global_load_dword v102, v1, s[12:13]
	v_add_u32_e32 v1, 0x1f800, v10
	global_load_dword v103, v1, s[12:13]
	s_waitcnt lgkmcnt(0)
	s_waitcnt vmcnt(0)
	v_and_b32_e32 v112, 0xff, v40
	v_and_b32_e32 v120, 0xff, v41
	v_and_b32_e32 v128, 0xff, v42
	v_and_b32_e32 v136, 0xff, v43
	v_lshlrev_b32_e32 v112, 2, v112
	v_lshlrev_b32_e32 v120, 2, v120
	v_lshlrev_b32_e32 v128, 2, v128
	v_lshlrev_b32_e32 v136, 2, v136
	v_add_u32_e32 v118, v112, v11
	v_add_u32_e32 v126, v120, v11
	v_add_u32_e32 v134, v128, v11
	v_add_u32_e32 v142, v136, v11
	ds_read_b32 v113, v112 offset:36864
	ds_read_b32 v114, v112 offset:34816
	ds_read_b32 v115, v118
	ds_read_b32 v121, v120 offset:36864
	ds_read_b32 v122, v120 offset:34816
	ds_read_b32 v123, v126 offset:512
	ds_read_b32 v129, v128 offset:36864
	ds_read_b32 v130, v128 offset:34816
	ds_read_b32 v131, v134 offset:1024
	ds_read_b32 v137, v136 offset:36864
	ds_read_b32 v138, v136 offset:34816
	ds_read_b32 v139, v142 offset:1536
	v_mov_b32_e32 v117, v36
	v_add_u32_e32 v125, 4, v36
	v_add_u32_e32 v133, 8, v36
	v_add_u32_e32 v141, 12, v36
	v_mul_hi_u32 v118, v117, v15
	v_mul_hi_u32 v126, v125, v15
	v_mul_hi_u32 v134, v133, v15
	v_mul_hi_u32 v142, v141, v15
	v_mul_lo_u32 v118, v118, s11
	v_mul_lo_u32 v126, v126, s11
	v_mul_lo_u32 v134, v134, s11
	v_mul_lo_u32 v142, v142, s11
	v_sub_u32_e32 v117, v117, v118
	v_sub_u32_e32 v125, v125, v126
	v_sub_u32_e32 v133, v133, v134
	v_sub_u32_e32 v141, v141, v142
	v_subrev_u32_e32 v118, s11, v117
	v_subrev_u32_e32 v126, s11, v125
	v_subrev_u32_e32 v134, s11, v133
	v_subrev_u32_e32 v142, s11, v141
	v_cmp_le_u32_e32 vcc, s11, v117
	v_cmp_le_u32_e64 s[0:1], s11, v125
	v_cmp_le_u32_e64 s[6:7], s11, v133
	v_cmp_le_u32_e64 s[8:9], s11, v141
	v_cndmask_b32_e32 v117, v117, v118, vcc
	v_cndmask_b32_e64 v125, v125, v126, s[0:1]
	v_cndmask_b32_e64 v133, v133, v134, s[6:7]
	v_cndmask_b32_e64 v141, v141, v142, s[8:9]
	v_subrev_u32_e32 v118, s11, v117
	v_subrev_u32_e32 v126, s11, v125
	v_subrev_u32_e32 v134, s11, v133
	v_subrev_u32_e32 v142, s11, v141
	v_cmp_le_u32_e32 vcc, s11, v117
	v_cmp_le_u32_e64 s[0:1], s11, v125
	v_cmp_le_u32_e64 s[6:7], s11, v133
	v_cmp_le_u32_e64 s[8:9], s11, v141
	v_cndmask_b32_e32 v117, v117, v118, vcc
	v_cndmask_b32_e64 v125, v125, v126, s[0:1]
	v_cndmask_b32_e64 v133, v133, v134, s[6:7]
	v_cndmask_b32_e64 v141, v141, v142, s[8:9]
	v_ashrrev_i32_e32 v116, 8, v40
	v_ashrrev_i32_e32 v124, 8, v41
	v_ashrrev_i32_e32 v132, 8, v42
	v_ashrrev_i32_e32 v140, 8, v43
	s_waitcnt lgkmcnt(0)
	v_add_u32_e32 v116, v116, v113
	v_add_u32_e32 v124, v124, v121
	v_add_u32_e32 v132, v132, v129
	v_add_u32_e32 v140, v140, v137
	v_add3_u32 v116, v116, v114, v115
	v_add3_u32 v124, v124, v122, v123
	v_add3_u32 v132, v132, v130, v131
	v_add3_u32 v140, v140, v138, v139
	v_cmp_eq_u32_e32 vcc, s93, v117
	v_mov_b32_e32 v1, v10
	s_and_saveexec_b64 s[24:25], vcc
	global_store_dword v1, v116, s[16:17]
	s_mov_b64 exec, s[24:25]
	v_cmp_eq_u32_e32 vcc, s93, v125
	v_add_u32_e32 v1, 0x800, v10
	s_and_saveexec_b64 s[24:25], vcc
	global_store_dword v1, v124, s[16:17]
	s_mov_b64 exec, s[24:25]
	v_cmp_eq_u32_e32 vcc, s93, v133
	v_add_u32_e32 v1, 0x1000, v10
	s_and_saveexec_b64 s[24:25], vcc
	global_store_dword v1, v132, s[16:17]
	s_mov_b64 exec, s[24:25]
	v_cmp_eq_u32_e32 vcc, s93, v141
	v_add_u32_e32 v1, 0x1800, v10
	s_and_saveexec_b64 s[24:25], vcc
	global_store_dword v1, v140, s[16:17]
	s_mov_b64 exec, s[24:25]
	v_ashrrev_i32_e32 v113, 8, v116
	v_ashrrev_i32_e32 v121, 8, v124
	v_ashrrev_i32_e32 v129, 8, v132
	v_ashrrev_i32_e32 v137, 8, v140
	v_and_b32_e32 v112, 0xff, v116
	v_and_b32_e32 v120, 0xff, v124
	v_and_b32_e32 v128, 0xff, v132
	v_and_b32_e32 v136, 0xff, v140
	v_lshl_add_u32 v112, v112, 2, s10
	v_lshl_add_u32 v120, v120, 2, s10
	v_lshl_add_u32 v128, v128, 2, s10
	v_lshl_add_u32 v136, v136, 2, s10
	v_mov_b32_e32 v114, v34
	v_add_u32_e32 v122, 0x100, v34
	v_add_u32_e32 v130, 0x200, v34
	v_add_u32_e32 v138, 0x300, v34
	v_mov_b32_e32 v119, -1
	v_mov_b32_e32 v127, -1
	v_mov_b32_e32 v135, -1
	v_mov_b32_e32 v143, -1
	v_cmp_eq_u32_e32 vcc, v113, v2
	v_cmp_eq_u32_e64 s[0:1], v121, v2
	v_cmp_eq_u32_e64 s[6:7], v129, v2
	v_cmp_eq_u32_e64 s[8:9], v137, v2
	v_cndmask_b32_e32 v119, v119, v104, vcc
	v_cndmask_b32_e64 v127, v127, v104, s[0:1]
	v_cndmask_b32_e64 v135, v135, v104, s[6:7]
	v_cndmask_b32_e64 v143, v143, v104, s[8:9]
	v_cmp_eq_u32_e32 vcc, v113, v3
	v_cmp_eq_u32_e64 s[0:1], v121, v3
	v_cmp_eq_u32_e64 s[6:7], v129, v3
	v_cmp_eq_u32_e64 s[8:9], v137, v3
	v_cndmask_b32_e32 v119, v119, v105, vcc
	v_cndmask_b32_e64 v127, v127, v105, s[0:1]
	v_cndmask_b32_e64 v135, v135, v105, s[6:7]
	v_cndmask_b32_e64 v143, v143, v105, s[8:9]
	v_cmp_eq_u32_e32 vcc, v113, v4
	v_cmp_eq_u32_e64 s[0:1], v121, v4
	v_cmp_eq_u32_e64 s[6:7], v129, v4
	v_cmp_eq_u32_e64 s[8:9], v137, v4
	v_cndmask_b32_e32 v119, v119, v106, vcc
	v_cndmask_b32_e64 v127, v127, v106, s[0:1]
	v_cndmask_b32_e64 v135, v135, v106, s[6:7]
	v_cndmask_b32_e64 v143, v143, v106, s[8:9]
	v_cmp_eq_u32_e32 vcc, v113, v5
	v_cmp_eq_u32_e64 s[0:1], v121, v5
	v_cmp_eq_u32_e64 s[6:7], v129, v5
	v_cmp_eq_u32_e64 s[8:9], v137, v5
	v_cndmask_b32_e32 v119, v119, v107, vcc
	v_cndmask_b32_e64 v127, v127, v107, s[0:1]
	v_cndmask_b32_e64 v135, v135, v107, s[6:7]
	v_cndmask_b32_e64 v143, v143, v107, s[8:9]
	v_cmp_eq_u32_e32 vcc, v113, v6
	v_cmp_eq_u32_e64 s[0:1], v121, v6
	v_cmp_eq_u32_e64 s[6:7], v129, v6
	v_cmp_eq_u32_e64 s[8:9], v137, v6
	v_cndmask_b32_e32 v119, v119, v108, vcc
	v_cndmask_b32_e64 v127, v127, v108, s[0:1]
	v_cndmask_b32_e64 v135, v135, v108, s[6:7]
	v_cndmask_b32_e64 v143, v143, v108, s[8:9]
	v_cmp_eq_u32_e32 vcc, v113, v7
	v_cmp_eq_u32_e64 s[0:1], v121, v7
	v_cmp_eq_u32_e64 s[6:7], v129, v7
	v_cmp_eq_u32_e64 s[8:9], v137, v7
	v_cndmask_b32_e32 v119, v119, v109, vcc
	v_cndmask_b32_e64 v127, v127, v109, s[0:1]
	v_cndmask_b32_e64 v135, v135, v109, s[6:7]
	v_cndmask_b32_e64 v143, v143, v109, s[8:9]
	v_cmp_eq_u32_e32 vcc, v113, v8
	v_cmp_eq_u32_e64 s[0:1], v121, v8
	v_cmp_eq_u32_e64 s[6:7], v129, v8
	v_cmp_eq_u32_e64 s[8:9], v137, v8
	v_cndmask_b32_e32 v119, v119, v110, vcc
	v_cndmask_b32_e64 v127, v127, v110, s[0:1]
	v_cndmask_b32_e64 v135, v135, v110, s[6:7]
	v_cndmask_b32_e64 v143, v143, v110, s[8:9]
	v_cmp_eq_u32_e32 vcc, v113, v9
	v_cmp_eq_u32_e64 s[0:1], v121, v9
	v_cmp_eq_u32_e64 s[6:7], v129, v9
	v_cmp_eq_u32_e64 s[8:9], v137, v9
	v_cndmask_b32_e32 v119, v119, v111, vcc
	v_cndmask_b32_e64 v127, v127, v111, s[0:1]
	v_cndmask_b32_e64 v135, v135, v111, s[6:7]
	v_cndmask_b32_e64 v143, v143, v111, s[8:9]
	v_add_u32_e32 v112, v112, v119
	v_add_u32_e32 v120, v120, v127
	v_add_u32_e32 v128, v128, v135
	v_add_u32_e32 v136, v136, v143
	v_cmp_ne_u32_e32 vcc, -1, v119
	s_and_saveexec_b64 s[24:25], vcc
	ds_write_b32 v112, v114
	s_mov_b64 exec, s[24:25]
	v_cmp_ne_u32_e32 vcc, -1, v127
	s_and_saveexec_b64 s[24:25], vcc
	ds_write_b32 v120, v122
	s_mov_b64 exec, s[24:25]
	v_cmp_ne_u32_e32 vcc, -1, v135
	s_and_saveexec_b64 s[24:25], vcc
	ds_write_b32 v128, v130
	s_mov_b64 exec, s[24:25]
	v_cmp_ne_u32_e32 vcc, -1, v143
	s_and_saveexec_b64 s[24:25], vcc
	ds_write_b32 v136, v138
	s_mov_b64 exec, s[24:25]
	v_and_b32_e32 v112, 0xff, v44
	v_and_b32_e32 v120, 0xff, v45
	v_and_b32_e32 v128, 0xff, v46
	v_and_b32_e32 v136, 0xff, v47
	v_lshlrev_b32_e32 v112, 2, v112
	v_lshlrev_b32_e32 v120, 2, v120
	v_lshlrev_b32_e32 v128, 2, v128
	v_lshlrev_b32_e32 v136, 2, v136
	v_add_u32_e32 v118, v112, v11
	v_add_u32_e32 v126, v120, v11
	v_add_u32_e32 v134, v128, v11
	v_add_u32_e32 v142, v136, v11
	ds_read_b32 v113, v112 offset:36864
	ds_read_b32 v114, v112 offset:34944
	ds_read_b32 v115, v118 offset:2048
	ds_read_b32 v121, v120 offset:36864
	ds_read_b32 v122, v120 offset:34944
	ds_read_b32 v123, v126 offset:2560
	ds_read_b32 v129, v128 offset:36864
	ds_read_b32 v130, v128 offset:34944
	ds_read_b32 v131, v134 offset:3072
	ds_read_b32 v137, v136 offset:36864
	ds_read_b32 v138, v136 offset:34944
	ds_read_b32 v139, v142 offset:3584
	v_add_u32_e32 v117, 16, v36
	v_add_u32_e32 v125, 20, v36
	v_add_u32_e32 v133, 24, v36
	v_add_u32_e32 v141, 28, v36
	v_mul_hi_u32 v118, v117, v15
	v_mul_hi_u32 v126, v125, v15
	v_mul_hi_u32 v134, v133, v15
	v_mul_hi_u32 v142, v141, v15
	v_mul_lo_u32 v118, v118, s11
	v_mul_lo_u32 v126, v126, s11
	v_mul_lo_u32 v134, v134, s11
	v_mul_lo_u32 v142, v142, s11
	v_sub_u32_e32 v117, v117, v118
	v_sub_u32_e32 v125, v125, v126
	v_sub_u32_e32 v133, v133, v134
	v_sub_u32_e32 v141, v141, v142
	v_subrev_u32_e32 v118, s11, v117
	v_subrev_u32_e32 v126, s11, v125
	v_subrev_u32_e32 v134, s11, v133
	v_subrev_u32_e32 v142, s11, v141
	v_cmp_le_u32_e32 vcc, s11, v117
	v_cmp_le_u32_e64 s[0:1], s11, v125
	v_cmp_le_u32_e64 s[6:7], s11, v133
	v_cmp_le_u32_e64 s[8:9], s11, v141
	v_cndmask_b32_e32 v117, v117, v118, vcc
	v_cndmask_b32_e64 v125, v125, v126, s[0:1]
	v_cndmask_b32_e64 v133, v133, v134, s[6:7]
	v_cndmask_b32_e64 v141, v141, v142, s[8:9]
	v_subrev_u32_e32 v118, s11, v117
	v_subrev_u32_e32 v126, s11, v125
	v_subrev_u32_e32 v134, s11, v133
	v_subrev_u32_e32 v142, s11, v141
	v_cmp_le_u32_e32 vcc, s11, v117
	v_cmp_le_u32_e64 s[0:1], s11, v125
	v_cmp_le_u32_e64 s[6:7], s11, v133
	v_cmp_le_u32_e64 s[8:9], s11, v141
	v_cndmask_b32_e32 v117, v117, v118, vcc
	v_cndmask_b32_e64 v125, v125, v126, s[0:1]
	v_cndmask_b32_e64 v133, v133, v134, s[6:7]
	v_cndmask_b32_e64 v141, v141, v142, s[8:9]
	v_ashrrev_i32_e32 v116, 8, v44
	v_ashrrev_i32_e32 v124, 8, v45
	v_ashrrev_i32_e32 v132, 8, v46
	v_ashrrev_i32_e32 v140, 8, v47
	s_waitcnt lgkmcnt(0)
	v_add_u32_e32 v116, v116, v113
	v_add_u32_e32 v124, v124, v121
	v_add_u32_e32 v132, v132, v129
	v_add_u32_e32 v140, v140, v137
	v_add3_u32 v116, v116, v114, v115
	v_add3_u32 v124, v124, v122, v123
	v_add3_u32 v132, v132, v130, v131
	v_add3_u32 v140, v140, v138, v139
	v_cmp_eq_u32_e32 vcc, s93, v117
	v_add_u32_e32 v1, 0x2000, v10
	s_and_saveexec_b64 s[24:25], vcc
	global_store_dword v1, v116, s[16:17]
	s_mov_b64 exec, s[24:25]
	v_cmp_eq_u32_e32 vcc, s93, v125
	v_add_u32_e32 v1, 0x2800, v10
	s_and_saveexec_b64 s[24:25], vcc
	global_store_dword v1, v124, s[16:17]
	s_mov_b64 exec, s[24:25]
	v_cmp_eq_u32_e32 vcc, s93, v133
	v_add_u32_e32 v1, 0x3000, v10
	s_and_saveexec_b64 s[24:25], vcc
	global_store_dword v1, v132, s[16:17]
	s_mov_b64 exec, s[24:25]
	v_cmp_eq_u32_e32 vcc, s93, v141
	v_add_u32_e32 v1, 0x3800, v10
	s_and_saveexec_b64 s[24:25], vcc
	global_store_dword v1, v140, s[16:17]
	s_mov_b64 exec, s[24:25]
	v_ashrrev_i32_e32 v113, 8, v116
	v_ashrrev_i32_e32 v121, 8, v124
	v_ashrrev_i32_e32 v129, 8, v132
	v_ashrrev_i32_e32 v137, 8, v140
	v_and_b32_e32 v112, 0xff, v116
	v_and_b32_e32 v120, 0xff, v124
	v_and_b32_e32 v128, 0xff, v132
	v_and_b32_e32 v136, 0xff, v140
	v_lshl_add_u32 v112, v112, 2, s10
	v_lshl_add_u32 v120, v120, 2, s10
	v_lshl_add_u32 v128, v128, 2, s10
	v_lshl_add_u32 v136, v136, 2, s10
	v_add_u32_e32 v114, 0x400, v34
	v_add_u32_e32 v122, 0x500, v34
	v_add_u32_e32 v130, 0x600, v34
	v_add_u32_e32 v138, 0x700, v34
	v_mov_b32_e32 v119, -1
	v_mov_b32_e32 v127, -1
	v_mov_b32_e32 v135, -1
	v_mov_b32_e32 v143, -1
	v_cmp_eq_u32_e32 vcc, v113, v2
	v_cmp_eq_u32_e64 s[0:1], v121, v2
	v_cmp_eq_u32_e64 s[6:7], v129, v2
	v_cmp_eq_u32_e64 s[8:9], v137, v2
	v_cndmask_b32_e32 v119, v119, v104, vcc
	v_cndmask_b32_e64 v127, v127, v104, s[0:1]
	v_cndmask_b32_e64 v135, v135, v104, s[6:7]
	v_cndmask_b32_e64 v143, v143, v104, s[8:9]
	v_cmp_eq_u32_e32 vcc, v113, v3
	v_cmp_eq_u32_e64 s[0:1], v121, v3
	v_cmp_eq_u32_e64 s[6:7], v129, v3
	v_cmp_eq_u32_e64 s[8:9], v137, v3
	v_cndmask_b32_e32 v119, v119, v105, vcc
	v_cndmask_b32_e64 v127, v127, v105, s[0:1]
	v_cndmask_b32_e64 v135, v135, v105, s[6:7]
	v_cndmask_b32_e64 v143, v143, v105, s[8:9]
	v_cmp_eq_u32_e32 vcc, v113, v4
	v_cmp_eq_u32_e64 s[0:1], v121, v4
	v_cmp_eq_u32_e64 s[6:7], v129, v4
	v_cmp_eq_u32_e64 s[8:9], v137, v4
	v_cndmask_b32_e32 v119, v119, v106, vcc
	v_cndmask_b32_e64 v127, v127, v106, s[0:1]
	v_cndmask_b32_e64 v135, v135, v106, s[6:7]
	v_cndmask_b32_e64 v143, v143, v106, s[8:9]
	v_cmp_eq_u32_e32 vcc, v113, v5
	v_cmp_eq_u32_e64 s[0:1], v121, v5
	v_cmp_eq_u32_e64 s[6:7], v129, v5
	v_cmp_eq_u32_e64 s[8:9], v137, v5
	v_cndmask_b32_e32 v119, v119, v107, vcc
	v_cndmask_b32_e64 v127, v127, v107, s[0:1]
	v_cndmask_b32_e64 v135, v135, v107, s[6:7]
	v_cndmask_b32_e64 v143, v143, v107, s[8:9]
	v_cmp_eq_u32_e32 vcc, v113, v6
	v_cmp_eq_u32_e64 s[0:1], v121, v6
	v_cmp_eq_u32_e64 s[6:7], v129, v6
	v_cmp_eq_u32_e64 s[8:9], v137, v6
	v_cndmask_b32_e32 v119, v119, v108, vcc
	v_cndmask_b32_e64 v127, v127, v108, s[0:1]
	v_cndmask_b32_e64 v135, v135, v108, s[6:7]
	v_cndmask_b32_e64 v143, v143, v108, s[8:9]
	v_cmp_eq_u32_e32 vcc, v113, v7
	v_cmp_eq_u32_e64 s[0:1], v121, v7
	v_cmp_eq_u32_e64 s[6:7], v129, v7
	v_cmp_eq_u32_e64 s[8:9], v137, v7
	v_cndmask_b32_e32 v119, v119, v109, vcc
	v_cndmask_b32_e64 v127, v127, v109, s[0:1]
	v_cndmask_b32_e64 v135, v135, v109, s[6:7]
	v_cndmask_b32_e64 v143, v143, v109, s[8:9]
	v_cmp_eq_u32_e32 vcc, v113, v8
	v_cmp_eq_u32_e64 s[0:1], v121, v8
	v_cmp_eq_u32_e64 s[6:7], v129, v8
	v_cmp_eq_u32_e64 s[8:9], v137, v8
	v_cndmask_b32_e32 v119, v119, v110, vcc
	v_cndmask_b32_e64 v127, v127, v110, s[0:1]
	v_cndmask_b32_e64 v135, v135, v110, s[6:7]
	v_cndmask_b32_e64 v143, v143, v110, s[8:9]
	v_cmp_eq_u32_e32 vcc, v113, v9
	v_cmp_eq_u32_e64 s[0:1], v121, v9
	v_cmp_eq_u32_e64 s[6:7], v129, v9
	v_cmp_eq_u32_e64 s[8:9], v137, v9
	v_cndmask_b32_e32 v119, v119, v111, vcc
	v_cndmask_b32_e64 v127, v127, v111, s[0:1]
	v_cndmask_b32_e64 v135, v135, v111, s[6:7]
	v_cndmask_b32_e64 v143, v143, v111, s[8:9]
	v_add_u32_e32 v112, v112, v119
	v_add_u32_e32 v120, v120, v127
	v_add_u32_e32 v128, v128, v135
	v_add_u32_e32 v136, v136, v143
	v_cmp_ne_u32_e32 vcc, -1, v119
	s_and_saveexec_b64 s[24:25], vcc
	ds_write_b32 v112, v114
	s_mov_b64 exec, s[24:25]
	v_cmp_ne_u32_e32 vcc, -1, v127
	s_and_saveexec_b64 s[24:25], vcc
	ds_write_b32 v120, v122
	s_mov_b64 exec, s[24:25]
	v_cmp_ne_u32_e32 vcc, -1, v135
	s_and_saveexec_b64 s[24:25], vcc
	ds_write_b32 v128, v130
	s_mov_b64 exec, s[24:25]
	v_cmp_ne_u32_e32 vcc, -1, v143
	s_and_saveexec_b64 s[24:25], vcc
	ds_write_b32 v136, v138
	s_mov_b64 exec, s[24:25]
	v_and_b32_e32 v112, 0xff, v48
	v_and_b32_e32 v120, 0xff, v49
	v_and_b32_e32 v128, 0xff, v50
	v_and_b32_e32 v136, 0xff, v51
	v_lshlrev_b32_e32 v112, 2, v112
	v_lshlrev_b32_e32 v120, 2, v120
	v_lshlrev_b32_e32 v128, 2, v128
	v_lshlrev_b32_e32 v136, 2, v136
	v_add_u32_e32 v118, v112, v11
	v_add_u32_e32 v126, v120, v11
	v_add_u32_e32 v134, v128, v11
	v_add_u32_e32 v142, v136, v11
	ds_read_b32 v113, v112 offset:36864
	ds_read_b32 v114, v112 offset:35072
	ds_read_b32 v115, v118 offset:4096
	ds_read_b32 v121, v120 offset:36864
	ds_read_b32 v122, v120 offset:35072
	ds_read_b32 v123, v126 offset:4608
	ds_read_b32 v129, v128 offset:36864
	ds_read_b32 v130, v128 offset:35072
	ds_read_b32 v131, v134 offset:5120
	ds_read_b32 v137, v136 offset:36864
	ds_read_b32 v138, v136 offset:35072
	ds_read_b32 v139, v142 offset:5632
	v_add_u32_e32 v117, 32, v36
	v_add_u32_e32 v125, 36, v36
	v_add_u32_e32 v133, 40, v36
	v_add_u32_e32 v141, 44, v36
	v_mul_hi_u32 v118, v117, v15
	v_mul_hi_u32 v126, v125, v15
	v_mul_hi_u32 v134, v133, v15
	v_mul_hi_u32 v142, v141, v15
	v_mul_lo_u32 v118, v118, s11
	v_mul_lo_u32 v126, v126, s11
	v_mul_lo_u32 v134, v134, s11
	v_mul_lo_u32 v142, v142, s11
	v_sub_u32_e32 v117, v117, v118
	v_sub_u32_e32 v125, v125, v126
	v_sub_u32_e32 v133, v133, v134
	v_sub_u32_e32 v141, v141, v142
	v_subrev_u32_e32 v118, s11, v117
	v_subrev_u32_e32 v126, s11, v125
	v_subrev_u32_e32 v134, s11, v133
	v_subrev_u32_e32 v142, s11, v141
	v_cmp_le_u32_e32 vcc, s11, v117
	v_cmp_le_u32_e64 s[0:1], s11, v125
	v_cmp_le_u32_e64 s[6:7], s11, v133
	v_cmp_le_u32_e64 s[8:9], s11, v141
	v_cndmask_b32_e32 v117, v117, v118, vcc
	v_cndmask_b32_e64 v125, v125, v126, s[0:1]
	v_cndmask_b32_e64 v133, v133, v134, s[6:7]
	v_cndmask_b32_e64 v141, v141, v142, s[8:9]
	v_subrev_u32_e32 v118, s11, v117
	v_subrev_u32_e32 v126, s11, v125
	v_subrev_u32_e32 v134, s11, v133
	v_subrev_u32_e32 v142, s11, v141
	v_cmp_le_u32_e32 vcc, s11, v117
	v_cmp_le_u32_e64 s[0:1], s11, v125
	v_cmp_le_u32_e64 s[6:7], s11, v133
	v_cmp_le_u32_e64 s[8:9], s11, v141
	v_cndmask_b32_e32 v117, v117, v118, vcc
	v_cndmask_b32_e64 v125, v125, v126, s[0:1]
	v_cndmask_b32_e64 v133, v133, v134, s[6:7]
	v_cndmask_b32_e64 v141, v141, v142, s[8:9]
	v_ashrrev_i32_e32 v116, 8, v48
	v_ashrrev_i32_e32 v124, 8, v49
	v_ashrrev_i32_e32 v132, 8, v50
	v_ashrrev_i32_e32 v140, 8, v51
	s_waitcnt lgkmcnt(0)
	v_add_u32_e32 v116, v116, v113
	v_add_u32_e32 v124, v124, v121
	v_add_u32_e32 v132, v132, v129
	v_add_u32_e32 v140, v140, v137
	v_add3_u32 v116, v116, v114, v115
	v_add3_u32 v124, v124, v122, v123
	v_add3_u32 v132, v132, v130, v131
	v_add3_u32 v140, v140, v138, v139
	v_cmp_eq_u32_e32 vcc, s93, v117
	v_add_u32_e32 v1, 0x4000, v10
	s_and_saveexec_b64 s[24:25], vcc
	global_store_dword v1, v116, s[16:17]
	s_mov_b64 exec, s[24:25]
	v_cmp_eq_u32_e32 vcc, s93, v125
	v_add_u32_e32 v1, 0x4800, v10
	s_and_saveexec_b64 s[24:25], vcc
	global_store_dword v1, v124, s[16:17]
	s_mov_b64 exec, s[24:25]
	v_cmp_eq_u32_e32 vcc, s93, v133
	v_add_u32_e32 v1, 0x5000, v10
	s_and_saveexec_b64 s[24:25], vcc
	global_store_dword v1, v132, s[16:17]
	s_mov_b64 exec, s[24:25]
	v_cmp_eq_u32_e32 vcc, s93, v141
	v_add_u32_e32 v1, 0x5800, v10
	s_and_saveexec_b64 s[24:25], vcc
	global_store_dword v1, v140, s[16:17]
	s_mov_b64 exec, s[24:25]
	v_ashrrev_i32_e32 v113, 8, v116
	v_ashrrev_i32_e32 v121, 8, v124
	v_ashrrev_i32_e32 v129, 8, v132
	v_ashrrev_i32_e32 v137, 8, v140
	v_and_b32_e32 v112, 0xff, v116
	v_and_b32_e32 v120, 0xff, v124
	v_and_b32_e32 v128, 0xff, v132
	v_and_b32_e32 v136, 0xff, v140
	v_lshl_add_u32 v112, v112, 2, s10
	v_lshl_add_u32 v120, v120, 2, s10
	v_lshl_add_u32 v128, v128, 2, s10
	v_lshl_add_u32 v136, v136, 2, s10
	v_add_u32_e32 v114, 0x800, v34
	v_add_u32_e32 v122, 0x900, v34
	v_add_u32_e32 v130, 0xa00, v34
	v_add_u32_e32 v138, 0xb00, v34
	v_mov_b32_e32 v119, -1
	v_mov_b32_e32 v127, -1
	v_mov_b32_e32 v135, -1
	v_mov_b32_e32 v143, -1
	v_cmp_eq_u32_e32 vcc, v113, v2
	v_cmp_eq_u32_e64 s[0:1], v121, v2
	v_cmp_eq_u32_e64 s[6:7], v129, v2
	v_cmp_eq_u32_e64 s[8:9], v137, v2
	v_cndmask_b32_e32 v119, v119, v104, vcc
	v_cndmask_b32_e64 v127, v127, v104, s[0:1]
	v_cndmask_b32_e64 v135, v135, v104, s[6:7]
	v_cndmask_b32_e64 v143, v143, v104, s[8:9]
	v_cmp_eq_u32_e32 vcc, v113, v3
	v_cmp_eq_u32_e64 s[0:1], v121, v3
	v_cmp_eq_u32_e64 s[6:7], v129, v3
	v_cmp_eq_u32_e64 s[8:9], v137, v3
	v_cndmask_b32_e32 v119, v119, v105, vcc
	v_cndmask_b32_e64 v127, v127, v105, s[0:1]
	v_cndmask_b32_e64 v135, v135, v105, s[6:7]
	v_cndmask_b32_e64 v143, v143, v105, s[8:9]
	v_cmp_eq_u32_e32 vcc, v113, v4
	v_cmp_eq_u32_e64 s[0:1], v121, v4
	v_cmp_eq_u32_e64 s[6:7], v129, v4
	v_cmp_eq_u32_e64 s[8:9], v137, v4
	v_cndmask_b32_e32 v119, v119, v106, vcc
	v_cndmask_b32_e64 v127, v127, v106, s[0:1]
	v_cndmask_b32_e64 v135, v135, v106, s[6:7]
	v_cndmask_b32_e64 v143, v143, v106, s[8:9]
	v_cmp_eq_u32_e32 vcc, v113, v5
	v_cmp_eq_u32_e64 s[0:1], v121, v5
	v_cmp_eq_u32_e64 s[6:7], v129, v5
	v_cmp_eq_u32_e64 s[8:9], v137, v5
	v_cndmask_b32_e32 v119, v119, v107, vcc
	v_cndmask_b32_e64 v127, v127, v107, s[0:1]
	v_cndmask_b32_e64 v135, v135, v107, s[6:7]
	v_cndmask_b32_e64 v143, v143, v107, s[8:9]
	v_cmp_eq_u32_e32 vcc, v113, v6
	v_cmp_eq_u32_e64 s[0:1], v121, v6
	v_cmp_eq_u32_e64 s[6:7], v129, v6
	v_cmp_eq_u32_e64 s[8:9], v137, v6
	v_cndmask_b32_e32 v119, v119, v108, vcc
	v_cndmask_b32_e64 v127, v127, v108, s[0:1]
	v_cndmask_b32_e64 v135, v135, v108, s[6:7]
	v_cndmask_b32_e64 v143, v143, v108, s[8:9]
	v_cmp_eq_u32_e32 vcc, v113, v7
	v_cmp_eq_u32_e64 s[0:1], v121, v7
	v_cmp_eq_u32_e64 s[6:7], v129, v7
	v_cmp_eq_u32_e64 s[8:9], v137, v7
	v_cndmask_b32_e32 v119, v119, v109, vcc
	v_cndmask_b32_e64 v127, v127, v109, s[0:1]
	v_cndmask_b32_e64 v135, v135, v109, s[6:7]
	v_cndmask_b32_e64 v143, v143, v109, s[8:9]
	v_cmp_eq_u32_e32 vcc, v113, v8
	v_cmp_eq_u32_e64 s[0:1], v121, v8
	v_cmp_eq_u32_e64 s[6:7], v129, v8
	v_cmp_eq_u32_e64 s[8:9], v137, v8
	v_cndmask_b32_e32 v119, v119, v110, vcc
	v_cndmask_b32_e64 v127, v127, v110, s[0:1]
	v_cndmask_b32_e64 v135, v135, v110, s[6:7]
	v_cndmask_b32_e64 v143, v143, v110, s[8:9]
	v_cmp_eq_u32_e32 vcc, v113, v9
	v_cmp_eq_u32_e64 s[0:1], v121, v9
	v_cmp_eq_u32_e64 s[6:7], v129, v9
	v_cmp_eq_u32_e64 s[8:9], v137, v9
	v_cndmask_b32_e32 v119, v119, v111, vcc
	v_cndmask_b32_e64 v127, v127, v111, s[0:1]
	v_cndmask_b32_e64 v135, v135, v111, s[6:7]
	v_cndmask_b32_e64 v143, v143, v111, s[8:9]
	v_add_u32_e32 v112, v112, v119
	v_add_u32_e32 v120, v120, v127
	v_add_u32_e32 v128, v128, v135
	v_add_u32_e32 v136, v136, v143
	v_cmp_ne_u32_e32 vcc, -1, v119
	s_and_saveexec_b64 s[24:25], vcc
	ds_write_b32 v112, v114
	s_mov_b64 exec, s[24:25]
	v_cmp_ne_u32_e32 vcc, -1, v127
	s_and_saveexec_b64 s[24:25], vcc
	ds_write_b32 v120, v122
	s_mov_b64 exec, s[24:25]
	v_cmp_ne_u32_e32 vcc, -1, v135
	s_and_saveexec_b64 s[24:25], vcc
	ds_write_b32 v128, v130
	s_mov_b64 exec, s[24:25]
	v_cmp_ne_u32_e32 vcc, -1, v143
	s_and_saveexec_b64 s[24:25], vcc
	ds_write_b32 v136, v138
	s_mov_b64 exec, s[24:25]
	v_and_b32_e32 v112, 0xff, v52
	v_and_b32_e32 v120, 0xff, v53
	v_and_b32_e32 v128, 0xff, v54
	v_and_b32_e32 v136, 0xff, v55
	v_lshlrev_b32_e32 v112, 2, v112
	v_lshlrev_b32_e32 v120, 2, v120
	v_lshlrev_b32_e32 v128, 2, v128
	v_lshlrev_b32_e32 v136, 2, v136
	v_add_u32_e32 v118, v112, v11
	v_add_u32_e32 v126, v120, v11
	v_add_u32_e32 v134, v128, v11
	v_add_u32_e32 v142, v136, v11
	ds_read_b32 v113, v112 offset:36864
	ds_read_b32 v114, v112 offset:35200
	ds_read_b32 v115, v118 offset:6144
	ds_read_b32 v121, v120 offset:36864
	ds_read_b32 v122, v120 offset:35200
	ds_read_b32 v123, v126 offset:6656
	ds_read_b32 v129, v128 offset:36864
	ds_read_b32 v130, v128 offset:35200
	ds_read_b32 v131, v134 offset:7168
	ds_read_b32 v137, v136 offset:36864
	ds_read_b32 v138, v136 offset:35200
	ds_read_b32 v139, v142 offset:7680
	v_add_u32_e32 v117, 48, v36
	v_add_u32_e32 v125, 52, v36
	v_add_u32_e32 v133, 56, v36
	v_add_u32_e32 v141, 60, v36
	v_mul_hi_u32 v118, v117, v15
	v_mul_hi_u32 v126, v125, v15
	v_mul_hi_u32 v134, v133, v15
	v_mul_hi_u32 v142, v141, v15
	v_mul_lo_u32 v118, v118, s11
	v_mul_lo_u32 v126, v126, s11
	v_mul_lo_u32 v134, v134, s11
	v_mul_lo_u32 v142, v142, s11
	v_sub_u32_e32 v117, v117, v118
	v_sub_u32_e32 v125, v125, v126
	v_sub_u32_e32 v133, v133, v134
	v_sub_u32_e32 v141, v141, v142
	v_subrev_u32_e32 v118, s11, v117
	v_subrev_u32_e32 v126, s11, v125
	v_subrev_u32_e32 v134, s11, v133
	v_subrev_u32_e32 v142, s11, v141
	v_cmp_le_u32_e32 vcc, s11, v117
	v_cmp_le_u32_e64 s[0:1], s11, v125
	v_cmp_le_u32_e64 s[6:7], s11, v133
	v_cmp_le_u32_e64 s[8:9], s11, v141
	v_cndmask_b32_e32 v117, v117, v118, vcc
	v_cndmask_b32_e64 v125, v125, v126, s[0:1]
	v_cndmask_b32_e64 v133, v133, v134, s[6:7]
	v_cndmask_b32_e64 v141, v141, v142, s[8:9]
	v_subrev_u32_e32 v118, s11, v117
	v_subrev_u32_e32 v126, s11, v125
	v_subrev_u32_e32 v134, s11, v133
	v_subrev_u32_e32 v142, s11, v141
	v_cmp_le_u32_e32 vcc, s11, v117
	v_cmp_le_u32_e64 s[0:1], s11, v125
	v_cmp_le_u32_e64 s[6:7], s11, v133
	v_cmp_le_u32_e64 s[8:9], s11, v141
	v_cndmask_b32_e32 v117, v117, v118, vcc
	v_cndmask_b32_e64 v125, v125, v126, s[0:1]
	v_cndmask_b32_e64 v133, v133, v134, s[6:7]
	v_cndmask_b32_e64 v141, v141, v142, s[8:9]
	v_ashrrev_i32_e32 v116, 8, v52
	v_ashrrev_i32_e32 v124, 8, v53
	v_ashrrev_i32_e32 v132, 8, v54
	v_ashrrev_i32_e32 v140, 8, v55
	s_waitcnt lgkmcnt(0)
	v_add_u32_e32 v116, v116, v113
	v_add_u32_e32 v124, v124, v121
	v_add_u32_e32 v132, v132, v129
	v_add_u32_e32 v140, v140, v137
	v_add3_u32 v116, v116, v114, v115
	v_add3_u32 v124, v124, v122, v123
	v_add3_u32 v132, v132, v130, v131
	v_add3_u32 v140, v140, v138, v139
	v_cmp_eq_u32_e32 vcc, s93, v117
	v_add_u32_e32 v1, 0x6000, v10
	s_and_saveexec_b64 s[24:25], vcc
	global_store_dword v1, v116, s[16:17]
	s_mov_b64 exec, s[24:25]
	v_cmp_eq_u32_e32 vcc, s93, v125
	v_add_u32_e32 v1, 0x6800, v10
	s_and_saveexec_b64 s[24:25], vcc
	global_store_dword v1, v124, s[16:17]
	s_mov_b64 exec, s[24:25]
	v_cmp_eq_u32_e32 vcc, s93, v133
	v_add_u32_e32 v1, 0x7000, v10
	s_and_saveexec_b64 s[24:25], vcc
	global_store_dword v1, v132, s[16:17]
	s_mov_b64 exec, s[24:25]
	v_cmp_eq_u32_e32 vcc, s93, v141
	v_add_u32_e32 v1, 0x7800, v10
	s_and_saveexec_b64 s[24:25], vcc
	global_store_dword v1, v140, s[16:17]
	s_mov_b64 exec, s[24:25]
	v_ashrrev_i32_e32 v113, 8, v116
	v_ashrrev_i32_e32 v121, 8, v124
	v_ashrrev_i32_e32 v129, 8, v132
	v_ashrrev_i32_e32 v137, 8, v140
	v_and_b32_e32 v112, 0xff, v116
	v_and_b32_e32 v120, 0xff, v124
	v_and_b32_e32 v128, 0xff, v132
	v_and_b32_e32 v136, 0xff, v140
	v_lshl_add_u32 v112, v112, 2, s10
	v_lshl_add_u32 v120, v120, 2, s10
	v_lshl_add_u32 v128, v128, 2, s10
	v_lshl_add_u32 v136, v136, 2, s10
	v_add_u32_e32 v114, 0xc00, v34
	v_add_u32_e32 v122, 0xd00, v34
	v_add_u32_e32 v130, 0xe00, v34
	v_add_u32_e32 v138, 0xf00, v34
	v_mov_b32_e32 v119, -1
	v_mov_b32_e32 v127, -1
	v_mov_b32_e32 v135, -1
	v_mov_b32_e32 v143, -1
	v_cmp_eq_u32_e32 vcc, v113, v2
	v_cmp_eq_u32_e64 s[0:1], v121, v2
	v_cmp_eq_u32_e64 s[6:7], v129, v2
	v_cmp_eq_u32_e64 s[8:9], v137, v2
	v_cndmask_b32_e32 v119, v119, v104, vcc
	v_cndmask_b32_e64 v127, v127, v104, s[0:1]
	v_cndmask_b32_e64 v135, v135, v104, s[6:7]
	v_cndmask_b32_e64 v143, v143, v104, s[8:9]
	v_cmp_eq_u32_e32 vcc, v113, v3
	v_cmp_eq_u32_e64 s[0:1], v121, v3
	v_cmp_eq_u32_e64 s[6:7], v129, v3
	v_cmp_eq_u32_e64 s[8:9], v137, v3
	v_cndmask_b32_e32 v119, v119, v105, vcc
	v_cndmask_b32_e64 v127, v127, v105, s[0:1]
	v_cndmask_b32_e64 v135, v135, v105, s[6:7]
	v_cndmask_b32_e64 v143, v143, v105, s[8:9]
	v_cmp_eq_u32_e32 vcc, v113, v4
	v_cmp_eq_u32_e64 s[0:1], v121, v4
	v_cmp_eq_u32_e64 s[6:7], v129, v4
	v_cmp_eq_u32_e64 s[8:9], v137, v4
	v_cndmask_b32_e32 v119, v119, v106, vcc
	v_cndmask_b32_e64 v127, v127, v106, s[0:1]
	v_cndmask_b32_e64 v135, v135, v106, s[6:7]
	v_cndmask_b32_e64 v143, v143, v106, s[8:9]
	v_cmp_eq_u32_e32 vcc, v113, v5
	v_cmp_eq_u32_e64 s[0:1], v121, v5
	v_cmp_eq_u32_e64 s[6:7], v129, v5
	v_cmp_eq_u32_e64 s[8:9], v137, v5
	v_cndmask_b32_e32 v119, v119, v107, vcc
	v_cndmask_b32_e64 v127, v127, v107, s[0:1]
	v_cndmask_b32_e64 v135, v135, v107, s[6:7]
	v_cndmask_b32_e64 v143, v143, v107, s[8:9]
	v_cmp_eq_u32_e32 vcc, v113, v6
	v_cmp_eq_u32_e64 s[0:1], v121, v6
	v_cmp_eq_u32_e64 s[6:7], v129, v6
	v_cmp_eq_u32_e64 s[8:9], v137, v6
	v_cndmask_b32_e32 v119, v119, v108, vcc
	v_cndmask_b32_e64 v127, v127, v108, s[0:1]
	v_cndmask_b32_e64 v135, v135, v108, s[6:7]
	v_cndmask_b32_e64 v143, v143, v108, s[8:9]
	v_cmp_eq_u32_e32 vcc, v113, v7
	v_cmp_eq_u32_e64 s[0:1], v121, v7
	v_cmp_eq_u32_e64 s[6:7], v129, v7
	v_cmp_eq_u32_e64 s[8:9], v137, v7
	v_cndmask_b32_e32 v119, v119, v109, vcc
	v_cndmask_b32_e64 v127, v127, v109, s[0:1]
	v_cndmask_b32_e64 v135, v135, v109, s[6:7]
	v_cndmask_b32_e64 v143, v143, v109, s[8:9]
	v_cmp_eq_u32_e32 vcc, v113, v8
	v_cmp_eq_u32_e64 s[0:1], v121, v8
	v_cmp_eq_u32_e64 s[6:7], v129, v8
	v_cmp_eq_u32_e64 s[8:9], v137, v8
	v_cndmask_b32_e32 v119, v119, v110, vcc
	v_cndmask_b32_e64 v127, v127, v110, s[0:1]
	v_cndmask_b32_e64 v135, v135, v110, s[6:7]
	v_cndmask_b32_e64 v143, v143, v110, s[8:9]
	v_cmp_eq_u32_e32 vcc, v113, v9
	v_cmp_eq_u32_e64 s[0:1], v121, v9
	v_cmp_eq_u32_e64 s[6:7], v129, v9
	v_cmp_eq_u32_e64 s[8:9], v137, v9
	v_cndmask_b32_e32 v119, v119, v111, vcc
	v_cndmask_b32_e64 v127, v127, v111, s[0:1]
	v_cndmask_b32_e64 v135, v135, v111, s[6:7]
	v_cndmask_b32_e64 v143, v143, v111, s[8:9]
	v_add_u32_e32 v112, v112, v119
	v_add_u32_e32 v120, v120, v127
	v_add_u32_e32 v128, v128, v135
	v_add_u32_e32 v136, v136, v143
	v_cmp_ne_u32_e32 vcc, -1, v119
	s_and_saveexec_b64 s[24:25], vcc
	ds_write_b32 v112, v114
	s_mov_b64 exec, s[24:25]
	v_cmp_ne_u32_e32 vcc, -1, v127
	s_and_saveexec_b64 s[24:25], vcc
	ds_write_b32 v120, v122
	s_mov_b64 exec, s[24:25]
	v_cmp_ne_u32_e32 vcc, -1, v135
	s_and_saveexec_b64 s[24:25], vcc
	ds_write_b32 v128, v130
	s_mov_b64 exec, s[24:25]
	v_cmp_ne_u32_e32 vcc, -1, v143
	s_and_saveexec_b64 s[24:25], vcc
	ds_write_b32 v136, v138
	s_mov_b64 exec, s[24:25]
	v_and_b32_e32 v112, 0xff, v56
	v_and_b32_e32 v120, 0xff, v57
	v_and_b32_e32 v128, 0xff, v58
	v_and_b32_e32 v136, 0xff, v59
	v_lshlrev_b32_e32 v112, 2, v112
	v_lshlrev_b32_e32 v120, 2, v120
	v_lshlrev_b32_e32 v128, 2, v128
	v_lshlrev_b32_e32 v136, 2, v136
	v_add_u32_e32 v118, v112, v11
	v_add_u32_e32 v126, v120, v11
	v_add_u32_e32 v134, v128, v11
	v_add_u32_e32 v142, v136, v11
	ds_read_b32 v113, v112 offset:36864
	ds_read_b32 v114, v112 offset:35328
	ds_read_b32 v115, v118 offset:8192
	ds_read_b32 v121, v120 offset:36864
	ds_read_b32 v122, v120 offset:35328
	ds_read_b32 v123, v126 offset:8704
	ds_read_b32 v129, v128 offset:36864
	ds_read_b32 v130, v128 offset:35328
	ds_read_b32 v131, v134 offset:9216
	ds_read_b32 v137, v136 offset:36864
	ds_read_b32 v138, v136 offset:35328
	ds_read_b32 v139, v142 offset:9728
	v_add_u32_e32 v117, 64, v36
	v_add_u32_e32 v125, 68, v36
	v_add_u32_e32 v133, 72, v36
	v_add_u32_e32 v141, 76, v36
	v_mul_hi_u32 v118, v117, v15
	v_mul_hi_u32 v126, v125, v15
	v_mul_hi_u32 v134, v133, v15
	v_mul_hi_u32 v142, v141, v15
	v_mul_lo_u32 v118, v118, s11
	v_mul_lo_u32 v126, v126, s11
	v_mul_lo_u32 v134, v134, s11
	v_mul_lo_u32 v142, v142, s11
	v_sub_u32_e32 v117, v117, v118
	v_sub_u32_e32 v125, v125, v126
	v_sub_u32_e32 v133, v133, v134
	v_sub_u32_e32 v141, v141, v142
	v_subrev_u32_e32 v118, s11, v117
	v_subrev_u32_e32 v126, s11, v125
	v_subrev_u32_e32 v134, s11, v133
	v_subrev_u32_e32 v142, s11, v141
	v_cmp_le_u32_e32 vcc, s11, v117
	v_cmp_le_u32_e64 s[0:1], s11, v125
	v_cmp_le_u32_e64 s[6:7], s11, v133
	v_cmp_le_u32_e64 s[8:9], s11, v141
	v_cndmask_b32_e32 v117, v117, v118, vcc
	v_cndmask_b32_e64 v125, v125, v126, s[0:1]
	v_cndmask_b32_e64 v133, v133, v134, s[6:7]
	v_cndmask_b32_e64 v141, v141, v142, s[8:9]
	v_subrev_u32_e32 v118, s11, v117
	v_subrev_u32_e32 v126, s11, v125
	v_subrev_u32_e32 v134, s11, v133
	v_subrev_u32_e32 v142, s11, v141
	v_cmp_le_u32_e32 vcc, s11, v117
	v_cmp_le_u32_e64 s[0:1], s11, v125
	v_cmp_le_u32_e64 s[6:7], s11, v133
	v_cmp_le_u32_e64 s[8:9], s11, v141
	v_cndmask_b32_e32 v117, v117, v118, vcc
	v_cndmask_b32_e64 v125, v125, v126, s[0:1]
	v_cndmask_b32_e64 v133, v133, v134, s[6:7]
	v_cndmask_b32_e64 v141, v141, v142, s[8:9]
	v_ashrrev_i32_e32 v116, 8, v56
	v_ashrrev_i32_e32 v124, 8, v57
	v_ashrrev_i32_e32 v132, 8, v58
	v_ashrrev_i32_e32 v140, 8, v59
	s_waitcnt lgkmcnt(0)
	v_add_u32_e32 v116, v116, v113
	v_add_u32_e32 v124, v124, v121
	v_add_u32_e32 v132, v132, v129
	v_add_u32_e32 v140, v140, v137
	v_add3_u32 v116, v116, v114, v115
	v_add3_u32 v124, v124, v122, v123
	v_add3_u32 v132, v132, v130, v131
	v_add3_u32 v140, v140, v138, v139
	v_cmp_eq_u32_e32 vcc, s93, v117
	v_add_u32_e32 v1, 0x8000, v10
	s_and_saveexec_b64 s[24:25], vcc
	global_store_dword v1, v116, s[16:17]
	s_mov_b64 exec, s[24:25]
	v_cmp_eq_u32_e32 vcc, s93, v125
	v_add_u32_e32 v1, 0x8800, v10
	s_and_saveexec_b64 s[24:25], vcc
	global_store_dword v1, v124, s[16:17]
	s_mov_b64 exec, s[24:25]
	v_cmp_eq_u32_e32 vcc, s93, v133
	v_add_u32_e32 v1, 0x9000, v10
	s_and_saveexec_b64 s[24:25], vcc
	global_store_dword v1, v132, s[16:17]
	s_mov_b64 exec, s[24:25]
	v_cmp_eq_u32_e32 vcc, s93, v141
	v_add_u32_e32 v1, 0x9800, v10
	s_and_saveexec_b64 s[24:25], vcc
	global_store_dword v1, v140, s[16:17]
	s_mov_b64 exec, s[24:25]
	v_ashrrev_i32_e32 v113, 8, v116
	v_ashrrev_i32_e32 v121, 8, v124
	v_ashrrev_i32_e32 v129, 8, v132
	v_ashrrev_i32_e32 v137, 8, v140
	v_and_b32_e32 v112, 0xff, v116
	v_and_b32_e32 v120, 0xff, v124
	v_and_b32_e32 v128, 0xff, v132
	v_and_b32_e32 v136, 0xff, v140
	v_lshl_add_u32 v112, v112, 2, s10
	v_lshl_add_u32 v120, v120, 2, s10
	v_lshl_add_u32 v128, v128, 2, s10
	v_lshl_add_u32 v136, v136, 2, s10
	v_add_u32_e32 v114, 0x1000, v34
	v_add_u32_e32 v122, 0x1100, v34
	v_add_u32_e32 v130, 0x1200, v34
	v_add_u32_e32 v138, 0x1300, v34
	v_mov_b32_e32 v119, -1
	v_mov_b32_e32 v127, -1
	v_mov_b32_e32 v135, -1
	v_mov_b32_e32 v143, -1
	v_cmp_eq_u32_e32 vcc, v113, v2
	v_cmp_eq_u32_e64 s[0:1], v121, v2
	v_cmp_eq_u32_e64 s[6:7], v129, v2
	v_cmp_eq_u32_e64 s[8:9], v137, v2
	v_cndmask_b32_e32 v119, v119, v104, vcc
	v_cndmask_b32_e64 v127, v127, v104, s[0:1]
	v_cndmask_b32_e64 v135, v135, v104, s[6:7]
	v_cndmask_b32_e64 v143, v143, v104, s[8:9]
	v_cmp_eq_u32_e32 vcc, v113, v3
	v_cmp_eq_u32_e64 s[0:1], v121, v3
	v_cmp_eq_u32_e64 s[6:7], v129, v3
	v_cmp_eq_u32_e64 s[8:9], v137, v3
	v_cndmask_b32_e32 v119, v119, v105, vcc
	v_cndmask_b32_e64 v127, v127, v105, s[0:1]
	v_cndmask_b32_e64 v135, v135, v105, s[6:7]
	v_cndmask_b32_e64 v143, v143, v105, s[8:9]
	v_cmp_eq_u32_e32 vcc, v113, v4
	v_cmp_eq_u32_e64 s[0:1], v121, v4
	v_cmp_eq_u32_e64 s[6:7], v129, v4
	v_cmp_eq_u32_e64 s[8:9], v137, v4
	v_cndmask_b32_e32 v119, v119, v106, vcc
	v_cndmask_b32_e64 v127, v127, v106, s[0:1]
	v_cndmask_b32_e64 v135, v135, v106, s[6:7]
	v_cndmask_b32_e64 v143, v143, v106, s[8:9]
	v_cmp_eq_u32_e32 vcc, v113, v5
	v_cmp_eq_u32_e64 s[0:1], v121, v5
	v_cmp_eq_u32_e64 s[6:7], v129, v5
	v_cmp_eq_u32_e64 s[8:9], v137, v5
	v_cndmask_b32_e32 v119, v119, v107, vcc
	v_cndmask_b32_e64 v127, v127, v107, s[0:1]
	v_cndmask_b32_e64 v135, v135, v107, s[6:7]
	v_cndmask_b32_e64 v143, v143, v107, s[8:9]
	v_cmp_eq_u32_e32 vcc, v113, v6
	v_cmp_eq_u32_e64 s[0:1], v121, v6
	v_cmp_eq_u32_e64 s[6:7], v129, v6
	v_cmp_eq_u32_e64 s[8:9], v137, v6
	v_cndmask_b32_e32 v119, v119, v108, vcc
	v_cndmask_b32_e64 v127, v127, v108, s[0:1]
	v_cndmask_b32_e64 v135, v135, v108, s[6:7]
	v_cndmask_b32_e64 v143, v143, v108, s[8:9]
	v_cmp_eq_u32_e32 vcc, v113, v7
	v_cmp_eq_u32_e64 s[0:1], v121, v7
	v_cmp_eq_u32_e64 s[6:7], v129, v7
	v_cmp_eq_u32_e64 s[8:9], v137, v7
	v_cndmask_b32_e32 v119, v119, v109, vcc
	v_cndmask_b32_e64 v127, v127, v109, s[0:1]
	v_cndmask_b32_e64 v135, v135, v109, s[6:7]
	v_cndmask_b32_e64 v143, v143, v109, s[8:9]
	v_cmp_eq_u32_e32 vcc, v113, v8
	v_cmp_eq_u32_e64 s[0:1], v121, v8
	v_cmp_eq_u32_e64 s[6:7], v129, v8
	v_cmp_eq_u32_e64 s[8:9], v137, v8
	v_cndmask_b32_e32 v119, v119, v110, vcc
	v_cndmask_b32_e64 v127, v127, v110, s[0:1]
	v_cndmask_b32_e64 v135, v135, v110, s[6:7]
	v_cndmask_b32_e64 v143, v143, v110, s[8:9]
	v_cmp_eq_u32_e32 vcc, v113, v9
	v_cmp_eq_u32_e64 s[0:1], v121, v9
	v_cmp_eq_u32_e64 s[6:7], v129, v9
	v_cmp_eq_u32_e64 s[8:9], v137, v9
	v_cndmask_b32_e32 v119, v119, v111, vcc
	v_cndmask_b32_e64 v127, v127, v111, s[0:1]
	v_cndmask_b32_e64 v135, v135, v111, s[6:7]
	v_cndmask_b32_e64 v143, v143, v111, s[8:9]
	v_add_u32_e32 v112, v112, v119
	v_add_u32_e32 v120, v120, v127
	v_add_u32_e32 v128, v128, v135
	v_add_u32_e32 v136, v136, v143
	v_cmp_ne_u32_e32 vcc, -1, v119
	s_and_saveexec_b64 s[24:25], vcc
	ds_write_b32 v112, v114
	s_mov_b64 exec, s[24:25]
	v_cmp_ne_u32_e32 vcc, -1, v127
	s_and_saveexec_b64 s[24:25], vcc
	ds_write_b32 v120, v122
	s_mov_b64 exec, s[24:25]
	v_cmp_ne_u32_e32 vcc, -1, v135
	s_and_saveexec_b64 s[24:25], vcc
	ds_write_b32 v128, v130
	s_mov_b64 exec, s[24:25]
	v_cmp_ne_u32_e32 vcc, -1, v143
	s_and_saveexec_b64 s[24:25], vcc
	ds_write_b32 v136, v138
	s_mov_b64 exec, s[24:25]
	v_and_b32_e32 v112, 0xff, v60
	v_and_b32_e32 v120, 0xff, v61
	v_and_b32_e32 v128, 0xff, v62
	v_and_b32_e32 v136, 0xff, v63
	v_lshlrev_b32_e32 v112, 2, v112
	v_lshlrev_b32_e32 v120, 2, v120
	v_lshlrev_b32_e32 v128, 2, v128
	v_lshlrev_b32_e32 v136, 2, v136
	v_add_u32_e32 v118, v112, v11
	v_add_u32_e32 v126, v120, v11
	v_add_u32_e32 v134, v128, v11
	v_add_u32_e32 v142, v136, v11
	ds_read_b32 v113, v112 offset:36864
	ds_read_b32 v114, v112 offset:35456
	ds_read_b32 v115, v118 offset:10240
	ds_read_b32 v121, v120 offset:36864
	ds_read_b32 v122, v120 offset:35456
	ds_read_b32 v123, v126 offset:10752
	ds_read_b32 v129, v128 offset:36864
	ds_read_b32 v130, v128 offset:35456
	ds_read_b32 v131, v134 offset:11264
	ds_read_b32 v137, v136 offset:36864
	ds_read_b32 v138, v136 offset:35456
	ds_read_b32 v139, v142 offset:11776
	v_add_u32_e32 v117, 80, v36
	v_add_u32_e32 v125, 84, v36
	v_add_u32_e32 v133, 88, v36
	v_add_u32_e32 v141, 92, v36
	v_mul_hi_u32 v118, v117, v15
	v_mul_hi_u32 v126, v125, v15
	v_mul_hi_u32 v134, v133, v15
	v_mul_hi_u32 v142, v141, v15
	v_mul_lo_u32 v118, v118, s11
	v_mul_lo_u32 v126, v126, s11
	v_mul_lo_u32 v134, v134, s11
	v_mul_lo_u32 v142, v142, s11
	v_sub_u32_e32 v117, v117, v118
	v_sub_u32_e32 v125, v125, v126
	v_sub_u32_e32 v133, v133, v134
	v_sub_u32_e32 v141, v141, v142
	v_subrev_u32_e32 v118, s11, v117
	v_subrev_u32_e32 v126, s11, v125
	v_subrev_u32_e32 v134, s11, v133
	v_subrev_u32_e32 v142, s11, v141
	v_cmp_le_u32_e32 vcc, s11, v117
	v_cmp_le_u32_e64 s[0:1], s11, v125
	v_cmp_le_u32_e64 s[6:7], s11, v133
	v_cmp_le_u32_e64 s[8:9], s11, v141
	v_cndmask_b32_e32 v117, v117, v118, vcc
	v_cndmask_b32_e64 v125, v125, v126, s[0:1]
	v_cndmask_b32_e64 v133, v133, v134, s[6:7]
	v_cndmask_b32_e64 v141, v141, v142, s[8:9]
	v_subrev_u32_e32 v118, s11, v117
	v_subrev_u32_e32 v126, s11, v125
	v_subrev_u32_e32 v134, s11, v133
	v_subrev_u32_e32 v142, s11, v141
	v_cmp_le_u32_e32 vcc, s11, v117
	v_cmp_le_u32_e64 s[0:1], s11, v125
	v_cmp_le_u32_e64 s[6:7], s11, v133
	v_cmp_le_u32_e64 s[8:9], s11, v141
	v_cndmask_b32_e32 v117, v117, v118, vcc
	v_cndmask_b32_e64 v125, v125, v126, s[0:1]
	v_cndmask_b32_e64 v133, v133, v134, s[6:7]
	v_cndmask_b32_e64 v141, v141, v142, s[8:9]
	v_ashrrev_i32_e32 v116, 8, v60
	v_ashrrev_i32_e32 v124, 8, v61
	v_ashrrev_i32_e32 v132, 8, v62
	v_ashrrev_i32_e32 v140, 8, v63
	s_waitcnt lgkmcnt(0)
	v_add_u32_e32 v116, v116, v113
	v_add_u32_e32 v124, v124, v121
	v_add_u32_e32 v132, v132, v129
	v_add_u32_e32 v140, v140, v137
	v_add3_u32 v116, v116, v114, v115
	v_add3_u32 v124, v124, v122, v123
	v_add3_u32 v132, v132, v130, v131
	v_add3_u32 v140, v140, v138, v139
	v_cmp_eq_u32_e32 vcc, s93, v117
	v_add_u32_e32 v1, 0xa000, v10
	s_and_saveexec_b64 s[24:25], vcc
	global_store_dword v1, v116, s[16:17]
	s_mov_b64 exec, s[24:25]
	v_cmp_eq_u32_e32 vcc, s93, v125
	v_add_u32_e32 v1, 0xa800, v10
	s_and_saveexec_b64 s[24:25], vcc
	global_store_dword v1, v124, s[16:17]
	s_mov_b64 exec, s[24:25]
	v_cmp_eq_u32_e32 vcc, s93, v133
	v_add_u32_e32 v1, 0xb000, v10
	s_and_saveexec_b64 s[24:25], vcc
	global_store_dword v1, v132, s[16:17]
	s_mov_b64 exec, s[24:25]
	v_cmp_eq_u32_e32 vcc, s93, v141
	v_add_u32_e32 v1, 0xb800, v10
	s_and_saveexec_b64 s[24:25], vcc
	global_store_dword v1, v140, s[16:17]
	s_mov_b64 exec, s[24:25]
	v_ashrrev_i32_e32 v113, 8, v116
	v_ashrrev_i32_e32 v121, 8, v124
	v_ashrrev_i32_e32 v129, 8, v132
	v_ashrrev_i32_e32 v137, 8, v140
	v_and_b32_e32 v112, 0xff, v116
	v_and_b32_e32 v120, 0xff, v124
	v_and_b32_e32 v128, 0xff, v132
	v_and_b32_e32 v136, 0xff, v140
	v_lshl_add_u32 v112, v112, 2, s10
	v_lshl_add_u32 v120, v120, 2, s10
	v_lshl_add_u32 v128, v128, 2, s10
	v_lshl_add_u32 v136, v136, 2, s10
	v_add_u32_e32 v114, 0x1400, v34
	v_add_u32_e32 v122, 0x1500, v34
	v_add_u32_e32 v130, 0x1600, v34
	v_add_u32_e32 v138, 0x1700, v34
	v_mov_b32_e32 v119, -1
	v_mov_b32_e32 v127, -1
	v_mov_b32_e32 v135, -1
	v_mov_b32_e32 v143, -1
	v_cmp_eq_u32_e32 vcc, v113, v2
	v_cmp_eq_u32_e64 s[0:1], v121, v2
	v_cmp_eq_u32_e64 s[6:7], v129, v2
	v_cmp_eq_u32_e64 s[8:9], v137, v2
	v_cndmask_b32_e32 v119, v119, v104, vcc
	v_cndmask_b32_e64 v127, v127, v104, s[0:1]
	v_cndmask_b32_e64 v135, v135, v104, s[6:7]
	v_cndmask_b32_e64 v143, v143, v104, s[8:9]
	v_cmp_eq_u32_e32 vcc, v113, v3
	v_cmp_eq_u32_e64 s[0:1], v121, v3
	v_cmp_eq_u32_e64 s[6:7], v129, v3
	v_cmp_eq_u32_e64 s[8:9], v137, v3
	v_cndmask_b32_e32 v119, v119, v105, vcc
	v_cndmask_b32_e64 v127, v127, v105, s[0:1]
	v_cndmask_b32_e64 v135, v135, v105, s[6:7]
	v_cndmask_b32_e64 v143, v143, v105, s[8:9]
	v_cmp_eq_u32_e32 vcc, v113, v4
	v_cmp_eq_u32_e64 s[0:1], v121, v4
	v_cmp_eq_u32_e64 s[6:7], v129, v4
	v_cmp_eq_u32_e64 s[8:9], v137, v4
	v_cndmask_b32_e32 v119, v119, v106, vcc
	v_cndmask_b32_e64 v127, v127, v106, s[0:1]
	v_cndmask_b32_e64 v135, v135, v106, s[6:7]
	v_cndmask_b32_e64 v143, v143, v106, s[8:9]
	v_cmp_eq_u32_e32 vcc, v113, v5
	v_cmp_eq_u32_e64 s[0:1], v121, v5
	v_cmp_eq_u32_e64 s[6:7], v129, v5
	v_cmp_eq_u32_e64 s[8:9], v137, v5
	v_cndmask_b32_e32 v119, v119, v107, vcc
	v_cndmask_b32_e64 v127, v127, v107, s[0:1]
	v_cndmask_b32_e64 v135, v135, v107, s[6:7]
	v_cndmask_b32_e64 v143, v143, v107, s[8:9]
	v_cmp_eq_u32_e32 vcc, v113, v6
	v_cmp_eq_u32_e64 s[0:1], v121, v6
	v_cmp_eq_u32_e64 s[6:7], v129, v6
	v_cmp_eq_u32_e64 s[8:9], v137, v6
	v_cndmask_b32_e32 v119, v119, v108, vcc
	v_cndmask_b32_e64 v127, v127, v108, s[0:1]
	v_cndmask_b32_e64 v135, v135, v108, s[6:7]
	v_cndmask_b32_e64 v143, v143, v108, s[8:9]
	v_cmp_eq_u32_e32 vcc, v113, v7
	v_cmp_eq_u32_e64 s[0:1], v121, v7
	v_cmp_eq_u32_e64 s[6:7], v129, v7
	v_cmp_eq_u32_e64 s[8:9], v137, v7
	v_cndmask_b32_e32 v119, v119, v109, vcc
	v_cndmask_b32_e64 v127, v127, v109, s[0:1]
	v_cndmask_b32_e64 v135, v135, v109, s[6:7]
	v_cndmask_b32_e64 v143, v143, v109, s[8:9]
	v_cmp_eq_u32_e32 vcc, v113, v8
	v_cmp_eq_u32_e64 s[0:1], v121, v8
	v_cmp_eq_u32_e64 s[6:7], v129, v8
	v_cmp_eq_u32_e64 s[8:9], v137, v8
	v_cndmask_b32_e32 v119, v119, v110, vcc
	v_cndmask_b32_e64 v127, v127, v110, s[0:1]
	v_cndmask_b32_e64 v135, v135, v110, s[6:7]
	v_cndmask_b32_e64 v143, v143, v110, s[8:9]
	v_cmp_eq_u32_e32 vcc, v113, v9
	v_cmp_eq_u32_e64 s[0:1], v121, v9
	v_cmp_eq_u32_e64 s[6:7], v129, v9
	v_cmp_eq_u32_e64 s[8:9], v137, v9
	v_cndmask_b32_e32 v119, v119, v111, vcc
	v_cndmask_b32_e64 v127, v127, v111, s[0:1]
	v_cndmask_b32_e64 v135, v135, v111, s[6:7]
	v_cndmask_b32_e64 v143, v143, v111, s[8:9]
	v_add_u32_e32 v112, v112, v119
	v_add_u32_e32 v120, v120, v127
	v_add_u32_e32 v128, v128, v135
	v_add_u32_e32 v136, v136, v143
	v_cmp_ne_u32_e32 vcc, -1, v119
	s_and_saveexec_b64 s[24:25], vcc
	ds_write_b32 v112, v114
	s_mov_b64 exec, s[24:25]
	v_cmp_ne_u32_e32 vcc, -1, v127
	s_and_saveexec_b64 s[24:25], vcc
	ds_write_b32 v120, v122
	s_mov_b64 exec, s[24:25]
	v_cmp_ne_u32_e32 vcc, -1, v135
	s_and_saveexec_b64 s[24:25], vcc
	ds_write_b32 v128, v130
	s_mov_b64 exec, s[24:25]
	v_cmp_ne_u32_e32 vcc, -1, v143
	s_and_saveexec_b64 s[24:25], vcc
	ds_write_b32 v136, v138
	s_mov_b64 exec, s[24:25]
	v_and_b32_e32 v112, 0xff, v64
	v_and_b32_e32 v120, 0xff, v65
	v_and_b32_e32 v128, 0xff, v66
	v_and_b32_e32 v136, 0xff, v67
	v_lshlrev_b32_e32 v112, 2, v112
	v_lshlrev_b32_e32 v120, 2, v120
	v_lshlrev_b32_e32 v128, 2, v128
	v_lshlrev_b32_e32 v136, 2, v136
	v_add_u32_e32 v118, v112, v11
	v_add_u32_e32 v126, v120, v11
	v_add_u32_e32 v134, v128, v11
	v_add_u32_e32 v142, v136, v11
	ds_read_b32 v113, v112 offset:36864
	ds_read_b32 v114, v112 offset:35584
	ds_read_b32 v115, v118 offset:12288
	ds_read_b32 v121, v120 offset:36864
	ds_read_b32 v122, v120 offset:35584
	ds_read_b32 v123, v126 offset:12800
	ds_read_b32 v129, v128 offset:36864
	ds_read_b32 v130, v128 offset:35584
	ds_read_b32 v131, v134 offset:13312
	ds_read_b32 v137, v136 offset:36864
	ds_read_b32 v138, v136 offset:35584
	ds_read_b32 v139, v142 offset:13824
	v_add_u32_e32 v117, 96, v36
	v_add_u32_e32 v125, 100, v36
	v_add_u32_e32 v133, 104, v36
	v_add_u32_e32 v141, 108, v36
	v_mul_hi_u32 v118, v117, v15
	v_mul_hi_u32 v126, v125, v15
	v_mul_hi_u32 v134, v133, v15
	v_mul_hi_u32 v142, v141, v15
	v_mul_lo_u32 v118, v118, s11
	v_mul_lo_u32 v126, v126, s11
	v_mul_lo_u32 v134, v134, s11
	v_mul_lo_u32 v142, v142, s11
	v_sub_u32_e32 v117, v117, v118
	v_sub_u32_e32 v125, v125, v126
	v_sub_u32_e32 v133, v133, v134
	v_sub_u32_e32 v141, v141, v142
	v_subrev_u32_e32 v118, s11, v117
	v_subrev_u32_e32 v126, s11, v125
	v_subrev_u32_e32 v134, s11, v133
	v_subrev_u32_e32 v142, s11, v141
	v_cmp_le_u32_e32 vcc, s11, v117
	v_cmp_le_u32_e64 s[0:1], s11, v125
	v_cmp_le_u32_e64 s[6:7], s11, v133
	v_cmp_le_u32_e64 s[8:9], s11, v141
	v_cndmask_b32_e32 v117, v117, v118, vcc
	v_cndmask_b32_e64 v125, v125, v126, s[0:1]
	v_cndmask_b32_e64 v133, v133, v134, s[6:7]
	v_cndmask_b32_e64 v141, v141, v142, s[8:9]
	v_subrev_u32_e32 v118, s11, v117
	v_subrev_u32_e32 v126, s11, v125
	v_subrev_u32_e32 v134, s11, v133
	v_subrev_u32_e32 v142, s11, v141
	v_cmp_le_u32_e32 vcc, s11, v117
	v_cmp_le_u32_e64 s[0:1], s11, v125
	v_cmp_le_u32_e64 s[6:7], s11, v133
	v_cmp_le_u32_e64 s[8:9], s11, v141
	v_cndmask_b32_e32 v117, v117, v118, vcc
	v_cndmask_b32_e64 v125, v125, v126, s[0:1]
	v_cndmask_b32_e64 v133, v133, v134, s[6:7]
	v_cndmask_b32_e64 v141, v141, v142, s[8:9]
	v_ashrrev_i32_e32 v116, 8, v64
	v_ashrrev_i32_e32 v124, 8, v65
	v_ashrrev_i32_e32 v132, 8, v66
	v_ashrrev_i32_e32 v140, 8, v67
	s_waitcnt lgkmcnt(0)
	v_add_u32_e32 v116, v116, v113
	v_add_u32_e32 v124, v124, v121
	v_add_u32_e32 v132, v132, v129
	v_add_u32_e32 v140, v140, v137
	v_add3_u32 v116, v116, v114, v115
	v_add3_u32 v124, v124, v122, v123
	v_add3_u32 v132, v132, v130, v131
	v_add3_u32 v140, v140, v138, v139
	v_cmp_eq_u32_e32 vcc, s93, v117
	v_add_u32_e32 v1, 0xc000, v10
	s_and_saveexec_b64 s[24:25], vcc
	global_store_dword v1, v116, s[16:17]
	s_mov_b64 exec, s[24:25]
	v_cmp_eq_u32_e32 vcc, s93, v125
	v_add_u32_e32 v1, 0xc800, v10
	s_and_saveexec_b64 s[24:25], vcc
	global_store_dword v1, v124, s[16:17]
	s_mov_b64 exec, s[24:25]
	v_cmp_eq_u32_e32 vcc, s93, v133
	v_add_u32_e32 v1, 0xd000, v10
	s_and_saveexec_b64 s[24:25], vcc
	global_store_dword v1, v132, s[16:17]
	s_mov_b64 exec, s[24:25]
	v_cmp_eq_u32_e32 vcc, s93, v141
	v_add_u32_e32 v1, 0xd800, v10
	s_and_saveexec_b64 s[24:25], vcc
	global_store_dword v1, v140, s[16:17]
	s_mov_b64 exec, s[24:25]
	v_ashrrev_i32_e32 v113, 8, v116
	v_ashrrev_i32_e32 v121, 8, v124
	v_ashrrev_i32_e32 v129, 8, v132
	v_ashrrev_i32_e32 v137, 8, v140
	v_and_b32_e32 v112, 0xff, v116
	v_and_b32_e32 v120, 0xff, v124
	v_and_b32_e32 v128, 0xff, v132
	v_and_b32_e32 v136, 0xff, v140
	v_lshl_add_u32 v112, v112, 2, s10
	v_lshl_add_u32 v120, v120, 2, s10
	v_lshl_add_u32 v128, v128, 2, s10
	v_lshl_add_u32 v136, v136, 2, s10
	v_add_u32_e32 v114, 0x1800, v34
	v_add_u32_e32 v122, 0x1900, v34
	v_add_u32_e32 v130, 0x1a00, v34
	v_add_u32_e32 v138, 0x1b00, v34
	v_mov_b32_e32 v119, -1
	v_mov_b32_e32 v127, -1
	v_mov_b32_e32 v135, -1
	v_mov_b32_e32 v143, -1
	v_cmp_eq_u32_e32 vcc, v113, v2
	v_cmp_eq_u32_e64 s[0:1], v121, v2
	v_cmp_eq_u32_e64 s[6:7], v129, v2
	v_cmp_eq_u32_e64 s[8:9], v137, v2
	v_cndmask_b32_e32 v119, v119, v104, vcc
	v_cndmask_b32_e64 v127, v127, v104, s[0:1]
	v_cndmask_b32_e64 v135, v135, v104, s[6:7]
	v_cndmask_b32_e64 v143, v143, v104, s[8:9]
	v_cmp_eq_u32_e32 vcc, v113, v3
	v_cmp_eq_u32_e64 s[0:1], v121, v3
	v_cmp_eq_u32_e64 s[6:7], v129, v3
	v_cmp_eq_u32_e64 s[8:9], v137, v3
	v_cndmask_b32_e32 v119, v119, v105, vcc
	v_cndmask_b32_e64 v127, v127, v105, s[0:1]
	v_cndmask_b32_e64 v135, v135, v105, s[6:7]
	v_cndmask_b32_e64 v143, v143, v105, s[8:9]
	v_cmp_eq_u32_e32 vcc, v113, v4
	v_cmp_eq_u32_e64 s[0:1], v121, v4
	v_cmp_eq_u32_e64 s[6:7], v129, v4
	v_cmp_eq_u32_e64 s[8:9], v137, v4
	v_cndmask_b32_e32 v119, v119, v106, vcc
	v_cndmask_b32_e64 v127, v127, v106, s[0:1]
	v_cndmask_b32_e64 v135, v135, v106, s[6:7]
	v_cndmask_b32_e64 v143, v143, v106, s[8:9]
	v_cmp_eq_u32_e32 vcc, v113, v5
	v_cmp_eq_u32_e64 s[0:1], v121, v5
	v_cmp_eq_u32_e64 s[6:7], v129, v5
	v_cmp_eq_u32_e64 s[8:9], v137, v5
	v_cndmask_b32_e32 v119, v119, v107, vcc
	v_cndmask_b32_e64 v127, v127, v107, s[0:1]
	v_cndmask_b32_e64 v135, v135, v107, s[6:7]
	v_cndmask_b32_e64 v143, v143, v107, s[8:9]
	v_cmp_eq_u32_e32 vcc, v113, v6
	v_cmp_eq_u32_e64 s[0:1], v121, v6
	v_cmp_eq_u32_e64 s[6:7], v129, v6
	v_cmp_eq_u32_e64 s[8:9], v137, v6
	v_cndmask_b32_e32 v119, v119, v108, vcc
	v_cndmask_b32_e64 v127, v127, v108, s[0:1]
	v_cndmask_b32_e64 v135, v135, v108, s[6:7]
	v_cndmask_b32_e64 v143, v143, v108, s[8:9]
	v_cmp_eq_u32_e32 vcc, v113, v7
	v_cmp_eq_u32_e64 s[0:1], v121, v7
	v_cmp_eq_u32_e64 s[6:7], v129, v7
	v_cmp_eq_u32_e64 s[8:9], v137, v7
	v_cndmask_b32_e32 v119, v119, v109, vcc
	v_cndmask_b32_e64 v127, v127, v109, s[0:1]
	v_cndmask_b32_e64 v135, v135, v109, s[6:7]
	v_cndmask_b32_e64 v143, v143, v109, s[8:9]
	v_cmp_eq_u32_e32 vcc, v113, v8
	v_cmp_eq_u32_e64 s[0:1], v121, v8
	v_cmp_eq_u32_e64 s[6:7], v129, v8
	v_cmp_eq_u32_e64 s[8:9], v137, v8
	v_cndmask_b32_e32 v119, v119, v110, vcc
	v_cndmask_b32_e64 v127, v127, v110, s[0:1]
	v_cndmask_b32_e64 v135, v135, v110, s[6:7]
	v_cndmask_b32_e64 v143, v143, v110, s[8:9]
	v_cmp_eq_u32_e32 vcc, v113, v9
	v_cmp_eq_u32_e64 s[0:1], v121, v9
	v_cmp_eq_u32_e64 s[6:7], v129, v9
	v_cmp_eq_u32_e64 s[8:9], v137, v9
	v_cndmask_b32_e32 v119, v119, v111, vcc
	v_cndmask_b32_e64 v127, v127, v111, s[0:1]
	v_cndmask_b32_e64 v135, v135, v111, s[6:7]
	v_cndmask_b32_e64 v143, v143, v111, s[8:9]
	v_add_u32_e32 v112, v112, v119
	v_add_u32_e32 v120, v120, v127
	v_add_u32_e32 v128, v128, v135
	v_add_u32_e32 v136, v136, v143
	v_cmp_ne_u32_e32 vcc, -1, v119
	s_and_saveexec_b64 s[24:25], vcc
	ds_write_b32 v112, v114
	s_mov_b64 exec, s[24:25]
	v_cmp_ne_u32_e32 vcc, -1, v127
	s_and_saveexec_b64 s[24:25], vcc
	ds_write_b32 v120, v122
	s_mov_b64 exec, s[24:25]
	v_cmp_ne_u32_e32 vcc, -1, v135
	s_and_saveexec_b64 s[24:25], vcc
	ds_write_b32 v128, v130
	s_mov_b64 exec, s[24:25]
	v_cmp_ne_u32_e32 vcc, -1, v143
	s_and_saveexec_b64 s[24:25], vcc
	ds_write_b32 v136, v138
	s_mov_b64 exec, s[24:25]
	v_and_b32_e32 v112, 0xff, v68
	v_and_b32_e32 v120, 0xff, v69
	v_and_b32_e32 v128, 0xff, v70
	v_and_b32_e32 v136, 0xff, v71
	v_lshlrev_b32_e32 v112, 2, v112
	v_lshlrev_b32_e32 v120, 2, v120
	v_lshlrev_b32_e32 v128, 2, v128
	v_lshlrev_b32_e32 v136, 2, v136
	v_add_u32_e32 v118, v112, v11
	v_add_u32_e32 v126, v120, v11
	v_add_u32_e32 v134, v128, v11
	v_add_u32_e32 v142, v136, v11
	ds_read_b32 v113, v112 offset:36864
	ds_read_b32 v114, v112 offset:35712
	ds_read_b32 v115, v118 offset:14336
	ds_read_b32 v121, v120 offset:36864
	ds_read_b32 v122, v120 offset:35712
	ds_read_b32 v123, v126 offset:14848
	ds_read_b32 v129, v128 offset:36864
	ds_read_b32 v130, v128 offset:35712
	ds_read_b32 v131, v134 offset:15360
	ds_read_b32 v137, v136 offset:36864
	ds_read_b32 v138, v136 offset:35712
	ds_read_b32 v139, v142 offset:15872
	v_add_u32_e32 v117, 112, v36
	v_add_u32_e32 v125, 116, v36
	v_add_u32_e32 v133, 120, v36
	v_add_u32_e32 v141, 124, v36
	v_mul_hi_u32 v118, v117, v15
	v_mul_hi_u32 v126, v125, v15
	v_mul_hi_u32 v134, v133, v15
	v_mul_hi_u32 v142, v141, v15
	v_mul_lo_u32 v118, v118, s11
	v_mul_lo_u32 v126, v126, s11
	v_mul_lo_u32 v134, v134, s11
	v_mul_lo_u32 v142, v142, s11
	v_sub_u32_e32 v117, v117, v118
	v_sub_u32_e32 v125, v125, v126
	v_sub_u32_e32 v133, v133, v134
	v_sub_u32_e32 v141, v141, v142
	v_subrev_u32_e32 v118, s11, v117
	v_subrev_u32_e32 v126, s11, v125
	v_subrev_u32_e32 v134, s11, v133
	v_subrev_u32_e32 v142, s11, v141
	v_cmp_le_u32_e32 vcc, s11, v117
	v_cmp_le_u32_e64 s[0:1], s11, v125
	v_cmp_le_u32_e64 s[6:7], s11, v133
	v_cmp_le_u32_e64 s[8:9], s11, v141
	v_cndmask_b32_e32 v117, v117, v118, vcc
	v_cndmask_b32_e64 v125, v125, v126, s[0:1]
	v_cndmask_b32_e64 v133, v133, v134, s[6:7]
	v_cndmask_b32_e64 v141, v141, v142, s[8:9]
	v_subrev_u32_e32 v118, s11, v117
	v_subrev_u32_e32 v126, s11, v125
	v_subrev_u32_e32 v134, s11, v133
	v_subrev_u32_e32 v142, s11, v141
	v_cmp_le_u32_e32 vcc, s11, v117
	v_cmp_le_u32_e64 s[0:1], s11, v125
	v_cmp_le_u32_e64 s[6:7], s11, v133
	v_cmp_le_u32_e64 s[8:9], s11, v141
	v_cndmask_b32_e32 v117, v117, v118, vcc
	v_cndmask_b32_e64 v125, v125, v126, s[0:1]
	v_cndmask_b32_e64 v133, v133, v134, s[6:7]
	v_cndmask_b32_e64 v141, v141, v142, s[8:9]
	v_ashrrev_i32_e32 v116, 8, v68
	v_ashrrev_i32_e32 v124, 8, v69
	v_ashrrev_i32_e32 v132, 8, v70
	v_ashrrev_i32_e32 v140, 8, v71
	s_waitcnt lgkmcnt(0)
	v_add_u32_e32 v116, v116, v113
	v_add_u32_e32 v124, v124, v121
	v_add_u32_e32 v132, v132, v129
	v_add_u32_e32 v140, v140, v137
	v_add3_u32 v116, v116, v114, v115
	v_add3_u32 v124, v124, v122, v123
	v_add3_u32 v132, v132, v130, v131
	v_add3_u32 v140, v140, v138, v139
	v_cmp_eq_u32_e32 vcc, s93, v117
	v_add_u32_e32 v1, 0xe000, v10
	s_and_saveexec_b64 s[24:25], vcc
	global_store_dword v1, v116, s[16:17]
	s_mov_b64 exec, s[24:25]
	v_cmp_eq_u32_e32 vcc, s93, v125
	v_add_u32_e32 v1, 0xe800, v10
	s_and_saveexec_b64 s[24:25], vcc
	global_store_dword v1, v124, s[16:17]
	s_mov_b64 exec, s[24:25]
	v_cmp_eq_u32_e32 vcc, s93, v133
	v_add_u32_e32 v1, 0xf000, v10
	s_and_saveexec_b64 s[24:25], vcc
	global_store_dword v1, v132, s[16:17]
	s_mov_b64 exec, s[24:25]
	v_cmp_eq_u32_e32 vcc, s93, v141
	v_add_u32_e32 v1, 0xf800, v10
	s_and_saveexec_b64 s[24:25], vcc
	global_store_dword v1, v140, s[16:17]
	s_mov_b64 exec, s[24:25]
	v_ashrrev_i32_e32 v113, 8, v116
	v_ashrrev_i32_e32 v121, 8, v124
	v_ashrrev_i32_e32 v129, 8, v132
	v_ashrrev_i32_e32 v137, 8, v140
	v_and_b32_e32 v112, 0xff, v116
	v_and_b32_e32 v120, 0xff, v124
	v_and_b32_e32 v128, 0xff, v132
	v_and_b32_e32 v136, 0xff, v140
	v_lshl_add_u32 v112, v112, 2, s10
	v_lshl_add_u32 v120, v120, 2, s10
	v_lshl_add_u32 v128, v128, 2, s10
	v_lshl_add_u32 v136, v136, 2, s10
	v_add_u32_e32 v114, 0x1c00, v34
	v_add_u32_e32 v122, 0x1d00, v34
	v_add_u32_e32 v130, 0x1e00, v34
	v_add_u32_e32 v138, 0x1f00, v34
	v_mov_b32_e32 v119, -1
	v_mov_b32_e32 v127, -1
	v_mov_b32_e32 v135, -1
	v_mov_b32_e32 v143, -1
	v_cmp_eq_u32_e32 vcc, v113, v2
	v_cmp_eq_u32_e64 s[0:1], v121, v2
	v_cmp_eq_u32_e64 s[6:7], v129, v2
	v_cmp_eq_u32_e64 s[8:9], v137, v2
	v_cndmask_b32_e32 v119, v119, v104, vcc
	v_cndmask_b32_e64 v127, v127, v104, s[0:1]
	v_cndmask_b32_e64 v135, v135, v104, s[6:7]
	v_cndmask_b32_e64 v143, v143, v104, s[8:9]
	v_cmp_eq_u32_e32 vcc, v113, v3
	v_cmp_eq_u32_e64 s[0:1], v121, v3
	v_cmp_eq_u32_e64 s[6:7], v129, v3
	v_cmp_eq_u32_e64 s[8:9], v137, v3
	v_cndmask_b32_e32 v119, v119, v105, vcc
	v_cndmask_b32_e64 v127, v127, v105, s[0:1]
	v_cndmask_b32_e64 v135, v135, v105, s[6:7]
	v_cndmask_b32_e64 v143, v143, v105, s[8:9]
	v_cmp_eq_u32_e32 vcc, v113, v4
	v_cmp_eq_u32_e64 s[0:1], v121, v4
	v_cmp_eq_u32_e64 s[6:7], v129, v4
	v_cmp_eq_u32_e64 s[8:9], v137, v4
	v_cndmask_b32_e32 v119, v119, v106, vcc
	v_cndmask_b32_e64 v127, v127, v106, s[0:1]
	v_cndmask_b32_e64 v135, v135, v106, s[6:7]
	v_cndmask_b32_e64 v143, v143, v106, s[8:9]
	v_cmp_eq_u32_e32 vcc, v113, v5
	v_cmp_eq_u32_e64 s[0:1], v121, v5
	v_cmp_eq_u32_e64 s[6:7], v129, v5
	v_cmp_eq_u32_e64 s[8:9], v137, v5
	v_cndmask_b32_e32 v119, v119, v107, vcc
	v_cndmask_b32_e64 v127, v127, v107, s[0:1]
	v_cndmask_b32_e64 v135, v135, v107, s[6:7]
	v_cndmask_b32_e64 v143, v143, v107, s[8:9]
	v_cmp_eq_u32_e32 vcc, v113, v6
	v_cmp_eq_u32_e64 s[0:1], v121, v6
	v_cmp_eq_u32_e64 s[6:7], v129, v6
	v_cmp_eq_u32_e64 s[8:9], v137, v6
	v_cndmask_b32_e32 v119, v119, v108, vcc
	v_cndmask_b32_e64 v127, v127, v108, s[0:1]
	v_cndmask_b32_e64 v135, v135, v108, s[6:7]
	v_cndmask_b32_e64 v143, v143, v108, s[8:9]
	v_cmp_eq_u32_e32 vcc, v113, v7
	v_cmp_eq_u32_e64 s[0:1], v121, v7
	v_cmp_eq_u32_e64 s[6:7], v129, v7
	v_cmp_eq_u32_e64 s[8:9], v137, v7
	v_cndmask_b32_e32 v119, v119, v109, vcc
	v_cndmask_b32_e64 v127, v127, v109, s[0:1]
	v_cndmask_b32_e64 v135, v135, v109, s[6:7]
	v_cndmask_b32_e64 v143, v143, v109, s[8:9]
	v_cmp_eq_u32_e32 vcc, v113, v8
	v_cmp_eq_u32_e64 s[0:1], v121, v8
	v_cmp_eq_u32_e64 s[6:7], v129, v8
	v_cmp_eq_u32_e64 s[8:9], v137, v8
	v_cndmask_b32_e32 v119, v119, v110, vcc
	v_cndmask_b32_e64 v127, v127, v110, s[0:1]
	v_cndmask_b32_e64 v135, v135, v110, s[6:7]
	v_cndmask_b32_e64 v143, v143, v110, s[8:9]
	v_cmp_eq_u32_e32 vcc, v113, v9
	v_cmp_eq_u32_e64 s[0:1], v121, v9
	v_cmp_eq_u32_e64 s[6:7], v129, v9
	v_cmp_eq_u32_e64 s[8:9], v137, v9
	v_cndmask_b32_e32 v119, v119, v111, vcc
	v_cndmask_b32_e64 v127, v127, v111, s[0:1]
	v_cndmask_b32_e64 v135, v135, v111, s[6:7]
	v_cndmask_b32_e64 v143, v143, v111, s[8:9]
	v_add_u32_e32 v112, v112, v119
	v_add_u32_e32 v120, v120, v127
	v_add_u32_e32 v128, v128, v135
	v_add_u32_e32 v136, v136, v143
	v_cmp_ne_u32_e32 vcc, -1, v119
	s_and_saveexec_b64 s[24:25], vcc
	ds_write_b32 v112, v114
	s_mov_b64 exec, s[24:25]
	v_cmp_ne_u32_e32 vcc, -1, v127
	s_and_saveexec_b64 s[24:25], vcc
	ds_write_b32 v120, v122
	s_mov_b64 exec, s[24:25]
	v_cmp_ne_u32_e32 vcc, -1, v135
	s_and_saveexec_b64 s[24:25], vcc
	ds_write_b32 v128, v130
	s_mov_b64 exec, s[24:25]
	v_cmp_ne_u32_e32 vcc, -1, v143
	s_and_saveexec_b64 s[24:25], vcc
	ds_write_b32 v136, v138
	s_mov_b64 exec, s[24:25]
	v_and_b32_e32 v112, 0xff, v72
	v_and_b32_e32 v120, 0xff, v73
	v_and_b32_e32 v128, 0xff, v74
	v_and_b32_e32 v136, 0xff, v75
	v_lshlrev_b32_e32 v112, 2, v112
	v_lshlrev_b32_e32 v120, 2, v120
	v_lshlrev_b32_e32 v128, 2, v128
	v_lshlrev_b32_e32 v136, 2, v136
	v_add_u32_e32 v118, v112, v11
	v_add_u32_e32 v126, v120, v11
	v_add_u32_e32 v134, v128, v11
	v_add_u32_e32 v142, v136, v11
	ds_read_b32 v113, v112 offset:36864
	ds_read_b32 v114, v112 offset:35840
	ds_read_b32 v115, v118 offset:16384
	ds_read_b32 v121, v120 offset:36864
	ds_read_b32 v122, v120 offset:35840
	ds_read_b32 v123, v126 offset:16896
	ds_read_b32 v129, v128 offset:36864
	ds_read_b32 v130, v128 offset:35840
	ds_read_b32 v131, v134 offset:17408
	ds_read_b32 v137, v136 offset:36864
	ds_read_b32 v138, v136 offset:35840
	ds_read_b32 v139, v142 offset:17920
	v_add_u32_e32 v117, 128, v36
	v_add_u32_e32 v125, 132, v36
	v_add_u32_e32 v133, 136, v36
	v_add_u32_e32 v141, 140, v36
	v_mul_hi_u32 v118, v117, v15
	v_mul_hi_u32 v126, v125, v15
	v_mul_hi_u32 v134, v133, v15
	v_mul_hi_u32 v142, v141, v15
	v_mul_lo_u32 v118, v118, s11
	v_mul_lo_u32 v126, v126, s11
	v_mul_lo_u32 v134, v134, s11
	v_mul_lo_u32 v142, v142, s11
	v_sub_u32_e32 v117, v117, v118
	v_sub_u32_e32 v125, v125, v126
	v_sub_u32_e32 v133, v133, v134
	v_sub_u32_e32 v141, v141, v142
	v_subrev_u32_e32 v118, s11, v117
	v_subrev_u32_e32 v126, s11, v125
	v_subrev_u32_e32 v134, s11, v133
	v_subrev_u32_e32 v142, s11, v141
	v_cmp_le_u32_e32 vcc, s11, v117
	v_cmp_le_u32_e64 s[0:1], s11, v125
	v_cmp_le_u32_e64 s[6:7], s11, v133
	v_cmp_le_u32_e64 s[8:9], s11, v141
	v_cndmask_b32_e32 v117, v117, v118, vcc
	v_cndmask_b32_e64 v125, v125, v126, s[0:1]
	v_cndmask_b32_e64 v133, v133, v134, s[6:7]
	v_cndmask_b32_e64 v141, v141, v142, s[8:9]
	v_subrev_u32_e32 v118, s11, v117
	v_subrev_u32_e32 v126, s11, v125
	v_subrev_u32_e32 v134, s11, v133
	v_subrev_u32_e32 v142, s11, v141
	v_cmp_le_u32_e32 vcc, s11, v117
	v_cmp_le_u32_e64 s[0:1], s11, v125
	v_cmp_le_u32_e64 s[6:7], s11, v133
	v_cmp_le_u32_e64 s[8:9], s11, v141
	v_cndmask_b32_e32 v117, v117, v118, vcc
	v_cndmask_b32_e64 v125, v125, v126, s[0:1]
	v_cndmask_b32_e64 v133, v133, v134, s[6:7]
	v_cndmask_b32_e64 v141, v141, v142, s[8:9]
	v_ashrrev_i32_e32 v116, 8, v72
	v_ashrrev_i32_e32 v124, 8, v73
	v_ashrrev_i32_e32 v132, 8, v74
	v_ashrrev_i32_e32 v140, 8, v75
	s_waitcnt lgkmcnt(0)
	v_add_u32_e32 v116, v116, v113
	v_add_u32_e32 v124, v124, v121
	v_add_u32_e32 v132, v132, v129
	v_add_u32_e32 v140, v140, v137
	v_add3_u32 v116, v116, v114, v115
	v_add3_u32 v124, v124, v122, v123
	v_add3_u32 v132, v132, v130, v131
	v_add3_u32 v140, v140, v138, v139
	v_cmp_eq_u32_e32 vcc, s93, v117
	v_add_u32_e32 v1, 0x10000, v10
	s_and_saveexec_b64 s[24:25], vcc
	global_store_dword v1, v116, s[16:17]
	s_mov_b64 exec, s[24:25]
	v_cmp_eq_u32_e32 vcc, s93, v125
	v_add_u32_e32 v1, 0x10800, v10
	s_and_saveexec_b64 s[24:25], vcc
	global_store_dword v1, v124, s[16:17]
	s_mov_b64 exec, s[24:25]
	v_cmp_eq_u32_e32 vcc, s93, v133
	v_add_u32_e32 v1, 0x11000, v10
	s_and_saveexec_b64 s[24:25], vcc
	global_store_dword v1, v132, s[16:17]
	s_mov_b64 exec, s[24:25]
	v_cmp_eq_u32_e32 vcc, s93, v141
	v_add_u32_e32 v1, 0x11800, v10
	s_and_saveexec_b64 s[24:25], vcc
	global_store_dword v1, v140, s[16:17]
	s_mov_b64 exec, s[24:25]
	v_ashrrev_i32_e32 v113, 8, v116
	v_ashrrev_i32_e32 v121, 8, v124
	v_ashrrev_i32_e32 v129, 8, v132
	v_ashrrev_i32_e32 v137, 8, v140
	v_and_b32_e32 v112, 0xff, v116
	v_and_b32_e32 v120, 0xff, v124
	v_and_b32_e32 v128, 0xff, v132
	v_and_b32_e32 v136, 0xff, v140
	v_lshl_add_u32 v112, v112, 2, s10
	v_lshl_add_u32 v120, v120, 2, s10
	v_lshl_add_u32 v128, v128, 2, s10
	v_lshl_add_u32 v136, v136, 2, s10
	v_add_u32_e32 v114, 0x2000, v34
	v_add_u32_e32 v122, 0x2100, v34
	v_add_u32_e32 v130, 0x2200, v34
	v_add_u32_e32 v138, 0x2300, v34
	v_mov_b32_e32 v119, -1
	v_mov_b32_e32 v127, -1
	v_mov_b32_e32 v135, -1
	v_mov_b32_e32 v143, -1
	v_cmp_eq_u32_e32 vcc, v113, v2
	v_cmp_eq_u32_e64 s[0:1], v121, v2
	v_cmp_eq_u32_e64 s[6:7], v129, v2
	v_cmp_eq_u32_e64 s[8:9], v137, v2
	v_cndmask_b32_e32 v119, v119, v104, vcc
	v_cndmask_b32_e64 v127, v127, v104, s[0:1]
	v_cndmask_b32_e64 v135, v135, v104, s[6:7]
	v_cndmask_b32_e64 v143, v143, v104, s[8:9]
	v_cmp_eq_u32_e32 vcc, v113, v3
	v_cmp_eq_u32_e64 s[0:1], v121, v3
	v_cmp_eq_u32_e64 s[6:7], v129, v3
	v_cmp_eq_u32_e64 s[8:9], v137, v3
	v_cndmask_b32_e32 v119, v119, v105, vcc
	v_cndmask_b32_e64 v127, v127, v105, s[0:1]
	v_cndmask_b32_e64 v135, v135, v105, s[6:7]
	v_cndmask_b32_e64 v143, v143, v105, s[8:9]
	v_cmp_eq_u32_e32 vcc, v113, v4
	v_cmp_eq_u32_e64 s[0:1], v121, v4
	v_cmp_eq_u32_e64 s[6:7], v129, v4
	v_cmp_eq_u32_e64 s[8:9], v137, v4
	v_cndmask_b32_e32 v119, v119, v106, vcc
	v_cndmask_b32_e64 v127, v127, v106, s[0:1]
	v_cndmask_b32_e64 v135, v135, v106, s[6:7]
	v_cndmask_b32_e64 v143, v143, v106, s[8:9]
	v_cmp_eq_u32_e32 vcc, v113, v5
	v_cmp_eq_u32_e64 s[0:1], v121, v5
	v_cmp_eq_u32_e64 s[6:7], v129, v5
	v_cmp_eq_u32_e64 s[8:9], v137, v5
	v_cndmask_b32_e32 v119, v119, v107, vcc
	v_cndmask_b32_e64 v127, v127, v107, s[0:1]
	v_cndmask_b32_e64 v135, v135, v107, s[6:7]
	v_cndmask_b32_e64 v143, v143, v107, s[8:9]
	v_cmp_eq_u32_e32 vcc, v113, v6
	v_cmp_eq_u32_e64 s[0:1], v121, v6
	v_cmp_eq_u32_e64 s[6:7], v129, v6
	v_cmp_eq_u32_e64 s[8:9], v137, v6
	v_cndmask_b32_e32 v119, v119, v108, vcc
	v_cndmask_b32_e64 v127, v127, v108, s[0:1]
	v_cndmask_b32_e64 v135, v135, v108, s[6:7]
	v_cndmask_b32_e64 v143, v143, v108, s[8:9]
	v_cmp_eq_u32_e32 vcc, v113, v7
	v_cmp_eq_u32_e64 s[0:1], v121, v7
	v_cmp_eq_u32_e64 s[6:7], v129, v7
	v_cmp_eq_u32_e64 s[8:9], v137, v7
	v_cndmask_b32_e32 v119, v119, v109, vcc
	v_cndmask_b32_e64 v127, v127, v109, s[0:1]
	v_cndmask_b32_e64 v135, v135, v109, s[6:7]
	v_cndmask_b32_e64 v143, v143, v109, s[8:9]
	v_cmp_eq_u32_e32 vcc, v113, v8
	v_cmp_eq_u32_e64 s[0:1], v121, v8
	v_cmp_eq_u32_e64 s[6:7], v129, v8
	v_cmp_eq_u32_e64 s[8:9], v137, v8
	v_cndmask_b32_e32 v119, v119, v110, vcc
	v_cndmask_b32_e64 v127, v127, v110, s[0:1]
	v_cndmask_b32_e64 v135, v135, v110, s[6:7]
	v_cndmask_b32_e64 v143, v143, v110, s[8:9]
	v_cmp_eq_u32_e32 vcc, v113, v9
	v_cmp_eq_u32_e64 s[0:1], v121, v9
	v_cmp_eq_u32_e64 s[6:7], v129, v9
	v_cmp_eq_u32_e64 s[8:9], v137, v9
	v_cndmask_b32_e32 v119, v119, v111, vcc
	v_cndmask_b32_e64 v127, v127, v111, s[0:1]
	v_cndmask_b32_e64 v135, v135, v111, s[6:7]
	v_cndmask_b32_e64 v143, v143, v111, s[8:9]
	v_add_u32_e32 v112, v112, v119
	v_add_u32_e32 v120, v120, v127
	v_add_u32_e32 v128, v128, v135
	v_add_u32_e32 v136, v136, v143
	v_cmp_ne_u32_e32 vcc, -1, v119
	s_and_saveexec_b64 s[24:25], vcc
	ds_write_b32 v112, v114
	s_mov_b64 exec, s[24:25]
	v_cmp_ne_u32_e32 vcc, -1, v127
	s_and_saveexec_b64 s[24:25], vcc
	ds_write_b32 v120, v122
	s_mov_b64 exec, s[24:25]
	v_cmp_ne_u32_e32 vcc, -1, v135
	s_and_saveexec_b64 s[24:25], vcc
	ds_write_b32 v128, v130
	s_mov_b64 exec, s[24:25]
	v_cmp_ne_u32_e32 vcc, -1, v143
	s_and_saveexec_b64 s[24:25], vcc
	ds_write_b32 v136, v138
	s_mov_b64 exec, s[24:25]
	v_and_b32_e32 v112, 0xff, v76
	v_and_b32_e32 v120, 0xff, v77
	v_and_b32_e32 v128, 0xff, v78
	v_and_b32_e32 v136, 0xff, v79
	v_lshlrev_b32_e32 v112, 2, v112
	v_lshlrev_b32_e32 v120, 2, v120
	v_lshlrev_b32_e32 v128, 2, v128
	v_lshlrev_b32_e32 v136, 2, v136
	v_add_u32_e32 v118, v112, v11
	v_add_u32_e32 v126, v120, v11
	v_add_u32_e32 v134, v128, v11
	v_add_u32_e32 v142, v136, v11
	ds_read_b32 v113, v112 offset:36864
	ds_read_b32 v114, v112 offset:35968
	ds_read_b32 v115, v118 offset:18432
	ds_read_b32 v121, v120 offset:36864
	ds_read_b32 v122, v120 offset:35968
	ds_read_b32 v123, v126 offset:18944
	ds_read_b32 v129, v128 offset:36864
	ds_read_b32 v130, v128 offset:35968
	ds_read_b32 v131, v134 offset:19456
	ds_read_b32 v137, v136 offset:36864
	ds_read_b32 v138, v136 offset:35968
	ds_read_b32 v139, v142 offset:19968
	v_add_u32_e32 v117, 144, v36
	v_add_u32_e32 v125, 148, v36
	v_add_u32_e32 v133, 152, v36
	v_add_u32_e32 v141, 156, v36
	v_mul_hi_u32 v118, v117, v15
	v_mul_hi_u32 v126, v125, v15
	v_mul_hi_u32 v134, v133, v15
	v_mul_hi_u32 v142, v141, v15
	v_mul_lo_u32 v118, v118, s11
	v_mul_lo_u32 v126, v126, s11
	v_mul_lo_u32 v134, v134, s11
	v_mul_lo_u32 v142, v142, s11
	v_sub_u32_e32 v117, v117, v118
	v_sub_u32_e32 v125, v125, v126
	v_sub_u32_e32 v133, v133, v134
	v_sub_u32_e32 v141, v141, v142
	v_subrev_u32_e32 v118, s11, v117
	v_subrev_u32_e32 v126, s11, v125
	v_subrev_u32_e32 v134, s11, v133
	v_subrev_u32_e32 v142, s11, v141
	v_cmp_le_u32_e32 vcc, s11, v117
	v_cmp_le_u32_e64 s[0:1], s11, v125
	v_cmp_le_u32_e64 s[6:7], s11, v133
	v_cmp_le_u32_e64 s[8:9], s11, v141
	v_cndmask_b32_e32 v117, v117, v118, vcc
	v_cndmask_b32_e64 v125, v125, v126, s[0:1]
	v_cndmask_b32_e64 v133, v133, v134, s[6:7]
	v_cndmask_b32_e64 v141, v141, v142, s[8:9]
	v_subrev_u32_e32 v118, s11, v117
	v_subrev_u32_e32 v126, s11, v125
	v_subrev_u32_e32 v134, s11, v133
	v_subrev_u32_e32 v142, s11, v141
	v_cmp_le_u32_e32 vcc, s11, v117
	v_cmp_le_u32_e64 s[0:1], s11, v125
	v_cmp_le_u32_e64 s[6:7], s11, v133
	v_cmp_le_u32_e64 s[8:9], s11, v141
	v_cndmask_b32_e32 v117, v117, v118, vcc
	v_cndmask_b32_e64 v125, v125, v126, s[0:1]
	v_cndmask_b32_e64 v133, v133, v134, s[6:7]
	v_cndmask_b32_e64 v141, v141, v142, s[8:9]
	v_ashrrev_i32_e32 v116, 8, v76
	v_ashrrev_i32_e32 v124, 8, v77
	v_ashrrev_i32_e32 v132, 8, v78
	v_ashrrev_i32_e32 v140, 8, v79
	s_waitcnt lgkmcnt(0)
	v_add_u32_e32 v116, v116, v113
	v_add_u32_e32 v124, v124, v121
	v_add_u32_e32 v132, v132, v129
	v_add_u32_e32 v140, v140, v137
	v_add3_u32 v116, v116, v114, v115
	v_add3_u32 v124, v124, v122, v123
	v_add3_u32 v132, v132, v130, v131
	v_add3_u32 v140, v140, v138, v139
	v_cmp_eq_u32_e32 vcc, s93, v117
	v_add_u32_e32 v1, 0x12000, v10
	s_and_saveexec_b64 s[24:25], vcc
	global_store_dword v1, v116, s[16:17]
	s_mov_b64 exec, s[24:25]
	v_cmp_eq_u32_e32 vcc, s93, v125
	v_add_u32_e32 v1, 0x12800, v10
	s_and_saveexec_b64 s[24:25], vcc
	global_store_dword v1, v124, s[16:17]
	s_mov_b64 exec, s[24:25]
	v_cmp_eq_u32_e32 vcc, s93, v133
	v_add_u32_e32 v1, 0x13000, v10
	s_and_saveexec_b64 s[24:25], vcc
	global_store_dword v1, v132, s[16:17]
	s_mov_b64 exec, s[24:25]
	v_cmp_eq_u32_e32 vcc, s93, v141
	v_add_u32_e32 v1, 0x13800, v10
	s_and_saveexec_b64 s[24:25], vcc
	global_store_dword v1, v140, s[16:17]
	s_mov_b64 exec, s[24:25]
	v_ashrrev_i32_e32 v113, 8, v116
	v_ashrrev_i32_e32 v121, 8, v124
	v_ashrrev_i32_e32 v129, 8, v132
	v_ashrrev_i32_e32 v137, 8, v140
	v_and_b32_e32 v112, 0xff, v116
	v_and_b32_e32 v120, 0xff, v124
	v_and_b32_e32 v128, 0xff, v132
	v_and_b32_e32 v136, 0xff, v140
	v_lshl_add_u32 v112, v112, 2, s10
	v_lshl_add_u32 v120, v120, 2, s10
	v_lshl_add_u32 v128, v128, 2, s10
	v_lshl_add_u32 v136, v136, 2, s10
	v_add_u32_e32 v114, 0x2400, v34
	v_add_u32_e32 v122, 0x2500, v34
	v_add_u32_e32 v130, 0x2600, v34
	v_add_u32_e32 v138, 0x2700, v34
	v_mov_b32_e32 v119, -1
	v_mov_b32_e32 v127, -1
	v_mov_b32_e32 v135, -1
	v_mov_b32_e32 v143, -1
	v_cmp_eq_u32_e32 vcc, v113, v2
	v_cmp_eq_u32_e64 s[0:1], v121, v2
	v_cmp_eq_u32_e64 s[6:7], v129, v2
	v_cmp_eq_u32_e64 s[8:9], v137, v2
	v_cndmask_b32_e32 v119, v119, v104, vcc
	v_cndmask_b32_e64 v127, v127, v104, s[0:1]
	v_cndmask_b32_e64 v135, v135, v104, s[6:7]
	v_cndmask_b32_e64 v143, v143, v104, s[8:9]
	v_cmp_eq_u32_e32 vcc, v113, v3
	v_cmp_eq_u32_e64 s[0:1], v121, v3
	v_cmp_eq_u32_e64 s[6:7], v129, v3
	v_cmp_eq_u32_e64 s[8:9], v137, v3
	v_cndmask_b32_e32 v119, v119, v105, vcc
	v_cndmask_b32_e64 v127, v127, v105, s[0:1]
	v_cndmask_b32_e64 v135, v135, v105, s[6:7]
	v_cndmask_b32_e64 v143, v143, v105, s[8:9]
	v_cmp_eq_u32_e32 vcc, v113, v4
	v_cmp_eq_u32_e64 s[0:1], v121, v4
	v_cmp_eq_u32_e64 s[6:7], v129, v4
	v_cmp_eq_u32_e64 s[8:9], v137, v4
	v_cndmask_b32_e32 v119, v119, v106, vcc
	v_cndmask_b32_e64 v127, v127, v106, s[0:1]
	v_cndmask_b32_e64 v135, v135, v106, s[6:7]
	v_cndmask_b32_e64 v143, v143, v106, s[8:9]
	v_cmp_eq_u32_e32 vcc, v113, v5
	v_cmp_eq_u32_e64 s[0:1], v121, v5
	v_cmp_eq_u32_e64 s[6:7], v129, v5
	v_cmp_eq_u32_e64 s[8:9], v137, v5
	v_cndmask_b32_e32 v119, v119, v107, vcc
	v_cndmask_b32_e64 v127, v127, v107, s[0:1]
	v_cndmask_b32_e64 v135, v135, v107, s[6:7]
	v_cndmask_b32_e64 v143, v143, v107, s[8:9]
	v_cmp_eq_u32_e32 vcc, v113, v6
	v_cmp_eq_u32_e64 s[0:1], v121, v6
	v_cmp_eq_u32_e64 s[6:7], v129, v6
	v_cmp_eq_u32_e64 s[8:9], v137, v6
	v_cndmask_b32_e32 v119, v119, v108, vcc
	v_cndmask_b32_e64 v127, v127, v108, s[0:1]
	v_cndmask_b32_e64 v135, v135, v108, s[6:7]
	v_cndmask_b32_e64 v143, v143, v108, s[8:9]
	v_cmp_eq_u32_e32 vcc, v113, v7
	v_cmp_eq_u32_e64 s[0:1], v121, v7
	v_cmp_eq_u32_e64 s[6:7], v129, v7
	v_cmp_eq_u32_e64 s[8:9], v137, v7
	v_cndmask_b32_e32 v119, v119, v109, vcc
	v_cndmask_b32_e64 v127, v127, v109, s[0:1]
	v_cndmask_b32_e64 v135, v135, v109, s[6:7]
	v_cndmask_b32_e64 v143, v143, v109, s[8:9]
	v_cmp_eq_u32_e32 vcc, v113, v8
	v_cmp_eq_u32_e64 s[0:1], v121, v8
	v_cmp_eq_u32_e64 s[6:7], v129, v8
	v_cmp_eq_u32_e64 s[8:9], v137, v8
	v_cndmask_b32_e32 v119, v119, v110, vcc
	v_cndmask_b32_e64 v127, v127, v110, s[0:1]
	v_cndmask_b32_e64 v135, v135, v110, s[6:7]
	v_cndmask_b32_e64 v143, v143, v110, s[8:9]
	v_cmp_eq_u32_e32 vcc, v113, v9
	v_cmp_eq_u32_e64 s[0:1], v121, v9
	v_cmp_eq_u32_e64 s[6:7], v129, v9
	v_cmp_eq_u32_e64 s[8:9], v137, v9
	v_cndmask_b32_e32 v119, v119, v111, vcc
	v_cndmask_b32_e64 v127, v127, v111, s[0:1]
	v_cndmask_b32_e64 v135, v135, v111, s[6:7]
	v_cndmask_b32_e64 v143, v143, v111, s[8:9]
	v_add_u32_e32 v112, v112, v119
	v_add_u32_e32 v120, v120, v127
	v_add_u32_e32 v128, v128, v135
	v_add_u32_e32 v136, v136, v143
	v_cmp_ne_u32_e32 vcc, -1, v119
	s_and_saveexec_b64 s[24:25], vcc
	ds_write_b32 v112, v114
	s_mov_b64 exec, s[24:25]
	v_cmp_ne_u32_e32 vcc, -1, v127
	s_and_saveexec_b64 s[24:25], vcc
	ds_write_b32 v120, v122
	s_mov_b64 exec, s[24:25]
	v_cmp_ne_u32_e32 vcc, -1, v135
	s_and_saveexec_b64 s[24:25], vcc
	ds_write_b32 v128, v130
	s_mov_b64 exec, s[24:25]
	v_cmp_ne_u32_e32 vcc, -1, v143
	s_and_saveexec_b64 s[24:25], vcc
	ds_write_b32 v136, v138
	s_mov_b64 exec, s[24:25]
	v_and_b32_e32 v112, 0xff, v80
	v_and_b32_e32 v120, 0xff, v81
	v_and_b32_e32 v128, 0xff, v82
	v_and_b32_e32 v136, 0xff, v83
	v_lshlrev_b32_e32 v112, 2, v112
	v_lshlrev_b32_e32 v120, 2, v120
	v_lshlrev_b32_e32 v128, 2, v128
	v_lshlrev_b32_e32 v136, 2, v136
	v_add_u32_e32 v118, v112, v11
	v_add_u32_e32 v126, v120, v11
	v_add_u32_e32 v134, v128, v11
	v_add_u32_e32 v142, v136, v11
	ds_read_b32 v113, v112 offset:36864
	ds_read_b32 v114, v112 offset:36096
	ds_read_b32 v115, v118 offset:20480
	ds_read_b32 v121, v120 offset:36864
	ds_read_b32 v122, v120 offset:36096
	ds_read_b32 v123, v126 offset:20992
	ds_read_b32 v129, v128 offset:36864
	ds_read_b32 v130, v128 offset:36096
	ds_read_b32 v131, v134 offset:21504
	ds_read_b32 v137, v136 offset:36864
	ds_read_b32 v138, v136 offset:36096
	ds_read_b32 v139, v142 offset:22016
	v_add_u32_e32 v117, 160, v36
	v_add_u32_e32 v125, 164, v36
	v_add_u32_e32 v133, 168, v36
	v_add_u32_e32 v141, 172, v36
	v_mul_hi_u32 v118, v117, v15
	v_mul_hi_u32 v126, v125, v15
	v_mul_hi_u32 v134, v133, v15
	v_mul_hi_u32 v142, v141, v15
	v_mul_lo_u32 v118, v118, s11
	v_mul_lo_u32 v126, v126, s11
	v_mul_lo_u32 v134, v134, s11
	v_mul_lo_u32 v142, v142, s11
	v_sub_u32_e32 v117, v117, v118
	v_sub_u32_e32 v125, v125, v126
	v_sub_u32_e32 v133, v133, v134
	v_sub_u32_e32 v141, v141, v142
	v_subrev_u32_e32 v118, s11, v117
	v_subrev_u32_e32 v126, s11, v125
	v_subrev_u32_e32 v134, s11, v133
	v_subrev_u32_e32 v142, s11, v141
	v_cmp_le_u32_e32 vcc, s11, v117
	v_cmp_le_u32_e64 s[0:1], s11, v125
	v_cmp_le_u32_e64 s[6:7], s11, v133
	v_cmp_le_u32_e64 s[8:9], s11, v141
	v_cndmask_b32_e32 v117, v117, v118, vcc
	v_cndmask_b32_e64 v125, v125, v126, s[0:1]
	v_cndmask_b32_e64 v133, v133, v134, s[6:7]
	v_cndmask_b32_e64 v141, v141, v142, s[8:9]
	v_subrev_u32_e32 v118, s11, v117
	v_subrev_u32_e32 v126, s11, v125
	v_subrev_u32_e32 v134, s11, v133
	v_subrev_u32_e32 v142, s11, v141
	v_cmp_le_u32_e32 vcc, s11, v117
	v_cmp_le_u32_e64 s[0:1], s11, v125
	v_cmp_le_u32_e64 s[6:7], s11, v133
	v_cmp_le_u32_e64 s[8:9], s11, v141
	v_cndmask_b32_e32 v117, v117, v118, vcc
	v_cndmask_b32_e64 v125, v125, v126, s[0:1]
	v_cndmask_b32_e64 v133, v133, v134, s[6:7]
	v_cndmask_b32_e64 v141, v141, v142, s[8:9]
	v_ashrrev_i32_e32 v116, 8, v80
	v_ashrrev_i32_e32 v124, 8, v81
	v_ashrrev_i32_e32 v132, 8, v82
	v_ashrrev_i32_e32 v140, 8, v83
	s_waitcnt lgkmcnt(0)
	v_add_u32_e32 v116, v116, v113
	v_add_u32_e32 v124, v124, v121
	v_add_u32_e32 v132, v132, v129
	v_add_u32_e32 v140, v140, v137
	v_add3_u32 v116, v116, v114, v115
	v_add3_u32 v124, v124, v122, v123
	v_add3_u32 v132, v132, v130, v131
	v_add3_u32 v140, v140, v138, v139
	v_cmp_eq_u32_e32 vcc, s93, v117
	v_add_u32_e32 v1, 0x14000, v10
	s_and_saveexec_b64 s[24:25], vcc
	global_store_dword v1, v116, s[16:17]
	s_mov_b64 exec, s[24:25]
	v_cmp_eq_u32_e32 vcc, s93, v125
	v_add_u32_e32 v1, 0x14800, v10
	s_and_saveexec_b64 s[24:25], vcc
	global_store_dword v1, v124, s[16:17]
	s_mov_b64 exec, s[24:25]
	v_cmp_eq_u32_e32 vcc, s93, v133
	v_add_u32_e32 v1, 0x15000, v10
	s_and_saveexec_b64 s[24:25], vcc
	global_store_dword v1, v132, s[16:17]
	s_mov_b64 exec, s[24:25]
	v_cmp_eq_u32_e32 vcc, s93, v141
	v_add_u32_e32 v1, 0x15800, v10
	s_and_saveexec_b64 s[24:25], vcc
	global_store_dword v1, v140, s[16:17]
	s_mov_b64 exec, s[24:25]
	v_ashrrev_i32_e32 v113, 8, v116
	v_ashrrev_i32_e32 v121, 8, v124
	v_ashrrev_i32_e32 v129, 8, v132
	v_ashrrev_i32_e32 v137, 8, v140
	v_and_b32_e32 v112, 0xff, v116
	v_and_b32_e32 v120, 0xff, v124
	v_and_b32_e32 v128, 0xff, v132
	v_and_b32_e32 v136, 0xff, v140
	v_lshl_add_u32 v112, v112, 2, s10
	v_lshl_add_u32 v120, v120, 2, s10
	v_lshl_add_u32 v128, v128, 2, s10
	v_lshl_add_u32 v136, v136, 2, s10
	v_add_u32_e32 v114, 0x2800, v34
	v_add_u32_e32 v122, 0x2900, v34
	v_add_u32_e32 v130, 0x2a00, v34
	v_add_u32_e32 v138, 0x2b00, v34
	v_mov_b32_e32 v119, -1
	v_mov_b32_e32 v127, -1
	v_mov_b32_e32 v135, -1
	v_mov_b32_e32 v143, -1
	v_cmp_eq_u32_e32 vcc, v113, v2
	v_cmp_eq_u32_e64 s[0:1], v121, v2
	v_cmp_eq_u32_e64 s[6:7], v129, v2
	v_cmp_eq_u32_e64 s[8:9], v137, v2
	v_cndmask_b32_e32 v119, v119, v104, vcc
	v_cndmask_b32_e64 v127, v127, v104, s[0:1]
	v_cndmask_b32_e64 v135, v135, v104, s[6:7]
	v_cndmask_b32_e64 v143, v143, v104, s[8:9]
	v_cmp_eq_u32_e32 vcc, v113, v3
	v_cmp_eq_u32_e64 s[0:1], v121, v3
	v_cmp_eq_u32_e64 s[6:7], v129, v3
	v_cmp_eq_u32_e64 s[8:9], v137, v3
	v_cndmask_b32_e32 v119, v119, v105, vcc
	v_cndmask_b32_e64 v127, v127, v105, s[0:1]
	v_cndmask_b32_e64 v135, v135, v105, s[6:7]
	v_cndmask_b32_e64 v143, v143, v105, s[8:9]
	v_cmp_eq_u32_e32 vcc, v113, v4
	v_cmp_eq_u32_e64 s[0:1], v121, v4
	v_cmp_eq_u32_e64 s[6:7], v129, v4
	v_cmp_eq_u32_e64 s[8:9], v137, v4
	v_cndmask_b32_e32 v119, v119, v106, vcc
	v_cndmask_b32_e64 v127, v127, v106, s[0:1]
	v_cndmask_b32_e64 v135, v135, v106, s[6:7]
	v_cndmask_b32_e64 v143, v143, v106, s[8:9]
	v_cmp_eq_u32_e32 vcc, v113, v5
	v_cmp_eq_u32_e64 s[0:1], v121, v5
	v_cmp_eq_u32_e64 s[6:7], v129, v5
	v_cmp_eq_u32_e64 s[8:9], v137, v5
	v_cndmask_b32_e32 v119, v119, v107, vcc
	v_cndmask_b32_e64 v127, v127, v107, s[0:1]
	v_cndmask_b32_e64 v135, v135, v107, s[6:7]
	v_cndmask_b32_e64 v143, v143, v107, s[8:9]
	v_cmp_eq_u32_e32 vcc, v113, v6
	v_cmp_eq_u32_e64 s[0:1], v121, v6
	v_cmp_eq_u32_e64 s[6:7], v129, v6
	v_cmp_eq_u32_e64 s[8:9], v137, v6
	v_cndmask_b32_e32 v119, v119, v108, vcc
	v_cndmask_b32_e64 v127, v127, v108, s[0:1]
	v_cndmask_b32_e64 v135, v135, v108, s[6:7]
	v_cndmask_b32_e64 v143, v143, v108, s[8:9]
	v_cmp_eq_u32_e32 vcc, v113, v7
	v_cmp_eq_u32_e64 s[0:1], v121, v7
	v_cmp_eq_u32_e64 s[6:7], v129, v7
	v_cmp_eq_u32_e64 s[8:9], v137, v7
	v_cndmask_b32_e32 v119, v119, v109, vcc
	v_cndmask_b32_e64 v127, v127, v109, s[0:1]
	v_cndmask_b32_e64 v135, v135, v109, s[6:7]
	v_cndmask_b32_e64 v143, v143, v109, s[8:9]
	v_cmp_eq_u32_e32 vcc, v113, v8
	v_cmp_eq_u32_e64 s[0:1], v121, v8
	v_cmp_eq_u32_e64 s[6:7], v129, v8
	v_cmp_eq_u32_e64 s[8:9], v137, v8
	v_cndmask_b32_e32 v119, v119, v110, vcc
	v_cndmask_b32_e64 v127, v127, v110, s[0:1]
	v_cndmask_b32_e64 v135, v135, v110, s[6:7]
	v_cndmask_b32_e64 v143, v143, v110, s[8:9]
	v_cmp_eq_u32_e32 vcc, v113, v9
	v_cmp_eq_u32_e64 s[0:1], v121, v9
	v_cmp_eq_u32_e64 s[6:7], v129, v9
	v_cmp_eq_u32_e64 s[8:9], v137, v9
	v_cndmask_b32_e32 v119, v119, v111, vcc
	v_cndmask_b32_e64 v127, v127, v111, s[0:1]
	v_cndmask_b32_e64 v135, v135, v111, s[6:7]
	v_cndmask_b32_e64 v143, v143, v111, s[8:9]
	v_add_u32_e32 v112, v112, v119
	v_add_u32_e32 v120, v120, v127
	v_add_u32_e32 v128, v128, v135
	v_add_u32_e32 v136, v136, v143
	v_cmp_ne_u32_e32 vcc, -1, v119
	s_and_saveexec_b64 s[24:25], vcc
	ds_write_b32 v112, v114
	s_mov_b64 exec, s[24:25]
	v_cmp_ne_u32_e32 vcc, -1, v127
	s_and_saveexec_b64 s[24:25], vcc
	ds_write_b32 v120, v122
	s_mov_b64 exec, s[24:25]
	v_cmp_ne_u32_e32 vcc, -1, v135
	s_and_saveexec_b64 s[24:25], vcc
	ds_write_b32 v128, v130
	s_mov_b64 exec, s[24:25]
	v_cmp_ne_u32_e32 vcc, -1, v143
	s_and_saveexec_b64 s[24:25], vcc
	ds_write_b32 v136, v138
	s_mov_b64 exec, s[24:25]
	v_and_b32_e32 v112, 0xff, v84
	v_and_b32_e32 v120, 0xff, v85
	v_and_b32_e32 v128, 0xff, v86
	v_and_b32_e32 v136, 0xff, v87
	v_lshlrev_b32_e32 v112, 2, v112
	v_lshlrev_b32_e32 v120, 2, v120
	v_lshlrev_b32_e32 v128, 2, v128
	v_lshlrev_b32_e32 v136, 2, v136
	v_add_u32_e32 v118, v112, v11
	v_add_u32_e32 v126, v120, v11
	v_add_u32_e32 v134, v128, v11
	v_add_u32_e32 v142, v136, v11
	ds_read_b32 v113, v112 offset:36864
	ds_read_b32 v114, v112 offset:36224
	ds_read_b32 v115, v118 offset:22528
	ds_read_b32 v121, v120 offset:36864
	ds_read_b32 v122, v120 offset:36224
	ds_read_b32 v123, v126 offset:23040
	ds_read_b32 v129, v128 offset:36864
	ds_read_b32 v130, v128 offset:36224
	ds_read_b32 v131, v134 offset:23552
	ds_read_b32 v137, v136 offset:36864
	ds_read_b32 v138, v136 offset:36224
	ds_read_b32 v139, v142 offset:24064
	v_add_u32_e32 v117, 176, v36
	v_add_u32_e32 v125, 180, v36
	v_add_u32_e32 v133, 184, v36
	v_add_u32_e32 v141, 188, v36
	v_mul_hi_u32 v118, v117, v15
	v_mul_hi_u32 v126, v125, v15
	v_mul_hi_u32 v134, v133, v15
	v_mul_hi_u32 v142, v141, v15
	v_mul_lo_u32 v118, v118, s11
	v_mul_lo_u32 v126, v126, s11
	v_mul_lo_u32 v134, v134, s11
	v_mul_lo_u32 v142, v142, s11
	v_sub_u32_e32 v117, v117, v118
	v_sub_u32_e32 v125, v125, v126
	v_sub_u32_e32 v133, v133, v134
	v_sub_u32_e32 v141, v141, v142
	v_subrev_u32_e32 v118, s11, v117
	v_subrev_u32_e32 v126, s11, v125
	v_subrev_u32_e32 v134, s11, v133
	v_subrev_u32_e32 v142, s11, v141
	v_cmp_le_u32_e32 vcc, s11, v117
	v_cmp_le_u32_e64 s[0:1], s11, v125
	v_cmp_le_u32_e64 s[6:7], s11, v133
	v_cmp_le_u32_e64 s[8:9], s11, v141
	v_cndmask_b32_e32 v117, v117, v118, vcc
	v_cndmask_b32_e64 v125, v125, v126, s[0:1]
	v_cndmask_b32_e64 v133, v133, v134, s[6:7]
	v_cndmask_b32_e64 v141, v141, v142, s[8:9]
	v_subrev_u32_e32 v118, s11, v117
	v_subrev_u32_e32 v126, s11, v125
	v_subrev_u32_e32 v134, s11, v133
	v_subrev_u32_e32 v142, s11, v141
	v_cmp_le_u32_e32 vcc, s11, v117
	v_cmp_le_u32_e64 s[0:1], s11, v125
	v_cmp_le_u32_e64 s[6:7], s11, v133
	v_cmp_le_u32_e64 s[8:9], s11, v141
	v_cndmask_b32_e32 v117, v117, v118, vcc
	v_cndmask_b32_e64 v125, v125, v126, s[0:1]
	v_cndmask_b32_e64 v133, v133, v134, s[6:7]
	v_cndmask_b32_e64 v141, v141, v142, s[8:9]
	v_ashrrev_i32_e32 v116, 8, v84
	v_ashrrev_i32_e32 v124, 8, v85
	v_ashrrev_i32_e32 v132, 8, v86
	v_ashrrev_i32_e32 v140, 8, v87
	s_waitcnt lgkmcnt(0)
	v_add_u32_e32 v116, v116, v113
	v_add_u32_e32 v124, v124, v121
	v_add_u32_e32 v132, v132, v129
	v_add_u32_e32 v140, v140, v137
	v_add3_u32 v116, v116, v114, v115
	v_add3_u32 v124, v124, v122, v123
	v_add3_u32 v132, v132, v130, v131
	v_add3_u32 v140, v140, v138, v139
	v_cmp_eq_u32_e32 vcc, s93, v117
	v_add_u32_e32 v1, 0x16000, v10
	s_and_saveexec_b64 s[24:25], vcc
	global_store_dword v1, v116, s[16:17]
	s_mov_b64 exec, s[24:25]
	v_cmp_eq_u32_e32 vcc, s93, v125
	v_add_u32_e32 v1, 0x16800, v10
	s_and_saveexec_b64 s[24:25], vcc
	global_store_dword v1, v124, s[16:17]
	s_mov_b64 exec, s[24:25]
	v_cmp_eq_u32_e32 vcc, s93, v133
	v_add_u32_e32 v1, 0x17000, v10
	s_and_saveexec_b64 s[24:25], vcc
	global_store_dword v1, v132, s[16:17]
	s_mov_b64 exec, s[24:25]
	v_cmp_eq_u32_e32 vcc, s93, v141
	v_add_u32_e32 v1, 0x17800, v10
	s_and_saveexec_b64 s[24:25], vcc
	global_store_dword v1, v140, s[16:17]
	s_mov_b64 exec, s[24:25]
	v_ashrrev_i32_e32 v113, 8, v116
	v_ashrrev_i32_e32 v121, 8, v124
	v_ashrrev_i32_e32 v129, 8, v132
	v_ashrrev_i32_e32 v137, 8, v140
	v_and_b32_e32 v112, 0xff, v116
	v_and_b32_e32 v120, 0xff, v124
	v_and_b32_e32 v128, 0xff, v132
	v_and_b32_e32 v136, 0xff, v140
	v_lshl_add_u32 v112, v112, 2, s10
	v_lshl_add_u32 v120, v120, 2, s10
	v_lshl_add_u32 v128, v128, 2, s10
	v_lshl_add_u32 v136, v136, 2, s10
	v_add_u32_e32 v114, 0x2c00, v34
	v_add_u32_e32 v122, 0x2d00, v34
	v_add_u32_e32 v130, 0x2e00, v34
	v_add_u32_e32 v138, 0x2f00, v34
	v_mov_b32_e32 v119, -1
	v_mov_b32_e32 v127, -1
	v_mov_b32_e32 v135, -1
	v_mov_b32_e32 v143, -1
	v_cmp_eq_u32_e32 vcc, v113, v2
	v_cmp_eq_u32_e64 s[0:1], v121, v2
	v_cmp_eq_u32_e64 s[6:7], v129, v2
	v_cmp_eq_u32_e64 s[8:9], v137, v2
	v_cndmask_b32_e32 v119, v119, v104, vcc
	v_cndmask_b32_e64 v127, v127, v104, s[0:1]
	v_cndmask_b32_e64 v135, v135, v104, s[6:7]
	v_cndmask_b32_e64 v143, v143, v104, s[8:9]
	v_cmp_eq_u32_e32 vcc, v113, v3
	v_cmp_eq_u32_e64 s[0:1], v121, v3
	v_cmp_eq_u32_e64 s[6:7], v129, v3
	v_cmp_eq_u32_e64 s[8:9], v137, v3
	v_cndmask_b32_e32 v119, v119, v105, vcc
	v_cndmask_b32_e64 v127, v127, v105, s[0:1]
	v_cndmask_b32_e64 v135, v135, v105, s[6:7]
	v_cndmask_b32_e64 v143, v143, v105, s[8:9]
	v_cmp_eq_u32_e32 vcc, v113, v4
	v_cmp_eq_u32_e64 s[0:1], v121, v4
	v_cmp_eq_u32_e64 s[6:7], v129, v4
	v_cmp_eq_u32_e64 s[8:9], v137, v4
	v_cndmask_b32_e32 v119, v119, v106, vcc
	v_cndmask_b32_e64 v127, v127, v106, s[0:1]
	v_cndmask_b32_e64 v135, v135, v106, s[6:7]
	v_cndmask_b32_e64 v143, v143, v106, s[8:9]
	v_cmp_eq_u32_e32 vcc, v113, v5
	v_cmp_eq_u32_e64 s[0:1], v121, v5
	v_cmp_eq_u32_e64 s[6:7], v129, v5
	v_cmp_eq_u32_e64 s[8:9], v137, v5
	v_cndmask_b32_e32 v119, v119, v107, vcc
	v_cndmask_b32_e64 v127, v127, v107, s[0:1]
	v_cndmask_b32_e64 v135, v135, v107, s[6:7]
	v_cndmask_b32_e64 v143, v143, v107, s[8:9]
	v_cmp_eq_u32_e32 vcc, v113, v6
	v_cmp_eq_u32_e64 s[0:1], v121, v6
	v_cmp_eq_u32_e64 s[6:7], v129, v6
	v_cmp_eq_u32_e64 s[8:9], v137, v6
	v_cndmask_b32_e32 v119, v119, v108, vcc
	v_cndmask_b32_e64 v127, v127, v108, s[0:1]
	v_cndmask_b32_e64 v135, v135, v108, s[6:7]
	v_cndmask_b32_e64 v143, v143, v108, s[8:9]
	v_cmp_eq_u32_e32 vcc, v113, v7
	v_cmp_eq_u32_e64 s[0:1], v121, v7
	v_cmp_eq_u32_e64 s[6:7], v129, v7
	v_cmp_eq_u32_e64 s[8:9], v137, v7
	v_cndmask_b32_e32 v119, v119, v109, vcc
	v_cndmask_b32_e64 v127, v127, v109, s[0:1]
	v_cndmask_b32_e64 v135, v135, v109, s[6:7]
	v_cndmask_b32_e64 v143, v143, v109, s[8:9]
	v_cmp_eq_u32_e32 vcc, v113, v8
	v_cmp_eq_u32_e64 s[0:1], v121, v8
	v_cmp_eq_u32_e64 s[6:7], v129, v8
	v_cmp_eq_u32_e64 s[8:9], v137, v8
	v_cndmask_b32_e32 v119, v119, v110, vcc
	v_cndmask_b32_e64 v127, v127, v110, s[0:1]
	v_cndmask_b32_e64 v135, v135, v110, s[6:7]
	v_cndmask_b32_e64 v143, v143, v110, s[8:9]
	v_cmp_eq_u32_e32 vcc, v113, v9
	v_cmp_eq_u32_e64 s[0:1], v121, v9
	v_cmp_eq_u32_e64 s[6:7], v129, v9
	v_cmp_eq_u32_e64 s[8:9], v137, v9
	v_cndmask_b32_e32 v119, v119, v111, vcc
	v_cndmask_b32_e64 v127, v127, v111, s[0:1]
	v_cndmask_b32_e64 v135, v135, v111, s[6:7]
	v_cndmask_b32_e64 v143, v143, v111, s[8:9]
	v_add_u32_e32 v112, v112, v119
	v_add_u32_e32 v120, v120, v127
	v_add_u32_e32 v128, v128, v135
	v_add_u32_e32 v136, v136, v143
	v_cmp_ne_u32_e32 vcc, -1, v119
	s_and_saveexec_b64 s[24:25], vcc
	ds_write_b32 v112, v114
	s_mov_b64 exec, s[24:25]
	v_cmp_ne_u32_e32 vcc, -1, v127
	s_and_saveexec_b64 s[24:25], vcc
	ds_write_b32 v120, v122
	s_mov_b64 exec, s[24:25]
	v_cmp_ne_u32_e32 vcc, -1, v135
	s_and_saveexec_b64 s[24:25], vcc
	ds_write_b32 v128, v130
	s_mov_b64 exec, s[24:25]
	v_cmp_ne_u32_e32 vcc, -1, v143
	s_and_saveexec_b64 s[24:25], vcc
	ds_write_b32 v136, v138
	s_mov_b64 exec, s[24:25]
	v_and_b32_e32 v112, 0xff, v88
	v_and_b32_e32 v120, 0xff, v89
	v_and_b32_e32 v128, 0xff, v90
	v_and_b32_e32 v136, 0xff, v91
	v_lshlrev_b32_e32 v112, 2, v112
	v_lshlrev_b32_e32 v120, 2, v120
	v_lshlrev_b32_e32 v128, 2, v128
	v_lshlrev_b32_e32 v136, 2, v136
	v_add_u32_e32 v118, v112, v11
	v_add_u32_e32 v126, v120, v11
	v_add_u32_e32 v134, v128, v11
	v_add_u32_e32 v142, v136, v11
	ds_read_b32 v113, v112 offset:36864
	ds_read_b32 v114, v112 offset:36352
	ds_read_b32 v115, v118 offset:24576
	ds_read_b32 v121, v120 offset:36864
	ds_read_b32 v122, v120 offset:36352
	ds_read_b32 v123, v126 offset:25088
	ds_read_b32 v129, v128 offset:36864
	ds_read_b32 v130, v128 offset:36352
	ds_read_b32 v131, v134 offset:25600
	ds_read_b32 v137, v136 offset:36864
	ds_read_b32 v138, v136 offset:36352
	ds_read_b32 v139, v142 offset:26112
	v_add_u32_e32 v117, 192, v36
	v_add_u32_e32 v125, 196, v36
	v_add_u32_e32 v133, 200, v36
	v_add_u32_e32 v141, 204, v36
	v_mul_hi_u32 v118, v117, v15
	v_mul_hi_u32 v126, v125, v15
	v_mul_hi_u32 v134, v133, v15
	v_mul_hi_u32 v142, v141, v15
	v_mul_lo_u32 v118, v118, s11
	v_mul_lo_u32 v126, v126, s11
	v_mul_lo_u32 v134, v134, s11
	v_mul_lo_u32 v142, v142, s11
	v_sub_u32_e32 v117, v117, v118
	v_sub_u32_e32 v125, v125, v126
	v_sub_u32_e32 v133, v133, v134
	v_sub_u32_e32 v141, v141, v142
	v_subrev_u32_e32 v118, s11, v117
	v_subrev_u32_e32 v126, s11, v125
	v_subrev_u32_e32 v134, s11, v133
	v_subrev_u32_e32 v142, s11, v141
	v_cmp_le_u32_e32 vcc, s11, v117
	v_cmp_le_u32_e64 s[0:1], s11, v125
	v_cmp_le_u32_e64 s[6:7], s11, v133
	v_cmp_le_u32_e64 s[8:9], s11, v141
	v_cndmask_b32_e32 v117, v117, v118, vcc
	v_cndmask_b32_e64 v125, v125, v126, s[0:1]
	v_cndmask_b32_e64 v133, v133, v134, s[6:7]
	v_cndmask_b32_e64 v141, v141, v142, s[8:9]
	v_subrev_u32_e32 v118, s11, v117
	v_subrev_u32_e32 v126, s11, v125
	v_subrev_u32_e32 v134, s11, v133
	v_subrev_u32_e32 v142, s11, v141
	v_cmp_le_u32_e32 vcc, s11, v117
	v_cmp_le_u32_e64 s[0:1], s11, v125
	v_cmp_le_u32_e64 s[6:7], s11, v133
	v_cmp_le_u32_e64 s[8:9], s11, v141
	v_cndmask_b32_e32 v117, v117, v118, vcc
	v_cndmask_b32_e64 v125, v125, v126, s[0:1]
	v_cndmask_b32_e64 v133, v133, v134, s[6:7]
	v_cndmask_b32_e64 v141, v141, v142, s[8:9]
	v_ashrrev_i32_e32 v116, 8, v88
	v_ashrrev_i32_e32 v124, 8, v89
	v_ashrrev_i32_e32 v132, 8, v90
	v_ashrrev_i32_e32 v140, 8, v91
	s_waitcnt lgkmcnt(0)
	v_add_u32_e32 v116, v116, v113
	v_add_u32_e32 v124, v124, v121
	v_add_u32_e32 v132, v132, v129
	v_add_u32_e32 v140, v140, v137
	v_add3_u32 v116, v116, v114, v115
	v_add3_u32 v124, v124, v122, v123
	v_add3_u32 v132, v132, v130, v131
	v_add3_u32 v140, v140, v138, v139
	v_cmp_eq_u32_e32 vcc, s93, v117
	v_add_u32_e32 v1, 0x18000, v10
	s_and_saveexec_b64 s[24:25], vcc
	global_store_dword v1, v116, s[16:17]
	s_mov_b64 exec, s[24:25]
	v_cmp_eq_u32_e32 vcc, s93, v125
	v_add_u32_e32 v1, 0x18800, v10
	s_and_saveexec_b64 s[24:25], vcc
	global_store_dword v1, v124, s[16:17]
	s_mov_b64 exec, s[24:25]
	v_cmp_eq_u32_e32 vcc, s93, v133
	v_add_u32_e32 v1, 0x19000, v10
	s_and_saveexec_b64 s[24:25], vcc
	global_store_dword v1, v132, s[16:17]
	s_mov_b64 exec, s[24:25]
	v_cmp_eq_u32_e32 vcc, s93, v141
	v_add_u32_e32 v1, 0x19800, v10
	s_and_saveexec_b64 s[24:25], vcc
	global_store_dword v1, v140, s[16:17]
	s_mov_b64 exec, s[24:25]
	v_ashrrev_i32_e32 v113, 8, v116
	v_ashrrev_i32_e32 v121, 8, v124
	v_ashrrev_i32_e32 v129, 8, v132
	v_ashrrev_i32_e32 v137, 8, v140
	v_and_b32_e32 v112, 0xff, v116
	v_and_b32_e32 v120, 0xff, v124
	v_and_b32_e32 v128, 0xff, v132
	v_and_b32_e32 v136, 0xff, v140
	v_lshl_add_u32 v112, v112, 2, s10
	v_lshl_add_u32 v120, v120, 2, s10
	v_lshl_add_u32 v128, v128, 2, s10
	v_lshl_add_u32 v136, v136, 2, s10
	v_add_u32_e32 v114, 0x3000, v34
	v_add_u32_e32 v122, 0x3100, v34
	v_add_u32_e32 v130, 0x3200, v34
	v_add_u32_e32 v138, 0x3300, v34
	v_mov_b32_e32 v119, -1
	v_mov_b32_e32 v127, -1
	v_mov_b32_e32 v135, -1
	v_mov_b32_e32 v143, -1
	v_cmp_eq_u32_e32 vcc, v113, v2
	v_cmp_eq_u32_e64 s[0:1], v121, v2
	v_cmp_eq_u32_e64 s[6:7], v129, v2
	v_cmp_eq_u32_e64 s[8:9], v137, v2
	v_cndmask_b32_e32 v119, v119, v104, vcc
	v_cndmask_b32_e64 v127, v127, v104, s[0:1]
	v_cndmask_b32_e64 v135, v135, v104, s[6:7]
	v_cndmask_b32_e64 v143, v143, v104, s[8:9]
	v_cmp_eq_u32_e32 vcc, v113, v3
	v_cmp_eq_u32_e64 s[0:1], v121, v3
	v_cmp_eq_u32_e64 s[6:7], v129, v3
	v_cmp_eq_u32_e64 s[8:9], v137, v3
	v_cndmask_b32_e32 v119, v119, v105, vcc
	v_cndmask_b32_e64 v127, v127, v105, s[0:1]
	v_cndmask_b32_e64 v135, v135, v105, s[6:7]
	v_cndmask_b32_e64 v143, v143, v105, s[8:9]
	v_cmp_eq_u32_e32 vcc, v113, v4
	v_cmp_eq_u32_e64 s[0:1], v121, v4
	v_cmp_eq_u32_e64 s[6:7], v129, v4
	v_cmp_eq_u32_e64 s[8:9], v137, v4
	v_cndmask_b32_e32 v119, v119, v106, vcc
	v_cndmask_b32_e64 v127, v127, v106, s[0:1]
	v_cndmask_b32_e64 v135, v135, v106, s[6:7]
	v_cndmask_b32_e64 v143, v143, v106, s[8:9]
	v_cmp_eq_u32_e32 vcc, v113, v5
	v_cmp_eq_u32_e64 s[0:1], v121, v5
	v_cmp_eq_u32_e64 s[6:7], v129, v5
	v_cmp_eq_u32_e64 s[8:9], v137, v5
	v_cndmask_b32_e32 v119, v119, v107, vcc
	v_cndmask_b32_e64 v127, v127, v107, s[0:1]
	v_cndmask_b32_e64 v135, v135, v107, s[6:7]
	v_cndmask_b32_e64 v143, v143, v107, s[8:9]
	v_cmp_eq_u32_e32 vcc, v113, v6
	v_cmp_eq_u32_e64 s[0:1], v121, v6
	v_cmp_eq_u32_e64 s[6:7], v129, v6
	v_cmp_eq_u32_e64 s[8:9], v137, v6
	v_cndmask_b32_e32 v119, v119, v108, vcc
	v_cndmask_b32_e64 v127, v127, v108, s[0:1]
	v_cndmask_b32_e64 v135, v135, v108, s[6:7]
	v_cndmask_b32_e64 v143, v143, v108, s[8:9]
	v_cmp_eq_u32_e32 vcc, v113, v7
	v_cmp_eq_u32_e64 s[0:1], v121, v7
	v_cmp_eq_u32_e64 s[6:7], v129, v7
	v_cmp_eq_u32_e64 s[8:9], v137, v7
	v_cndmask_b32_e32 v119, v119, v109, vcc
	v_cndmask_b32_e64 v127, v127, v109, s[0:1]
	v_cndmask_b32_e64 v135, v135, v109, s[6:7]
	v_cndmask_b32_e64 v143, v143, v109, s[8:9]
	v_cmp_eq_u32_e32 vcc, v113, v8
	v_cmp_eq_u32_e64 s[0:1], v121, v8
	v_cmp_eq_u32_e64 s[6:7], v129, v8
	v_cmp_eq_u32_e64 s[8:9], v137, v8
	v_cndmask_b32_e32 v119, v119, v110, vcc
	v_cndmask_b32_e64 v127, v127, v110, s[0:1]
	v_cndmask_b32_e64 v135, v135, v110, s[6:7]
	v_cndmask_b32_e64 v143, v143, v110, s[8:9]
	v_cmp_eq_u32_e32 vcc, v113, v9
	v_cmp_eq_u32_e64 s[0:1], v121, v9
	v_cmp_eq_u32_e64 s[6:7], v129, v9
	v_cmp_eq_u32_e64 s[8:9], v137, v9
	v_cndmask_b32_e32 v119, v119, v111, vcc
	v_cndmask_b32_e64 v127, v127, v111, s[0:1]
	v_cndmask_b32_e64 v135, v135, v111, s[6:7]
	v_cndmask_b32_e64 v143, v143, v111, s[8:9]
	v_add_u32_e32 v112, v112, v119
	v_add_u32_e32 v120, v120, v127
	v_add_u32_e32 v128, v128, v135
	v_add_u32_e32 v136, v136, v143
	v_cmp_ne_u32_e32 vcc, -1, v119
	s_and_saveexec_b64 s[24:25], vcc
	ds_write_b32 v112, v114
	s_mov_b64 exec, s[24:25]
	v_cmp_ne_u32_e32 vcc, -1, v127
	s_and_saveexec_b64 s[24:25], vcc
	ds_write_b32 v120, v122
	s_mov_b64 exec, s[24:25]
	v_cmp_ne_u32_e32 vcc, -1, v135
	s_and_saveexec_b64 s[24:25], vcc
	ds_write_b32 v128, v130
	s_mov_b64 exec, s[24:25]
	v_cmp_ne_u32_e32 vcc, -1, v143
	s_and_saveexec_b64 s[24:25], vcc
	ds_write_b32 v136, v138
	s_mov_b64 exec, s[24:25]
	v_and_b32_e32 v112, 0xff, v92
	v_and_b32_e32 v120, 0xff, v93
	v_and_b32_e32 v128, 0xff, v94
	v_and_b32_e32 v136, 0xff, v95
	v_lshlrev_b32_e32 v112, 2, v112
	v_lshlrev_b32_e32 v120, 2, v120
	v_lshlrev_b32_e32 v128, 2, v128
	v_lshlrev_b32_e32 v136, 2, v136
	v_add_u32_e32 v118, v112, v11
	v_add_u32_e32 v126, v120, v11
	v_add_u32_e32 v134, v128, v11
	v_add_u32_e32 v142, v136, v11
	ds_read_b32 v113, v112 offset:36864
	ds_read_b32 v114, v112 offset:36480
	ds_read_b32 v115, v118 offset:26624
	ds_read_b32 v121, v120 offset:36864
	ds_read_b32 v122, v120 offset:36480
	ds_read_b32 v123, v126 offset:27136
	ds_read_b32 v129, v128 offset:36864
	ds_read_b32 v130, v128 offset:36480
	ds_read_b32 v131, v134 offset:27648
	ds_read_b32 v137, v136 offset:36864
	ds_read_b32 v138, v136 offset:36480
	ds_read_b32 v139, v142 offset:28160
	v_add_u32_e32 v117, 208, v36
	v_add_u32_e32 v125, 212, v36
	v_add_u32_e32 v133, 216, v36
	v_add_u32_e32 v141, 220, v36
	v_mul_hi_u32 v118, v117, v15
	v_mul_hi_u32 v126, v125, v15
	v_mul_hi_u32 v134, v133, v15
	v_mul_hi_u32 v142, v141, v15
	v_mul_lo_u32 v118, v118, s11
	v_mul_lo_u32 v126, v126, s11
	v_mul_lo_u32 v134, v134, s11
	v_mul_lo_u32 v142, v142, s11
	v_sub_u32_e32 v117, v117, v118
	v_sub_u32_e32 v125, v125, v126
	v_sub_u32_e32 v133, v133, v134
	v_sub_u32_e32 v141, v141, v142
	v_subrev_u32_e32 v118, s11, v117
	v_subrev_u32_e32 v126, s11, v125
	v_subrev_u32_e32 v134, s11, v133
	v_subrev_u32_e32 v142, s11, v141
	v_cmp_le_u32_e32 vcc, s11, v117
	v_cmp_le_u32_e64 s[0:1], s11, v125
	v_cmp_le_u32_e64 s[6:7], s11, v133
	v_cmp_le_u32_e64 s[8:9], s11, v141
	v_cndmask_b32_e32 v117, v117, v118, vcc
	v_cndmask_b32_e64 v125, v125, v126, s[0:1]
	v_cndmask_b32_e64 v133, v133, v134, s[6:7]
	v_cndmask_b32_e64 v141, v141, v142, s[8:9]
	v_subrev_u32_e32 v118, s11, v117
	v_subrev_u32_e32 v126, s11, v125
	v_subrev_u32_e32 v134, s11, v133
	v_subrev_u32_e32 v142, s11, v141
	v_cmp_le_u32_e32 vcc, s11, v117
	v_cmp_le_u32_e64 s[0:1], s11, v125
	v_cmp_le_u32_e64 s[6:7], s11, v133
	v_cmp_le_u32_e64 s[8:9], s11, v141
	v_cndmask_b32_e32 v117, v117, v118, vcc
	v_cndmask_b32_e64 v125, v125, v126, s[0:1]
	v_cndmask_b32_e64 v133, v133, v134, s[6:7]
	v_cndmask_b32_e64 v141, v141, v142, s[8:9]
	v_ashrrev_i32_e32 v116, 8, v92
	v_ashrrev_i32_e32 v124, 8, v93
	v_ashrrev_i32_e32 v132, 8, v94
	v_ashrrev_i32_e32 v140, 8, v95
	s_waitcnt lgkmcnt(0)
	v_add_u32_e32 v116, v116, v113
	v_add_u32_e32 v124, v124, v121
	v_add_u32_e32 v132, v132, v129
	v_add_u32_e32 v140, v140, v137
	v_add3_u32 v116, v116, v114, v115
	v_add3_u32 v124, v124, v122, v123
	v_add3_u32 v132, v132, v130, v131
	v_add3_u32 v140, v140, v138, v139
	v_cmp_eq_u32_e32 vcc, s93, v117
	v_add_u32_e32 v1, 0x1a000, v10
	s_and_saveexec_b64 s[24:25], vcc
	global_store_dword v1, v116, s[16:17]
	s_mov_b64 exec, s[24:25]
	v_cmp_eq_u32_e32 vcc, s93, v125
	v_add_u32_e32 v1, 0x1a800, v10
	s_and_saveexec_b64 s[24:25], vcc
	global_store_dword v1, v124, s[16:17]
	s_mov_b64 exec, s[24:25]
	v_cmp_eq_u32_e32 vcc, s93, v133
	v_add_u32_e32 v1, 0x1b000, v10
	s_and_saveexec_b64 s[24:25], vcc
	global_store_dword v1, v132, s[16:17]
	s_mov_b64 exec, s[24:25]
	v_cmp_eq_u32_e32 vcc, s93, v141
	v_add_u32_e32 v1, 0x1b800, v10
	s_and_saveexec_b64 s[24:25], vcc
	global_store_dword v1, v140, s[16:17]
	s_mov_b64 exec, s[24:25]
	v_ashrrev_i32_e32 v113, 8, v116
	v_ashrrev_i32_e32 v121, 8, v124
	v_ashrrev_i32_e32 v129, 8, v132
	v_ashrrev_i32_e32 v137, 8, v140
	v_and_b32_e32 v112, 0xff, v116
	v_and_b32_e32 v120, 0xff, v124
	v_and_b32_e32 v128, 0xff, v132
	v_and_b32_e32 v136, 0xff, v140
	v_lshl_add_u32 v112, v112, 2, s10
	v_lshl_add_u32 v120, v120, 2, s10
	v_lshl_add_u32 v128, v128, 2, s10
	v_lshl_add_u32 v136, v136, 2, s10
	v_add_u32_e32 v114, 0x3400, v34
	v_add_u32_e32 v122, 0x3500, v34
	v_add_u32_e32 v130, 0x3600, v34
	v_add_u32_e32 v138, 0x3700, v34
	v_mov_b32_e32 v119, -1
	v_mov_b32_e32 v127, -1
	v_mov_b32_e32 v135, -1
	v_mov_b32_e32 v143, -1
	v_cmp_eq_u32_e32 vcc, v113, v2
	v_cmp_eq_u32_e64 s[0:1], v121, v2
	v_cmp_eq_u32_e64 s[6:7], v129, v2
	v_cmp_eq_u32_e64 s[8:9], v137, v2
	v_cndmask_b32_e32 v119, v119, v104, vcc
	v_cndmask_b32_e64 v127, v127, v104, s[0:1]
	v_cndmask_b32_e64 v135, v135, v104, s[6:7]
	v_cndmask_b32_e64 v143, v143, v104, s[8:9]
	v_cmp_eq_u32_e32 vcc, v113, v3
	v_cmp_eq_u32_e64 s[0:1], v121, v3
	v_cmp_eq_u32_e64 s[6:7], v129, v3
	v_cmp_eq_u32_e64 s[8:9], v137, v3
	v_cndmask_b32_e32 v119, v119, v105, vcc
	v_cndmask_b32_e64 v127, v127, v105, s[0:1]
	v_cndmask_b32_e64 v135, v135, v105, s[6:7]
	v_cndmask_b32_e64 v143, v143, v105, s[8:9]
	v_cmp_eq_u32_e32 vcc, v113, v4
	v_cmp_eq_u32_e64 s[0:1], v121, v4
	v_cmp_eq_u32_e64 s[6:7], v129, v4
	v_cmp_eq_u32_e64 s[8:9], v137, v4
	v_cndmask_b32_e32 v119, v119, v106, vcc
	v_cndmask_b32_e64 v127, v127, v106, s[0:1]
	v_cndmask_b32_e64 v135, v135, v106, s[6:7]
	v_cndmask_b32_e64 v143, v143, v106, s[8:9]
	v_cmp_eq_u32_e32 vcc, v113, v5
	v_cmp_eq_u32_e64 s[0:1], v121, v5
	v_cmp_eq_u32_e64 s[6:7], v129, v5
	v_cmp_eq_u32_e64 s[8:9], v137, v5
	v_cndmask_b32_e32 v119, v119, v107, vcc
	v_cndmask_b32_e64 v127, v127, v107, s[0:1]
	v_cndmask_b32_e64 v135, v135, v107, s[6:7]
	v_cndmask_b32_e64 v143, v143, v107, s[8:9]
	v_cmp_eq_u32_e32 vcc, v113, v6
	v_cmp_eq_u32_e64 s[0:1], v121, v6
	v_cmp_eq_u32_e64 s[6:7], v129, v6
	v_cmp_eq_u32_e64 s[8:9], v137, v6
	v_cndmask_b32_e32 v119, v119, v108, vcc
	v_cndmask_b32_e64 v127, v127, v108, s[0:1]
	v_cndmask_b32_e64 v135, v135, v108, s[6:7]
	v_cndmask_b32_e64 v143, v143, v108, s[8:9]
	v_cmp_eq_u32_e32 vcc, v113, v7
	v_cmp_eq_u32_e64 s[0:1], v121, v7
	v_cmp_eq_u32_e64 s[6:7], v129, v7
	v_cmp_eq_u32_e64 s[8:9], v137, v7
	v_cndmask_b32_e32 v119, v119, v109, vcc
	v_cndmask_b32_e64 v127, v127, v109, s[0:1]
	v_cndmask_b32_e64 v135, v135, v109, s[6:7]
	v_cndmask_b32_e64 v143, v143, v109, s[8:9]
	v_cmp_eq_u32_e32 vcc, v113, v8
	v_cmp_eq_u32_e64 s[0:1], v121, v8
	v_cmp_eq_u32_e64 s[6:7], v129, v8
	v_cmp_eq_u32_e64 s[8:9], v137, v8
	v_cndmask_b32_e32 v119, v119, v110, vcc
	v_cndmask_b32_e64 v127, v127, v110, s[0:1]
	v_cndmask_b32_e64 v135, v135, v110, s[6:7]
	v_cndmask_b32_e64 v143, v143, v110, s[8:9]
	v_cmp_eq_u32_e32 vcc, v113, v9
	v_cmp_eq_u32_e64 s[0:1], v121, v9
	v_cmp_eq_u32_e64 s[6:7], v129, v9
	v_cmp_eq_u32_e64 s[8:9], v137, v9
	v_cndmask_b32_e32 v119, v119, v111, vcc
	v_cndmask_b32_e64 v127, v127, v111, s[0:1]
	v_cndmask_b32_e64 v135, v135, v111, s[6:7]
	v_cndmask_b32_e64 v143, v143, v111, s[8:9]
	v_add_u32_e32 v112, v112, v119
	v_add_u32_e32 v120, v120, v127
	v_add_u32_e32 v128, v128, v135
	v_add_u32_e32 v136, v136, v143
	v_cmp_ne_u32_e32 vcc, -1, v119
	s_and_saveexec_b64 s[24:25], vcc
	ds_write_b32 v112, v114
	s_mov_b64 exec, s[24:25]
	v_cmp_ne_u32_e32 vcc, -1, v127
	s_and_saveexec_b64 s[24:25], vcc
	ds_write_b32 v120, v122
	s_mov_b64 exec, s[24:25]
	v_cmp_ne_u32_e32 vcc, -1, v135
	s_and_saveexec_b64 s[24:25], vcc
	ds_write_b32 v128, v130
	s_mov_b64 exec, s[24:25]
	v_cmp_ne_u32_e32 vcc, -1, v143
	s_and_saveexec_b64 s[24:25], vcc
	ds_write_b32 v136, v138
	s_mov_b64 exec, s[24:25]
	v_and_b32_e32 v112, 0xff, v96
	v_and_b32_e32 v120, 0xff, v97
	v_and_b32_e32 v128, 0xff, v98
	v_and_b32_e32 v136, 0xff, v99
	v_lshlrev_b32_e32 v112, 2, v112
	v_lshlrev_b32_e32 v120, 2, v120
	v_lshlrev_b32_e32 v128, 2, v128
	v_lshlrev_b32_e32 v136, 2, v136
	v_add_u32_e32 v118, v112, v11
	v_add_u32_e32 v126, v120, v11
	v_add_u32_e32 v134, v128, v11
	v_add_u32_e32 v142, v136, v11
	ds_read_b32 v113, v112 offset:36864
	ds_read_b32 v114, v112 offset:36608
	ds_read_b32 v115, v118 offset:28672
	ds_read_b32 v121, v120 offset:36864
	ds_read_b32 v122, v120 offset:36608
	ds_read_b32 v123, v126 offset:29184
	ds_read_b32 v129, v128 offset:36864
	ds_read_b32 v130, v128 offset:36608
	ds_read_b32 v131, v134 offset:29696
	ds_read_b32 v137, v136 offset:36864
	ds_read_b32 v138, v136 offset:36608
	ds_read_b32 v139, v142 offset:30208
	v_add_u32_e32 v117, 224, v36
	v_add_u32_e32 v125, 228, v36
	v_add_u32_e32 v133, 232, v36
	v_add_u32_e32 v141, 236, v36
	v_mul_hi_u32 v118, v117, v15
	v_mul_hi_u32 v126, v125, v15
	v_mul_hi_u32 v134, v133, v15
	v_mul_hi_u32 v142, v141, v15
	v_mul_lo_u32 v118, v118, s11
	v_mul_lo_u32 v126, v126, s11
	v_mul_lo_u32 v134, v134, s11
	v_mul_lo_u32 v142, v142, s11
	v_sub_u32_e32 v117, v117, v118
	v_sub_u32_e32 v125, v125, v126
	v_sub_u32_e32 v133, v133, v134
	v_sub_u32_e32 v141, v141, v142
	v_subrev_u32_e32 v118, s11, v117
	v_subrev_u32_e32 v126, s11, v125
	v_subrev_u32_e32 v134, s11, v133
	v_subrev_u32_e32 v142, s11, v141
	v_cmp_le_u32_e32 vcc, s11, v117
	v_cmp_le_u32_e64 s[0:1], s11, v125
	v_cmp_le_u32_e64 s[6:7], s11, v133
	v_cmp_le_u32_e64 s[8:9], s11, v141
	v_cndmask_b32_e32 v117, v117, v118, vcc
	v_cndmask_b32_e64 v125, v125, v126, s[0:1]
	v_cndmask_b32_e64 v133, v133, v134, s[6:7]
	v_cndmask_b32_e64 v141, v141, v142, s[8:9]
	v_subrev_u32_e32 v118, s11, v117
	v_subrev_u32_e32 v126, s11, v125
	v_subrev_u32_e32 v134, s11, v133
	v_subrev_u32_e32 v142, s11, v141
	v_cmp_le_u32_e32 vcc, s11, v117
	v_cmp_le_u32_e64 s[0:1], s11, v125
	v_cmp_le_u32_e64 s[6:7], s11, v133
	v_cmp_le_u32_e64 s[8:9], s11, v141
	v_cndmask_b32_e32 v117, v117, v118, vcc
	v_cndmask_b32_e64 v125, v125, v126, s[0:1]
	v_cndmask_b32_e64 v133, v133, v134, s[6:7]
	v_cndmask_b32_e64 v141, v141, v142, s[8:9]
	v_ashrrev_i32_e32 v116, 8, v96
	v_ashrrev_i32_e32 v124, 8, v97
	v_ashrrev_i32_e32 v132, 8, v98
	v_ashrrev_i32_e32 v140, 8, v99
	s_waitcnt lgkmcnt(0)
	v_add_u32_e32 v116, v116, v113
	v_add_u32_e32 v124, v124, v121
	v_add_u32_e32 v132, v132, v129
	v_add_u32_e32 v140, v140, v137
	v_add3_u32 v116, v116, v114, v115
	v_add3_u32 v124, v124, v122, v123
	v_add3_u32 v132, v132, v130, v131
	v_add3_u32 v140, v140, v138, v139
	v_cmp_eq_u32_e32 vcc, s93, v117
	v_add_u32_e32 v1, 0x1c000, v10
	s_and_saveexec_b64 s[24:25], vcc
	global_store_dword v1, v116, s[16:17]
	s_mov_b64 exec, s[24:25]
	v_cmp_eq_u32_e32 vcc, s93, v125
	v_add_u32_e32 v1, 0x1c800, v10
	s_and_saveexec_b64 s[24:25], vcc
	global_store_dword v1, v124, s[16:17]
	s_mov_b64 exec, s[24:25]
	v_cmp_eq_u32_e32 vcc, s93, v133
	v_add_u32_e32 v1, 0x1d000, v10
	s_and_saveexec_b64 s[24:25], vcc
	global_store_dword v1, v132, s[16:17]
	s_mov_b64 exec, s[24:25]
	v_cmp_eq_u32_e32 vcc, s93, v141
	v_add_u32_e32 v1, 0x1d800, v10
	s_and_saveexec_b64 s[24:25], vcc
	global_store_dword v1, v140, s[16:17]
	s_mov_b64 exec, s[24:25]
	v_ashrrev_i32_e32 v113, 8, v116
	v_ashrrev_i32_e32 v121, 8, v124
	v_ashrrev_i32_e32 v129, 8, v132
	v_ashrrev_i32_e32 v137, 8, v140
	v_and_b32_e32 v112, 0xff, v116
	v_and_b32_e32 v120, 0xff, v124
	v_and_b32_e32 v128, 0xff, v132
	v_and_b32_e32 v136, 0xff, v140
	v_lshl_add_u32 v112, v112, 2, s10
	v_lshl_add_u32 v120, v120, 2, s10
	v_lshl_add_u32 v128, v128, 2, s10
	v_lshl_add_u32 v136, v136, 2, s10
	v_add_u32_e32 v114, 0x3800, v34
	v_add_u32_e32 v122, 0x3900, v34
	v_add_u32_e32 v130, 0x3a00, v34
	v_add_u32_e32 v138, 0x3b00, v34
	v_mov_b32_e32 v119, -1
	v_mov_b32_e32 v127, -1
	v_mov_b32_e32 v135, -1
	v_mov_b32_e32 v143, -1
	v_cmp_eq_u32_e32 vcc, v113, v2
	v_cmp_eq_u32_e64 s[0:1], v121, v2
	v_cmp_eq_u32_e64 s[6:7], v129, v2
	v_cmp_eq_u32_e64 s[8:9], v137, v2
	v_cndmask_b32_e32 v119, v119, v104, vcc
	v_cndmask_b32_e64 v127, v127, v104, s[0:1]
	v_cndmask_b32_e64 v135, v135, v104, s[6:7]
	v_cndmask_b32_e64 v143, v143, v104, s[8:9]
	v_cmp_eq_u32_e32 vcc, v113, v3
	v_cmp_eq_u32_e64 s[0:1], v121, v3
	v_cmp_eq_u32_e64 s[6:7], v129, v3
	v_cmp_eq_u32_e64 s[8:9], v137, v3
	v_cndmask_b32_e32 v119, v119, v105, vcc
	v_cndmask_b32_e64 v127, v127, v105, s[0:1]
	v_cndmask_b32_e64 v135, v135, v105, s[6:7]
	v_cndmask_b32_e64 v143, v143, v105, s[8:9]
	v_cmp_eq_u32_e32 vcc, v113, v4
	v_cmp_eq_u32_e64 s[0:1], v121, v4
	v_cmp_eq_u32_e64 s[6:7], v129, v4
	v_cmp_eq_u32_e64 s[8:9], v137, v4
	v_cndmask_b32_e32 v119, v119, v106, vcc
	v_cndmask_b32_e64 v127, v127, v106, s[0:1]
	v_cndmask_b32_e64 v135, v135, v106, s[6:7]
	v_cndmask_b32_e64 v143, v143, v106, s[8:9]
	v_cmp_eq_u32_e32 vcc, v113, v5
	v_cmp_eq_u32_e64 s[0:1], v121, v5
	v_cmp_eq_u32_e64 s[6:7], v129, v5
	v_cmp_eq_u32_e64 s[8:9], v137, v5
	v_cndmask_b32_e32 v119, v119, v107, vcc
	v_cndmask_b32_e64 v127, v127, v107, s[0:1]
	v_cndmask_b32_e64 v135, v135, v107, s[6:7]
	v_cndmask_b32_e64 v143, v143, v107, s[8:9]
	v_cmp_eq_u32_e32 vcc, v113, v6
	v_cmp_eq_u32_e64 s[0:1], v121, v6
	v_cmp_eq_u32_e64 s[6:7], v129, v6
	v_cmp_eq_u32_e64 s[8:9], v137, v6
	v_cndmask_b32_e32 v119, v119, v108, vcc
	v_cndmask_b32_e64 v127, v127, v108, s[0:1]
	v_cndmask_b32_e64 v135, v135, v108, s[6:7]
	v_cndmask_b32_e64 v143, v143, v108, s[8:9]
	v_cmp_eq_u32_e32 vcc, v113, v7
	v_cmp_eq_u32_e64 s[0:1], v121, v7
	v_cmp_eq_u32_e64 s[6:7], v129, v7
	v_cmp_eq_u32_e64 s[8:9], v137, v7
	v_cndmask_b32_e32 v119, v119, v109, vcc
	v_cndmask_b32_e64 v127, v127, v109, s[0:1]
	v_cndmask_b32_e64 v135, v135, v109, s[6:7]
	v_cndmask_b32_e64 v143, v143, v109, s[8:9]
	v_cmp_eq_u32_e32 vcc, v113, v8
	v_cmp_eq_u32_e64 s[0:1], v121, v8
	v_cmp_eq_u32_e64 s[6:7], v129, v8
	v_cmp_eq_u32_e64 s[8:9], v137, v8
	v_cndmask_b32_e32 v119, v119, v110, vcc
	v_cndmask_b32_e64 v127, v127, v110, s[0:1]
	v_cndmask_b32_e64 v135, v135, v110, s[6:7]
	v_cndmask_b32_e64 v143, v143, v110, s[8:9]
	v_cmp_eq_u32_e32 vcc, v113, v9
	v_cmp_eq_u32_e64 s[0:1], v121, v9
	v_cmp_eq_u32_e64 s[6:7], v129, v9
	v_cmp_eq_u32_e64 s[8:9], v137, v9
	v_cndmask_b32_e32 v119, v119, v111, vcc
	v_cndmask_b32_e64 v127, v127, v111, s[0:1]
	v_cndmask_b32_e64 v135, v135, v111, s[6:7]
	v_cndmask_b32_e64 v143, v143, v111, s[8:9]
	v_add_u32_e32 v112, v112, v119
	v_add_u32_e32 v120, v120, v127
	v_add_u32_e32 v128, v128, v135
	v_add_u32_e32 v136, v136, v143
	v_cmp_ne_u32_e32 vcc, -1, v119
	s_and_saveexec_b64 s[24:25], vcc
	ds_write_b32 v112, v114
	s_mov_b64 exec, s[24:25]
	v_cmp_ne_u32_e32 vcc, -1, v127
	s_and_saveexec_b64 s[24:25], vcc
	ds_write_b32 v120, v122
	s_mov_b64 exec, s[24:25]
	v_cmp_ne_u32_e32 vcc, -1, v135
	s_and_saveexec_b64 s[24:25], vcc
	ds_write_b32 v128, v130
	s_mov_b64 exec, s[24:25]
	v_cmp_ne_u32_e32 vcc, -1, v143
	s_and_saveexec_b64 s[24:25], vcc
	ds_write_b32 v136, v138
	s_mov_b64 exec, s[24:25]
	v_and_b32_e32 v112, 0xff, v100
	v_and_b32_e32 v120, 0xff, v101
	v_and_b32_e32 v128, 0xff, v102
	v_and_b32_e32 v136, 0xff, v103
	v_lshlrev_b32_e32 v112, 2, v112
	v_lshlrev_b32_e32 v120, 2, v120
	v_lshlrev_b32_e32 v128, 2, v128
	v_lshlrev_b32_e32 v136, 2, v136
	v_add_u32_e32 v118, v112, v11
	v_add_u32_e32 v126, v120, v11
	v_add_u32_e32 v134, v128, v11
	v_add_u32_e32 v142, v136, v11
	ds_read_b32 v113, v112 offset:36864
	ds_read_b32 v114, v112 offset:36736
	ds_read_b32 v115, v118 offset:30720
	ds_read_b32 v121, v120 offset:36864
	ds_read_b32 v122, v120 offset:36736
	ds_read_b32 v123, v126 offset:31232
	ds_read_b32 v129, v128 offset:36864
	ds_read_b32 v130, v128 offset:36736
	ds_read_b32 v131, v134 offset:31744
	ds_read_b32 v137, v136 offset:36864
	ds_read_b32 v138, v136 offset:36736
	ds_read_b32 v139, v142 offset:32256
	v_add_u32_e32 v117, 240, v36
	v_add_u32_e32 v125, 244, v36
	v_add_u32_e32 v133, 248, v36
	v_add_u32_e32 v141, 252, v36
	v_mul_hi_u32 v118, v117, v15
	v_mul_hi_u32 v126, v125, v15
	v_mul_hi_u32 v134, v133, v15
	v_mul_hi_u32 v142, v141, v15
	v_mul_lo_u32 v118, v118, s11
	v_mul_lo_u32 v126, v126, s11
	v_mul_lo_u32 v134, v134, s11
	v_mul_lo_u32 v142, v142, s11
	v_sub_u32_e32 v117, v117, v118
	v_sub_u32_e32 v125, v125, v126
	v_sub_u32_e32 v133, v133, v134
	v_sub_u32_e32 v141, v141, v142
	v_subrev_u32_e32 v118, s11, v117
	v_subrev_u32_e32 v126, s11, v125
	v_subrev_u32_e32 v134, s11, v133
	v_subrev_u32_e32 v142, s11, v141
	v_cmp_le_u32_e32 vcc, s11, v117
	v_cmp_le_u32_e64 s[0:1], s11, v125
	v_cmp_le_u32_e64 s[6:7], s11, v133
	v_cmp_le_u32_e64 s[8:9], s11, v141
	v_cndmask_b32_e32 v117, v117, v118, vcc
	v_cndmask_b32_e64 v125, v125, v126, s[0:1]
	v_cndmask_b32_e64 v133, v133, v134, s[6:7]
	v_cndmask_b32_e64 v141, v141, v142, s[8:9]
	v_subrev_u32_e32 v118, s11, v117
	v_subrev_u32_e32 v126, s11, v125
	v_subrev_u32_e32 v134, s11, v133
	v_subrev_u32_e32 v142, s11, v141
	v_cmp_le_u32_e32 vcc, s11, v117
	v_cmp_le_u32_e64 s[0:1], s11, v125
	v_cmp_le_u32_e64 s[6:7], s11, v133
	v_cmp_le_u32_e64 s[8:9], s11, v141
	v_cndmask_b32_e32 v117, v117, v118, vcc
	v_cndmask_b32_e64 v125, v125, v126, s[0:1]
	v_cndmask_b32_e64 v133, v133, v134, s[6:7]
	v_cndmask_b32_e64 v141, v141, v142, s[8:9]
	v_ashrrev_i32_e32 v116, 8, v100
	v_ashrrev_i32_e32 v124, 8, v101
	v_ashrrev_i32_e32 v132, 8, v102
	v_ashrrev_i32_e32 v140, 8, v103
	s_waitcnt lgkmcnt(0)
	v_add_u32_e32 v116, v116, v113
	v_add_u32_e32 v124, v124, v121
	v_add_u32_e32 v132, v132, v129
	v_add_u32_e32 v140, v140, v137
	v_add3_u32 v116, v116, v114, v115
	v_add3_u32 v124, v124, v122, v123
	v_add3_u32 v132, v132, v130, v131
	v_add3_u32 v140, v140, v138, v139
	v_cmp_eq_u32_e32 vcc, s93, v117
	v_add_u32_e32 v1, 0x1e000, v10
	s_and_saveexec_b64 s[24:25], vcc
	global_store_dword v1, v116, s[16:17]
	s_mov_b64 exec, s[24:25]
	v_cmp_eq_u32_e32 vcc, s93, v125
	v_add_u32_e32 v1, 0x1e800, v10
	s_and_saveexec_b64 s[24:25], vcc
	global_store_dword v1, v124, s[16:17]
	s_mov_b64 exec, s[24:25]
	v_cmp_eq_u32_e32 vcc, s93, v133
	v_add_u32_e32 v1, 0x1f000, v10
	s_and_saveexec_b64 s[24:25], vcc
	global_store_dword v1, v132, s[16:17]
	s_mov_b64 exec, s[24:25]
	v_cmp_eq_u32_e32 vcc, s93, v141
	v_add_u32_e32 v1, 0x1f800, v10
	s_and_saveexec_b64 s[24:25], vcc
	global_store_dword v1, v140, s[16:17]
	s_mov_b64 exec, s[24:25]
	v_ashrrev_i32_e32 v113, 8, v116
	v_ashrrev_i32_e32 v121, 8, v124
	v_ashrrev_i32_e32 v129, 8, v132
	v_ashrrev_i32_e32 v137, 8, v140
	v_and_b32_e32 v112, 0xff, v116
	v_and_b32_e32 v120, 0xff, v124
	v_and_b32_e32 v128, 0xff, v132
	v_and_b32_e32 v136, 0xff, v140
	v_lshl_add_u32 v112, v112, 2, s10
	v_lshl_add_u32 v120, v120, 2, s10
	v_lshl_add_u32 v128, v128, 2, s10
	v_lshl_add_u32 v136, v136, 2, s10
	v_add_u32_e32 v114, 0x3c00, v34
	v_add_u32_e32 v122, 0x3d00, v34
	v_add_u32_e32 v130, 0x3e00, v34
	v_add_u32_e32 v138, 0x3f00, v34
	v_mov_b32_e32 v119, -1
	v_mov_b32_e32 v127, -1
	v_mov_b32_e32 v135, -1
	v_mov_b32_e32 v143, -1
	v_cmp_eq_u32_e32 vcc, v113, v2
	v_cmp_eq_u32_e64 s[0:1], v121, v2
	v_cmp_eq_u32_e64 s[6:7], v129, v2
	v_cmp_eq_u32_e64 s[8:9], v137, v2
	v_cndmask_b32_e32 v119, v119, v104, vcc
	v_cndmask_b32_e64 v127, v127, v104, s[0:1]
	v_cndmask_b32_e64 v135, v135, v104, s[6:7]
	v_cndmask_b32_e64 v143, v143, v104, s[8:9]
	v_cmp_eq_u32_e32 vcc, v113, v3
	v_cmp_eq_u32_e64 s[0:1], v121, v3
	v_cmp_eq_u32_e64 s[6:7], v129, v3
	v_cmp_eq_u32_e64 s[8:9], v137, v3
	v_cndmask_b32_e32 v119, v119, v105, vcc
	v_cndmask_b32_e64 v127, v127, v105, s[0:1]
	v_cndmask_b32_e64 v135, v135, v105, s[6:7]
	v_cndmask_b32_e64 v143, v143, v105, s[8:9]
	v_cmp_eq_u32_e32 vcc, v113, v4
	v_cmp_eq_u32_e64 s[0:1], v121, v4
	v_cmp_eq_u32_e64 s[6:7], v129, v4
	v_cmp_eq_u32_e64 s[8:9], v137, v4
	v_cndmask_b32_e32 v119, v119, v106, vcc
	v_cndmask_b32_e64 v127, v127, v106, s[0:1]
	v_cndmask_b32_e64 v135, v135, v106, s[6:7]
	v_cndmask_b32_e64 v143, v143, v106, s[8:9]
	v_cmp_eq_u32_e32 vcc, v113, v5
	v_cmp_eq_u32_e64 s[0:1], v121, v5
	v_cmp_eq_u32_e64 s[6:7], v129, v5
	v_cmp_eq_u32_e64 s[8:9], v137, v5
	v_cndmask_b32_e32 v119, v119, v107, vcc
	v_cndmask_b32_e64 v127, v127, v107, s[0:1]
	v_cndmask_b32_e64 v135, v135, v107, s[6:7]
	v_cndmask_b32_e64 v143, v143, v107, s[8:9]
	v_cmp_eq_u32_e32 vcc, v113, v6
	v_cmp_eq_u32_e64 s[0:1], v121, v6
	v_cmp_eq_u32_e64 s[6:7], v129, v6
	v_cmp_eq_u32_e64 s[8:9], v137, v6
	v_cndmask_b32_e32 v119, v119, v108, vcc
	v_cndmask_b32_e64 v127, v127, v108, s[0:1]
	v_cndmask_b32_e64 v135, v135, v108, s[6:7]
	v_cndmask_b32_e64 v143, v143, v108, s[8:9]
	v_cmp_eq_u32_e32 vcc, v113, v7
	v_cmp_eq_u32_e64 s[0:1], v121, v7
	v_cmp_eq_u32_e64 s[6:7], v129, v7
	v_cmp_eq_u32_e64 s[8:9], v137, v7
	v_cndmask_b32_e32 v119, v119, v109, vcc
	v_cndmask_b32_e64 v127, v127, v109, s[0:1]
	v_cndmask_b32_e64 v135, v135, v109, s[6:7]
	v_cndmask_b32_e64 v143, v143, v109, s[8:9]
	v_cmp_eq_u32_e32 vcc, v113, v8
	v_cmp_eq_u32_e64 s[0:1], v121, v8
	v_cmp_eq_u32_e64 s[6:7], v129, v8
	v_cmp_eq_u32_e64 s[8:9], v137, v8
	v_cndmask_b32_e32 v119, v119, v110, vcc
	v_cndmask_b32_e64 v127, v127, v110, s[0:1]
	v_cndmask_b32_e64 v135, v135, v110, s[6:7]
	v_cndmask_b32_e64 v143, v143, v110, s[8:9]
	v_cmp_eq_u32_e32 vcc, v113, v9
	v_cmp_eq_u32_e64 s[0:1], v121, v9
	v_cmp_eq_u32_e64 s[6:7], v129, v9
	v_cmp_eq_u32_e64 s[8:9], v137, v9
	v_cndmask_b32_e32 v119, v119, v111, vcc
	v_cndmask_b32_e64 v127, v127, v111, s[0:1]
	v_cndmask_b32_e64 v135, v135, v111, s[6:7]
	v_cndmask_b32_e64 v143, v143, v111, s[8:9]
	v_add_u32_e32 v112, v112, v119
	v_add_u32_e32 v120, v120, v127
	v_add_u32_e32 v128, v128, v135
	v_add_u32_e32 v136, v136, v143
	v_cmp_ne_u32_e32 vcc, -1, v119
	s_and_saveexec_b64 s[24:25], vcc
	ds_write_b32 v112, v114
	s_mov_b64 exec, s[24:25]
	v_cmp_ne_u32_e32 vcc, -1, v127
	s_and_saveexec_b64 s[24:25], vcc
	ds_write_b32 v120, v122
	s_mov_b64 exec, s[24:25]
	v_cmp_ne_u32_e32 vcc, -1, v135
	s_and_saveexec_b64 s[24:25], vcc
	ds_write_b32 v128, v130
	s_mov_b64 exec, s[24:25]
	v_cmp_ne_u32_e32 vcc, -1, v143
	s_and_saveexec_b64 s[24:25], vcc
	ds_write_b32 v136, v138
	s_mov_b64 exec, s[24:25]
	s_mov_b64 s[0:1], 0
